# all per-segment s_setprio flips removed from the GEMM main loops (plus P4b in-register scan state)
# speedup vs baseline: 1.0052x; 1.0052x over previous
; #define GAS __attribute__((address_space(1)))
; __device__ __forceinline__ void p0_prologue(Frame& F0, const In& I) {
;     ...
;     for (size_t i = gt; i < (size_t)T * D / 8; i += NGT) { const f32x4 a = ((const GAS f32x4*)I.x)[2 * i], b = ((const GAS f32x4*)I.x)[2 * i + 1];
;         int w0 = __builtin_amdgcn_cvt_pk_fp8_f32(a.x, a.y, 0, false); w0 = __builtin_amdgcn_cvt_pk_fp8_f32(a.z, a.w, w0, true);
;         int w1 = __builtin_amdgcn_cvt_pk_fp8_f32(b.x, b.y, 0, false); w1 = __builtin_amdgcn_cvt_pk_fp8_f32(b.z, b.w, w1, true);
;         ((GAS v2u*)(ws + WS_XB8))[i] = (v2u){(unsigned)w0, (unsigned)w1}; }
.LBB0_58:
	s_or_b64 exec, exec, s[2:3]
	s_mov_b32 s0, 0x800000
	v_cmp_gt_u32_e32 vcc, s0, v6
	s_and_saveexec_b64 s[0:1], vcc
	s_cbranch_execz .LBB0_61
	v_mov_b32_e32 v7, 0
	v_readlane_b32 s16, v254, 5
	v_lshlrev_b64 v[4:5], 5, v[6:7]
	v_readlane_b32 s17, v254, 6
	s_ashr_i32 s13, s12, 31
	v_lshl_add_u64 v[2:3], v[6:7], 3, s[96:97]
	s_mov_b64 s[2:3], 0xe8000000
	v_lshl_add_u64 v[4:5], s[16:17], 0, v[4:5]
	v_lshl_add_u64 v[2:3], v[2:3], 0, s[2:3]
	s_lshl_b64 s[2:3], s[12:13], 3
	v_lshl_add_u64 v[4:5], v[4:5], 0, 16
	s_lshl_b64 s[4:5], s[12:13], 5
	s_mov_b64 s[6:7], 0
	s_mov_b64 s[8:9], 0x7fffff
	v_readlane_b32 s18, v254, 7
	v_readlane_b32 s19, v254, 8
	v_readlane_b32 s20, v254, 9
	v_readlane_b32 s21, v254, 10
	v_readlane_b32 s22, v254, 11
	v_readlane_b32 s23, v254, 12
	v_readlane_b32 s24, v254, 13
	v_readlane_b32 s25, v254, 14
	v_readlane_b32 s26, v254, 15
	v_readlane_b32 s27, v254, 16
	v_readlane_b32 s28, v254, 17
	v_readlane_b32 s29, v254, 18
	v_readlane_b32 s30, v254, 19
	v_readlane_b32 s31, v254, 20
.LBB0_60:
	global_load_dwordx4 v[8:11], v[4:5], off offset:-16
	global_load_dwordx4 v[12:15], v[4:5], off
	v_mov_b32_e32 v16, 0
	v_mov_b32_e32 v17, 0
	v_lshl_add_u64 v[6:7], v[6:7], 0, s[12:13]
	v_cmp_lt_u64_e32 vcc, s[8:9], v[6:7]
	v_lshl_add_u64 v[4:5], v[4:5], 0, s[4:5]
	s_or_b64 s[6:7], vcc, s[6:7]
	s_waitcnt vmcnt(1)
	v_cvt_pk_fp8_f32 v16, v8, v9
	s_waitcnt vmcnt(0)
	v_cvt_pk_fp8_f32 v17, v12, v13
	v_cvt_pk_fp8_f32 v16, v10, v11 op_sel:[0,0,1]
	v_cvt_pk_fp8_f32 v17, v14, v15 op_sel:[0,0,1]
	global_store_dwordx2 v[2:3], v[16:17], off
	v_lshl_add_u64 v[2:3], v[2:3], 0, s[2:3]
	s_andn2_b64 exec, exec, s[6:7]
	s_cbranch_execnz .LBB0_60

; #define PG8_STAGE(bufoff, goff, voff) do { _Pragma("unroll") for (int _i = 0; _i < 2; ++_i) \
;         __builtin_amdgcn_raw_ptr_buffer_load_lds(rsrc, (PG8_LAS void*)(lds + (bufoff) + ldsw + _i * 8192), 16, (int)(voff), (int)((goff) + _i * p1##voff), 0, 0); } while (0)
; #define PG8_LDA(dst, b, h) do { _Pragma("unroll") for (int m = 0; m < 4; ++m) dst[m] = PG8_LD8(lds + PG8_SA(b, h) + aoff + m * 2048); } while (0)
; #define PG8_LDB(dst, b, h) do { _Pragma("unroll") for (int n = 0; n < 2; ++n) dst[n] = PG8_LD8(lds + PG8_SB(b, h) + boff + n * 2048); } while (0)
; #define PG8_WAIT_V(n) asm volatile("s_waitcnt vmcnt(" #n ")" ::: "memory")
; #define PG8_WAIT_L(n) asm volatile("s_waitcnt lgkmcnt(" #n ")" ::: "memory")
; #define PG8_BAR __builtin_amdgcn_s_barrier()
; #define PG8_SCHED __builtin_amdgcn_sched_barrier(0)
; template <class Epi, class Sched, bool ALIGN_EPI, bool F8 = false, int F8SC = F8_SCALES>
; __device__ __forceinline__ void gemm_phase(PG8_LAS unsigned char* lds, const __amdgpu_buffer_rsrc_t rsrc, const int lda, const int ldb, const int K, const Sched& S, const Epi& E) {
;     ...
;             PG8_LDB(B0, 0, 0); PG8_LDB(B1, 0, 1); PG8_SCHED; PG8_LDA(At, 0, 0); PG8_STAGE(PG8_SA(1, 1), a1 + hsA, voffA);
;             PG8_WAIT_V(8); PG8_WAIT_L(0); PG8_BAR; PG8_MMA(0, 0, At, B0); PG8_MMA(0, 1, At, B1); PG8_BAR; PG8_SCHED;
;             PG8_LDA(At, 0, 1); PG8_STAGE(PG8_SB(0, 0), b2, voffB); PG8_STAGE(PG8_SB(0, 1), b2 + hsB, voffB); PG8_STAGE(PG8_SA(0, 0), a2, voffA);
;             PG8_WAIT_V(8); PG8_WAIT_L(0); PG8_BAR; PG8_MMA(1, 0, At, B0); PG8_MMA(1, 1, At, B1); PG8_BAR; PG8_SCHED;
.LBB0_127:
	ds_read_b128 v[158:161], v151
	ds_read_b128 v[162:165], v151 offset:1024
	ds_read_b128 v[166:169], v151 offset:2048
	ds_read_b128 v[170:173], v151 offset:3072
	ds_read_b128 v[174:177], v152
	ds_read_b128 v[178:181], v152 offset:1024
	ds_read_b128 v[182:185], v152 offset:2048
	ds_read_b128 v[186:189], v152 offset:3072
	s_add_i32 s7, s0, 0xfffa0080
	s_cmp_eq_u32 s6, 12
	s_cselect_b32 s7, s59, s7
	s_cselect_b32 s9, s60, s1
	s_add_i32 s8, s7, 0x80
	s_add_i32 s10, s0, 0xfffe0000
	s_mov_b32 s80, s96
	s_mov_b32 m0, s53
	ds_read_b128 v[190:193], v153
	ds_read_b128 v[194:197], v153 offset:1024
	ds_read_b128 v[198:201], v153 offset:2048
	ds_read_b128 v[202:205], v153 offset:3072
	ds_read_b128 v[206:209], v153 offset:4096
	ds_read_b128 v[210:213], v153 offset:5120
	ds_read_b128 v[214:217], v153 offset:6144
	ds_read_b128 v[218:221], v153 offset:7168
	buffer_load_dwordx4 v1, s[80:83], s10 offen lds
	s_mov_b32 m0, s54
	s_nop 0
	buffer_load_dwordx4 v1, s[80:83], s0 offen lds
	s_waitcnt vmcnt(8)
	s_waitcnt lgkmcnt(0)
	s_barrier
	s_waitcnt lgkmcnt(4)
	v_mfma_scale_f32_16x16x128_f8f6f4 v[126:129], v[158:165], v[198:205], v[126:129], v154, v154 op_sel:[0,1,0] op_sel_hi:[0,0,0]
	v_mfma_scale_f32_16x16x128_f8f6f4 v[122:125], v[166:173], v[198:205], v[122:125], v154, v154 op_sel:[0,1,0] op_sel_hi:[0,0,0]
	s_waitcnt lgkmcnt(2)
	v_mfma_scale_f32_16x16x128_f8f6f4 v[118:121], v[158:165], v[206:213], v[118:121], v154, v154 op_sel:[0,1,0] op_sel_hi:[0,0,0]
	v_mfma_scale_f32_16x16x128_f8f6f4 v[114:117], v[166:173], v[206:213], v[114:117], v154, v154 op_sel:[0,1,0] op_sel_hi:[0,0,0]
	s_waitcnt lgkmcnt(0)
	v_mfma_scale_f32_16x16x128_f8f6f4 v[110:113], v[158:165], v[214:221], v[110:113], v154, v154 op_sel:[0,1,0] op_sel_hi:[0,0,0]
	v_mfma_scale_f32_16x16x128_f8f6f4 v[106:109], v[166:173], v[214:221], v[106:109], v154, v154 op_sel:[0,1,0] op_sel_hi:[0,0,0]
	v_mfma_scale_f32_16x16x128_f8f6f4 v[94:97], v[158:165], v[190:197], v[134:137], v154, v154 op_sel:[0,1,0] op_sel_hi:[0,0,0]
	v_mfma_scale_f32_16x16x128_f8f6f4 v[102:105], v[166:173], v[190:197], v[130:133], v154, v154 op_sel:[0,1,0] op_sel_hi:[0,0,0]
	v_mfma_scale_f32_16x16x128_f8f6f4 v[144:147], v[174:181], v[190:197], v[62:65], v154, v154 op_sel:[0,1,0] op_sel_hi:[0,0,0]
	v_mfma_scale_f32_16x16x128_f8f6f4 v[190:193], v[182:189], v[190:197], v[58:61], v154, v154 op_sel:[0,1,0] op_sel_hi:[0,0,0]
	v_mfma_scale_f32_16x16x128_f8f6f4 v[194:197], v[174:181], v[198:205], v[54:57], v154, v154 op_sel:[0,1,0] op_sel_hi:[0,0,0]
	v_mfma_scale_f32_16x16x128_f8f6f4 v[198:201], v[182:189], v[198:205], v[50:53], v154, v154 op_sel:[0,1,0] op_sel_hi:[0,0,0]
	v_mfma_scale_f32_16x16x128_f8f6f4 v[202:205], v[174:181], v[206:213], v[46:49], v154, v154 op_sel:[0,1,0] op_sel_hi:[0,0,0]
	v_mfma_scale_f32_16x16x128_f8f6f4 v[206:209], v[182:189], v[206:213], v[42:45], v154, v154 op_sel:[0,1,0] op_sel_hi:[0,0,0]
	v_mfma_scale_f32_16x16x128_f8f6f4 v[210:213], v[174:181], v[214:221], v[38:41], v154, v154 op_sel:[0,1,0] op_sel_hi:[0,0,0]
	v_mfma_scale_f32_16x16x128_f8f6f4 v[214:217], v[182:189], v[214:221], v[34:37], v154, v154 op_sel:[0,1,0] op_sel_hi:[0,0,0]
	s_barrier
	s_mov_b32 m0, s34
	s_nop 3
	ds_read_b128 v[34:37], v153 offset:16384
	ds_read_b128 v[38:41], v153 offset:17408
	ds_read_b128 v[42:45], v153 offset:18432
	ds_read_b128 v[46:49], v153 offset:19456
	ds_read_b128 v[50:53], v153 offset:20480
	ds_read_b128 v[54:57], v153 offset:21504
	ds_read_b128 v[58:61], v153 offset:22528
	ds_read_b128 v[62:65], v153 offset:23552
	buffer_load_dwordx4 v150, s[80:83], s9 offen lds
	s_add_i32 s10, s9, 0x20000
	s_mov_b32 m0, s35
	s_nop 0
	buffer_load_dwordx4 v150, s[80:83], s10 offen lds
	s_add_i32 s10, s9, 0x40000
	s_mov_b32 m0, s36
	s_nop 0
	buffer_load_dwordx4 v150, s[80:83], s10 offen lds
	s_add_i32 s10, s9, 0x60000
	s_mov_b32 m0, s37
	s_nop 0
	buffer_load_dwordx4 v150, s[80:83], s10 offen lds
	s_mov_b32 m0, s13
	s_add_i32 s10, s7, 0x20000
	buffer_load_dwordx4 v1, s[80:83], s7 offen lds
	s_mov_b32 m0, s38
	s_nop 0
	buffer_load_dwordx4 v1, s[80:83], s10 offen lds
	s_waitcnt vmcnt(8)
	s_waitcnt lgkmcnt(0)
	s_barrier
	s_waitcnt lgkmcnt(6)
	v_mfma_scale_f32_16x16x128_f8f6f4 v[98:101], v[158:165], v[34:41], v[98:101], v154, v154 op_sel:[0,1,0] op_sel_hi:[0,0,0]
	v_mfma_scale_f32_16x16x128_f8f6f4 v[90:93], v[166:173], v[34:41], v[90:93], v154, v154 op_sel:[0,1,0] op_sel_hi:[0,0,0]
	s_waitcnt lgkmcnt(4)
	v_mfma_scale_f32_16x16x128_f8f6f4 v[86:89], v[158:165], v[42:49], v[86:89], v154, v154 op_sel:[0,1,0] op_sel_hi:[0,0,0]
	v_mfma_scale_f32_16x16x128_f8f6f4 v[82:85], v[166:173], v[42:49], v[82:85], v154, v154 op_sel:[0,1,0] op_sel_hi:[0,0,0]
	s_waitcnt lgkmcnt(2)
	v_mfma_scale_f32_16x16x128_f8f6f4 v[78:81], v[158:165], v[50:57], v[78:81], v154, v154 op_sel:[0,1,0] op_sel_hi:[0,0,0]
	v_mfma_scale_f32_16x16x128_f8f6f4 v[74:77], v[166:173], v[50:57], v[74:77], v154, v154 op_sel:[0,1,0] op_sel_hi:[0,0,0]
	s_waitcnt lgkmcnt(0)
	v_mfma_scale_f32_16x16x128_f8f6f4 v[218:221], v[158:165], v[58:65], v[70:73], v154, v154 op_sel:[0,1,0] op_sel_hi:[0,0,0]
	v_mfma_scale_f32_16x16x128_f8f6f4 v[222:225], v[166:173], v[58:65], v[66:69], v154, v154 op_sel:[0,1,0] op_sel_hi:[0,0,0]
	v_mfma_scale_f32_16x16x128_f8f6f4 v[226:229], v[174:181], v[34:41], v[30:33], v154, v154 op_sel:[0,1,0] op_sel_hi:[0,0,0]
	v_mfma_scale_f32_16x16x128_f8f6f4 v[230:233], v[182:189], v[34:41], v[26:29], v154, v154 op_sel:[0,1,0] op_sel_hi:[0,0,0]
	v_mfma_scale_f32_16x16x128_f8f6f4 v[234:237], v[174:181], v[42:49], v[22:25], v154, v154 op_sel:[0,1,0] op_sel_hi:[0,0,0]
	v_mfma_scale_f32_16x16x128_f8f6f4 v[238:241], v[182:189], v[42:49], v[18:21], v154, v154 op_sel:[0,1,0] op_sel_hi:[0,0,0]
	v_mfma_scale_f32_16x16x128_f8f6f4 v[242:245], v[174:181], v[50:57], v[14:17], v154, v154 op_sel:[0,1,0] op_sel_hi:[0,0,0]
	v_mfma_scale_f32_16x16x128_f8f6f4 v[246:249], v[182:189], v[50:57], v[10:13], v154, v154 op_sel:[0,1,0] op_sel_hi:[0,0,0]
	v_mfma_scale_f32_16x16x128_f8f6f4 v[250:253], v[174:181], v[58:65], v[6:9], v154, v154 op_sel:[0,1,0] op_sel_hi:[0,0,0]
	v_mfma_scale_f32_16x16x128_f8f6f4 v[138:141], v[182:189], v[58:65], v[2:5], v154, v154 op_sel:[0,1,0] op_sel_hi:[0,0,0]
	s_barrier
; #define PG8_STAGE(bufoff, goff, voff) do { _Pragma("unroll") for (int _i = 0; _i < 2; ++_i) \
;         __builtin_amdgcn_raw_ptr_buffer_load_lds(rsrc, (PG8_LAS void*)(lds + (bufoff) + ldsw + _i * 8192), 16, (int)(voff), (int)((goff) + _i * p1##voff), 0, 0); } while (0)
; #define PG8_LDA(dst, b, h) do { _Pragma("unroll") for (int m = 0; m < 4; ++m) dst[m] = PG8_LD8(lds + PG8_SA(b, h) + aoff + m * 2048); } while (0)
; #define PG8_LDB(dst, b, h) do { _Pragma("unroll") for (int n = 0; n < 2; ++n) dst[n] = PG8_LD8(lds + PG8_SB(b, h) + boff + n * 2048); } while (0)
; #define PG8_WAIT_V(n) asm volatile("s_waitcnt vmcnt(" #n ")" ::: "memory")
; #define PG8_WAIT_L(n) asm volatile("s_waitcnt lgkmcnt(" #n ")" ::: "memory")
; #define PG8_BAR __builtin_amdgcn_s_barrier()
; #define PG8_SCHED __builtin_amdgcn_sched_barrier(0)
; template <class Epi, class Sched, bool ALIGN_EPI, bool F8 = false, int F8SC = F8_SCALES>
; __device__ __forceinline__ void gemm_phase(PG8_LAS unsigned char* lds, const __amdgpu_buffer_rsrc_t rsrc, const int lda, const int ldb, const int K, const Sched& S, const Epi& E) {
;     ...
;             PG8_LDB(B0, 1, 0); PG8_LDB(B1, 1, 1); PG8_SCHED; PG8_LDA(At, 1, 0); PG8_STAGE(PG8_SA(0, 1), a2 + hsA, voffA);
;             PG8_WAIT_V(8); PG8_WAIT_L(0); PG8_BAR; PG8_MMA(0, 0, At, B0); PG8_MMA(0, 1, At, B1); PG8_BAR; PG8_SCHED;
;             PG8_LDA(At, 1, 1); PG8_STAGE(PG8_SB(1, 0), b3, voffB); PG8_STAGE(PG8_SB(1, 1), b3 + hsB, voffB); PG8_STAGE(PG8_SA(1, 0), a3, voffA);
;             PG8_WAIT_V(8); PG8_WAIT_L(0); PG8_BAR; PG8_MMA(1, 0, At, B0); PG8_MMA(1, 1, At, B1); PG8_BAR; PG8_SCHED;
;         }
	s_nop 4
	ds_read_b128 v[2:5], v155
	ds_read_b128 v[6:9], v155 offset:1024
	ds_read_b128 v[10:13], v155 offset:2048
	ds_read_b128 v[14:17], v155 offset:3072
	ds_read_b128 v[158:161], v156
	ds_read_b128 v[162:165], v156 offset:1024
	ds_read_b128 v[166:169], v156 offset:2048
	ds_read_b128 v[170:173], v156 offset:3072
	s_mov_b32 m0, s39
	s_add_i32 s10, s7, 0x40000
	ds_read_b128 v[18:21], v153 offset:32768
	ds_read_b128 v[22:25], v153 offset:33792
	ds_read_b128 v[26:29], v153 offset:34816
	ds_read_b128 v[30:33], v153 offset:35840
	ds_read_b128 v[34:37], v153 offset:36864
	ds_read_b128 v[38:41], v153 offset:37888
	ds_read_b128 v[66:69], v153 offset:38912
	ds_read_b128 v[70:73], v153 offset:39936
	buffer_load_dwordx4 v1, s[80:83], s10 offen lds
	s_add_i32 s10, s7, 0x60000
	s_mov_b32 m0, s40
	s_nop 0
	buffer_load_dwordx4 v1, s[80:83], s10 offen lds
	s_waitcnt vmcnt(8)
	s_waitcnt lgkmcnt(0)
	s_barrier
	s_waitcnt lgkmcnt(6)
	v_mfma_scale_f32_16x16x128_f8f6f4 v[134:137], v[2:9], v[18:25], v[94:97], v154, v154 op_sel:[0,1,0] op_sel_hi:[0,0,0]
	v_mfma_scale_f32_16x16x128_f8f6f4 v[130:133], v[10:17], v[18:25], v[102:105], v154, v154 op_sel:[0,1,0] op_sel_hi:[0,0,0]
	s_waitcnt lgkmcnt(4)
	v_mfma_scale_f32_16x16x128_f8f6f4 v[126:129], v[2:9], v[26:33], v[126:129], v154, v154 op_sel:[0,1,0] op_sel_hi:[0,0,0]
	v_mfma_scale_f32_16x16x128_f8f6f4 v[122:125], v[10:17], v[26:33], v[122:125], v154, v154 op_sel:[0,1,0] op_sel_hi:[0,0,0]
	s_waitcnt lgkmcnt(2)
	v_mfma_scale_f32_16x16x128_f8f6f4 v[118:121], v[2:9], v[34:41], v[118:121], v154, v154 op_sel:[0,1,0] op_sel_hi:[0,0,0]
	v_mfma_scale_f32_16x16x128_f8f6f4 v[114:117], v[10:17], v[34:41], v[114:117], v154, v154 op_sel:[0,1,0] op_sel_hi:[0,0,0]
	s_waitcnt lgkmcnt(0)
	v_mfma_scale_f32_16x16x128_f8f6f4 v[110:113], v[2:9], v[66:73], v[110:113], v154, v154 op_sel:[0,1,0] op_sel_hi:[0,0,0]
	v_mfma_scale_f32_16x16x128_f8f6f4 v[106:109], v[10:17], v[66:73], v[106:109], v154, v154 op_sel:[0,1,0] op_sel_hi:[0,0,0]
	v_mfma_scale_f32_16x16x128_f8f6f4 v[62:65], v[158:165], v[18:25], v[144:147], v154, v154 op_sel:[0,1,0] op_sel_hi:[0,0,0]
	v_mfma_scale_f32_16x16x128_f8f6f4 v[58:61], v[166:173], v[18:25], v[190:193], v154, v154 op_sel:[0,1,0] op_sel_hi:[0,0,0]
	v_mfma_scale_f32_16x16x128_f8f6f4 v[54:57], v[158:165], v[26:33], v[194:197], v154, v154 op_sel:[0,1,0] op_sel_hi:[0,0,0]
	v_mfma_scale_f32_16x16x128_f8f6f4 v[50:53], v[166:173], v[26:33], v[198:201], v154, v154 op_sel:[0,1,0] op_sel_hi:[0,0,0]
	v_mfma_scale_f32_16x16x128_f8f6f4 v[46:49], v[158:165], v[34:41], v[202:205], v154, v154 op_sel:[0,1,0] op_sel_hi:[0,0,0]
	v_mfma_scale_f32_16x16x128_f8f6f4 v[42:45], v[166:173], v[34:41], v[206:209], v154, v154 op_sel:[0,1,0] op_sel_hi:[0,0,0]
	v_mfma_scale_f32_16x16x128_f8f6f4 v[38:41], v[158:165], v[66:73], v[210:213], v154, v154 op_sel:[0,1,0] op_sel_hi:[0,0,0]
	v_mfma_scale_f32_16x16x128_f8f6f4 v[34:37], v[166:173], v[66:73], v[214:217], v154, v154 op_sel:[0,1,0] op_sel_hi:[0,0,0]
	s_barrier
	s_mov_b32 m0, s46
	s_add_i32 s10, s9, 0x80
	ds_read_b128 v[18:21], v153 offset:49152
	ds_read_b128 v[22:25], v153 offset:50176
	ds_read_b128 v[174:177], v153 offset:51200
	ds_read_b128 v[178:181], v153 offset:52224
	ds_read_b128 v[182:185], v153 offset:53248
	ds_read_b128 v[186:189], v153 offset:54272
	ds_read_b128 v[190:193], v153 offset:55296
	ds_read_b128 v[194:197], v153 offset:56320
	buffer_load_dwordx4 v150, s[80:83], s10 offen lds
	s_add_i32 s10, s9, 0x20080
	s_mov_b32 m0, s47
	s_add_i32 s7, s7, 0x20080
	buffer_load_dwordx4 v150, s[80:83], s10 offen lds
	s_add_i32 s10, s9, 0x40080
	s_mov_b32 m0, s50
	s_add_i32 s9, s9, 0x60080
	buffer_load_dwordx4 v150, s[80:83], s10 offen lds
	s_mov_b32 m0, s51
	s_nop 0
	buffer_load_dwordx4 v150, s[80:83], s9 offen lds
	s_mov_b32 m0, s48
	s_nop 0
	buffer_load_dwordx4 v1, s[80:83], s8 offen lds
	s_mov_b32 m0, s49
	s_nop 0
	buffer_load_dwordx4 v1, s[80:83], s7 offen lds
	s_waitcnt vmcnt(8)
	s_waitcnt lgkmcnt(0)
	s_barrier
	s_waitcnt lgkmcnt(6)
	v_mfma_scale_f32_16x16x128_f8f6f4 v[98:101], v[2:9], v[18:25], v[98:101], v154, v154 op_sel:[0,1,0] op_sel_hi:[0,0,0]
	v_mfma_scale_f32_16x16x128_f8f6f4 v[90:93], v[10:17], v[18:25], v[90:93], v154, v154 op_sel:[0,1,0] op_sel_hi:[0,0,0]
	s_waitcnt lgkmcnt(4)
	v_mfma_scale_f32_16x16x128_f8f6f4 v[86:89], v[2:9], v[174:181], v[86:89], v154, v154 op_sel:[0,1,0] op_sel_hi:[0,0,0]
	v_mfma_scale_f32_16x16x128_f8f6f4 v[82:85], v[10:17], v[174:181], v[82:85], v154, v154 op_sel:[0,1,0] op_sel_hi:[0,0,0]
	s_waitcnt lgkmcnt(2)
	v_mfma_scale_f32_16x16x128_f8f6f4 v[78:81], v[2:9], v[182:189], v[78:81], v154, v154 op_sel:[0,1,0] op_sel_hi:[0,0,0]
	v_mfma_scale_f32_16x16x128_f8f6f4 v[74:77], v[10:17], v[182:189], v[74:77], v154, v154 op_sel:[0,1,0] op_sel_hi:[0,0,0]
	s_waitcnt lgkmcnt(0)
	v_mfma_scale_f32_16x16x128_f8f6f4 v[70:73], v[2:9], v[190:197], v[218:221], v154, v154 op_sel:[0,1,0] op_sel_hi:[0,0,0]
	v_mfma_scale_f32_16x16x128_f8f6f4 v[66:69], v[10:17], v[190:197], v[222:225], v154, v154 op_sel:[0,1,0] op_sel_hi:[0,0,0]
	v_mfma_scale_f32_16x16x128_f8f6f4 v[30:33], v[158:165], v[18:25], v[226:229], v154, v154 op_sel:[0,1,0] op_sel_hi:[0,0,0]
	v_mfma_scale_f32_16x16x128_f8f6f4 v[26:29], v[166:173], v[18:25], v[230:233], v154, v154 op_sel:[0,1,0] op_sel_hi:[0,0,0]
	v_mfma_scale_f32_16x16x128_f8f6f4 v[22:25], v[158:165], v[174:181], v[234:237], v154, v154 op_sel:[0,1,0] op_sel_hi:[0,0,0]
	v_mfma_scale_f32_16x16x128_f8f6f4 v[18:21], v[166:173], v[174:181], v[238:241], v154, v154 op_sel:[0,1,0] op_sel_hi:[0,0,0]
	v_mfma_scale_f32_16x16x128_f8f6f4 v[14:17], v[158:165], v[182:189], v[242:245], v154, v154 op_sel:[0,1,0] op_sel_hi:[0,0,0]
	v_mfma_scale_f32_16x16x128_f8f6f4 v[10:13], v[166:173], v[182:189], v[246:249], v154, v154 op_sel:[0,1,0] op_sel_hi:[0,0,0]
	v_mfma_scale_f32_16x16x128_f8f6f4 v[6:9], v[158:165], v[190:197], v[250:253], v154, v154 op_sel:[0,1,0] op_sel_hi:[0,0,0]
	v_mfma_scale_f32_16x16x128_f8f6f4 v[2:5], v[166:173], v[190:197], v[138:141], v154, v154 op_sel:[0,1,0] op_sel_hi:[0,0,0]
	s_barrier
	s_add_i32 s6, s6, 2
	s_addk_i32 s0, 0x100
	s_addk_i32 s1, 0x100
	s_cmp_gt_u32 s6, 13
	s_cbranch_scc0 .LBB0_127
	s_and_b64 vcc, exec, s[88:89]
	s_cbranch_vccz .LBB0_130
	s_barrier

; #define PG8_STAGE(bufoff, goff, voff) do { _Pragma("unroll") for (int _i = 0; _i < 2; ++_i) \
;         __builtin_amdgcn_raw_ptr_buffer_load_lds(rsrc, (PG8_LAS void*)(lds + (bufoff) + ldsw + _i * 8192), 16, (int)(voff), (int)((goff) + _i * p1##voff), 0, 0); } while (0)
; #define PG8_LDA(dst, b, h) do { _Pragma("unroll") for (int m = 0; m < 4; ++m) dst[m] = PG8_LD8(lds + PG8_SA(b, h) + aoff + m * 2048); } while (0)
; #define PG8_LDB(dst, b, h) do { _Pragma("unroll") for (int n = 0; n < 2; ++n) dst[n] = PG8_LD8(lds + PG8_SB(b, h) + boff + n * 2048); } while (0)
; #define PG8_WAIT_V(n) asm volatile("s_waitcnt vmcnt(" #n ")" ::: "memory")
; #define PG8_WAIT_L(n) asm volatile("s_waitcnt lgkmcnt(" #n ")" ::: "memory")
; #define PG8_BAR __builtin_amdgcn_s_barrier()
; #define PG8_SCHED __builtin_amdgcn_sched_barrier(0)
; template <class Epi, class Sched, bool ALIGN_EPI, bool F8 = false, int F8SC = F8_SCALES>
; __device__ __forceinline__ void gemm_phase(PG8_LAS unsigned char* lds, const __amdgpu_buffer_rsrc_t rsrc, const int lda, const int ldb, const int K, const Sched& S, const Epi& E) {
;     ...
;             PG8_LDB(B0, 0, 0); PG8_LDB(B1, 0, 1); PG8_SCHED; PG8_LDA(At, 0, 0); PG8_STAGE(PG8_SA(1, 1), a1 + hsA, voffA);
;             PG8_WAIT_V(8); PG8_WAIT_L(0); PG8_BAR; PG8_MMA(0, 0, At, B0); PG8_MMA(0, 1, At, B1); PG8_BAR; PG8_SCHED;
;             PG8_LDA(At, 0, 1); PG8_STAGE(PG8_SB(0, 0), b2, voffB); PG8_STAGE(PG8_SB(0, 1), b2 + hsB, voffB); PG8_STAGE(PG8_SA(0, 0), a2, voffA);
;             PG8_WAIT_V(8); PG8_WAIT_L(0); PG8_BAR; PG8_MMA(1, 0, At, B0); PG8_MMA(1, 1, At, B1); PG8_BAR; PG8_SCHED;
.LBB0_739:
	ds_read_b128 v[148:151], v140
	ds_read_b128 v[152:155], v140 offset:1024
	ds_read_b128 v[156:159], v140 offset:2048
	ds_read_b128 v[160:163], v140 offset:3072
	ds_read_b128 v[164:167], v141
	ds_read_b128 v[168:171], v141 offset:1024
	ds_read_b128 v[172:175], v141 offset:2048
	ds_read_b128 v[176:179], v141 offset:3072
	s_add_i32 s39, s36, 0xfffa0080
	s_cmp_eq_u32 s38, 12
	s_cselect_b32 s39, s4, s39
	s_cselect_b32 s41, s5, s37
	s_add_i32 s40, s39, 0x80
	s_add_i32 s42, s36, 0xfffe0000
	s_mov_b32 s80, s96
	s_mov_b32 m0, s27
	ds_read_b128 v[180:183], v142
	ds_read_b128 v[184:187], v142 offset:1024
	ds_read_b128 v[188:191], v142 offset:2048
	ds_read_b128 v[192:195], v142 offset:3072
	ds_read_b128 v[196:199], v142 offset:4096
	ds_read_b128 v[200:203], v142 offset:5120
	ds_read_b128 v[204:207], v142 offset:6144
	ds_read_b128 v[208:211], v142 offset:7168
	buffer_load_dwordx4 v1, s[80:83], s42 offen lds
	s_mov_b32 m0, s28
	s_nop 0
	buffer_load_dwordx4 v1, s[80:83], s36 offen lds
	s_waitcnt vmcnt(8)
	s_waitcnt lgkmcnt(0)
	s_barrier
	s_waitcnt lgkmcnt(6)
	v_mfma_scale_f32_16x16x128_f8f6f4 v[126:129], v[148:155], v[180:187], v[126:129], v143, v143 op_sel:[0,1,0] op_sel_hi:[0,0,0]
	v_mfma_scale_f32_16x16x128_f8f6f4 v[122:125], v[156:163], v[180:187], v[122:125], v143, v143 op_sel:[0,1,0] op_sel_hi:[0,0,0]
	s_waitcnt lgkmcnt(4)
	v_mfma_scale_f32_16x16x128_f8f6f4 v[118:121], v[148:155], v[188:195], v[118:121], v143, v143 op_sel:[0,1,0] op_sel_hi:[0,0,0]
	v_mfma_scale_f32_16x16x128_f8f6f4 v[110:113], v[156:163], v[188:195], v[110:113], v143, v143 op_sel:[0,1,0] op_sel_hi:[0,0,0]
	s_waitcnt lgkmcnt(2)
	v_mfma_scale_f32_16x16x128_f8f6f4 v[102:105], v[148:155], v[196:203], v[102:105], v143, v143 op_sel:[0,1,0] op_sel_hi:[0,0,0]
	v_mfma_scale_f32_16x16x128_f8f6f4 v[136:139], v[156:163], v[196:203], v[94:97], v143, v143 op_sel:[0,1,0] op_sel_hi:[0,0,0]
	s_waitcnt lgkmcnt(0)
	v_mfma_scale_f32_16x16x128_f8f6f4 v[212:215], v[148:155], v[204:211], v[86:89], v143, v143 op_sel:[0,1,0] op_sel_hi:[0,0,0]
	v_mfma_scale_f32_16x16x128_f8f6f4 v[216:219], v[156:163], v[204:211], v[78:81], v143, v143 op_sel:[0,1,0] op_sel_hi:[0,0,0]
	v_mfma_scale_f32_16x16x128_f8f6f4 v[114:117], v[164:171], v[180:187], v[114:117], v143, v143 op_sel:[0,1,0] op_sel_hi:[0,0,0]
	v_mfma_scale_f32_16x16x128_f8f6f4 v[106:109], v[172:179], v[180:187], v[106:109], v143, v143 op_sel:[0,1,0] op_sel_hi:[0,0,0]
	v_mfma_scale_f32_16x16x128_f8f6f4 v[98:101], v[164:171], v[188:195], v[98:101], v143, v143 op_sel:[0,1,0] op_sel_hi:[0,0,0]
	v_mfma_scale_f32_16x16x128_f8f6f4 v[180:183], v[172:179], v[188:195], v[90:93], v143, v143 op_sel:[0,1,0] op_sel_hi:[0,0,0]
	v_mfma_scale_f32_16x16x128_f8f6f4 v[184:187], v[164:171], v[196:203], v[82:85], v143, v143 op_sel:[0,1,0] op_sel_hi:[0,0,0]
	v_mfma_scale_f32_16x16x128_f8f6f4 v[188:191], v[172:179], v[196:203], v[74:77], v143, v143 op_sel:[0,1,0] op_sel_hi:[0,0,0]
	v_mfma_scale_f32_16x16x128_f8f6f4 v[192:195], v[164:171], v[204:211], v[70:73], v143, v143 op_sel:[0,1,0] op_sel_hi:[0,0,0]
	v_mfma_scale_f32_16x16x128_f8f6f4 v[196:199], v[172:179], v[204:211], v[66:69], v143, v143 op_sel:[0,1,0] op_sel_hi:[0,0,0]
	s_barrier
	s_mov_b32 m0, s10
	s_nop 3
	ds_read_b128 v[66:69], v142 offset:16384
	ds_read_b128 v[70:73], v142 offset:17408
	ds_read_b128 v[74:77], v142 offset:18432
	ds_read_b128 v[78:81], v142 offset:19456
	ds_read_b128 v[82:85], v142 offset:20480
	ds_read_b128 v[86:89], v142 offset:21504
	ds_read_b128 v[90:93], v142 offset:22528
	ds_read_b128 v[94:97], v142 offset:23552
	buffer_load_dwordx4 v135, s[80:83], s41 offen lds
	s_add_i32 s42, s41, 0x20000
	s_mov_b32 m0, s11
	s_nop 0
	buffer_load_dwordx4 v135, s[80:83], s42 offen lds
	s_add_i32 s42, s41, 0x40000
	s_mov_b32 m0, s13
	s_nop 0
	buffer_load_dwordx4 v135, s[80:83], s42 offen lds
	s_add_i32 s42, s41, 0x60000
	s_mov_b32 m0, s16
	s_nop 0
	buffer_load_dwordx4 v135, s[80:83], s42 offen lds
	s_mov_b32 m0, s9
	s_add_i32 s42, s39, 0x20000
	buffer_load_dwordx4 v1, s[80:83], s39 offen lds
	s_mov_b32 m0, s17
	s_nop 0
	buffer_load_dwordx4 v1, s[80:83], s42 offen lds
	s_waitcnt vmcnt(8)
	s_waitcnt lgkmcnt(0)
	s_barrier
	s_waitcnt lgkmcnt(6)
	v_mfma_scale_f32_16x16x128_f8f6f4 v[62:65], v[148:155], v[66:73], v[62:65], v143, v143 op_sel:[0,1,0] op_sel_hi:[0,0,0]
	v_mfma_scale_f32_16x16x128_f8f6f4 v[58:61], v[156:163], v[66:73], v[58:61], v143, v143 op_sel:[0,1,0] op_sel_hi:[0,0,0]
	s_waitcnt lgkmcnt(4)
	v_mfma_scale_f32_16x16x128_f8f6f4 v[54:57], v[148:155], v[74:81], v[54:57], v143, v143 op_sel:[0,1,0] op_sel_hi:[0,0,0]
	v_mfma_scale_f32_16x16x128_f8f6f4 v[200:203], v[156:163], v[74:81], v[46:49], v143, v143 op_sel:[0,1,0] op_sel_hi:[0,0,0]
	s_waitcnt lgkmcnt(2)
	v_mfma_scale_f32_16x16x128_f8f6f4 v[204:207], v[148:155], v[82:89], v[38:41], v143, v143 op_sel:[0,1,0] op_sel_hi:[0,0,0]
	v_mfma_scale_f32_16x16x128_f8f6f4 v[208:211], v[156:163], v[82:89], v[30:33], v143, v143 op_sel:[0,1,0] op_sel_hi:[0,0,0]
	s_waitcnt lgkmcnt(0)
	v_mfma_scale_f32_16x16x128_f8f6f4 v[220:223], v[148:155], v[90:97], v[22:25], v143, v143 op_sel:[0,1,0] op_sel_hi:[0,0,0]
	v_mfma_scale_f32_16x16x128_f8f6f4 v[224:227], v[156:163], v[90:97], v[14:17], v143, v143 op_sel:[0,1,0] op_sel_hi:[0,0,0]
	v_mfma_scale_f32_16x16x128_f8f6f4 v[50:53], v[164:171], v[66:73], v[50:53], v143, v143 op_sel:[0,1,0] op_sel_hi:[0,0,0]
	v_mfma_scale_f32_16x16x128_f8f6f4 v[228:231], v[172:179], v[66:73], v[42:45], v143, v143 op_sel:[0,1,0] op_sel_hi:[0,0,0]
	v_mfma_scale_f32_16x16x128_f8f6f4 v[232:235], v[164:171], v[74:81], v[34:37], v143, v143 op_sel:[0,1,0] op_sel_hi:[0,0,0]
	v_mfma_scale_f32_16x16x128_f8f6f4 v[236:239], v[172:179], v[74:81], v[26:29], v143, v143 op_sel:[0,1,0] op_sel_hi:[0,0,0]
	v_mfma_scale_f32_16x16x128_f8f6f4 v[240:243], v[164:171], v[82:89], v[18:21], v143, v143 op_sel:[0,1,0] op_sel_hi:[0,0,0]
	v_mfma_scale_f32_16x16x128_f8f6f4 v[244:247], v[172:179], v[82:89], v[10:13], v143, v143 op_sel:[0,1,0] op_sel_hi:[0,0,0]
	v_mfma_scale_f32_16x16x128_f8f6f4 v[248:251], v[164:171], v[90:97], v[6:9], v143, v143 op_sel:[0,1,0] op_sel_hi:[0,0,0]
	v_mfma_scale_f32_16x16x128_f8f6f4 v[130:133], v[172:179], v[90:97], v[2:5], v143, v143 op_sel:[0,1,0] op_sel_hi:[0,0,0]
	s_barrier
; #define PG8_STAGE(bufoff, goff, voff) do { _Pragma("unroll") for (int _i = 0; _i < 2; ++_i) \
;         __builtin_amdgcn_raw_ptr_buffer_load_lds(rsrc, (PG8_LAS void*)(lds + (bufoff) + ldsw + _i * 8192), 16, (int)(voff), (int)((goff) + _i * p1##voff), 0, 0); } while (0)
; #define PG8_LDA(dst, b, h) do { _Pragma("unroll") for (int m = 0; m < 4; ++m) dst[m] = PG8_LD8(lds + PG8_SA(b, h) + aoff + m * 2048); } while (0)
; #define PG8_LDB(dst, b, h) do { _Pragma("unroll") for (int n = 0; n < 2; ++n) dst[n] = PG8_LD8(lds + PG8_SB(b, h) + boff + n * 2048); } while (0)
; #define PG8_WAIT_V(n) asm volatile("s_waitcnt vmcnt(" #n ")" ::: "memory")
; #define PG8_WAIT_L(n) asm volatile("s_waitcnt lgkmcnt(" #n ")" ::: "memory")
; #define PG8_BAR __builtin_amdgcn_s_barrier()
; #define PG8_SCHED __builtin_amdgcn_sched_barrier(0)
; template <class Epi, class Sched, bool ALIGN_EPI, bool F8 = false, int F8SC = F8_SCALES>
; __device__ __forceinline__ void gemm_phase(PG8_LAS unsigned char* lds, const __amdgpu_buffer_rsrc_t rsrc, const int lda, const int ldb, const int K, const Sched& S, const Epi& E) {
;     ...
;             PG8_LDB(B0, 1, 0); PG8_LDB(B1, 1, 1); PG8_SCHED; PG8_LDA(At, 1, 0); PG8_STAGE(PG8_SA(0, 1), a2 + hsA, voffA);
;             PG8_WAIT_V(8); PG8_WAIT_L(0); PG8_BAR; PG8_MMA(0, 0, At, B0); PG8_MMA(0, 1, At, B1); PG8_BAR; PG8_SCHED;
;             PG8_LDA(At, 1, 1); PG8_STAGE(PG8_SB(1, 0), b3, voffB); PG8_STAGE(PG8_SB(1, 1), b3 + hsB, voffB); PG8_STAGE(PG8_SA(1, 0), a3, voffA);
;             PG8_WAIT_V(8); PG8_WAIT_L(0); PG8_BAR; PG8_MMA(1, 0, At, B0); PG8_MMA(1, 1, At, B1); PG8_BAR; PG8_SCHED;
;         }
	s_nop 4
	ds_read_b128 v[2:5], v144
	ds_read_b128 v[6:9], v144 offset:1024
	ds_read_b128 v[10:13], v144 offset:2048
	ds_read_b128 v[14:17], v144 offset:3072
	ds_read_b128 v[148:151], v145
	ds_read_b128 v[152:155], v145 offset:1024
	ds_read_b128 v[156:159], v145 offset:2048
	ds_read_b128 v[160:163], v145 offset:3072
	s_mov_b32 m0, s18
	s_add_i32 s42, s39, 0x40000
	ds_read_b128 v[18:21], v142 offset:32768
	ds_read_b128 v[22:25], v142 offset:33792
	ds_read_b128 v[26:29], v142 offset:34816
	ds_read_b128 v[30:33], v142 offset:35840
	ds_read_b128 v[34:37], v142 offset:36864
	ds_read_b128 v[38:41], v142 offset:37888
	ds_read_b128 v[42:45], v142 offset:38912
	ds_read_b128 v[46:49], v142 offset:39936
	buffer_load_dwordx4 v1, s[80:83], s42 offen lds
	s_add_i32 s42, s39, 0x60000
	s_mov_b32 m0, s19
	s_nop 0
	buffer_load_dwordx4 v1, s[80:83], s42 offen lds
	s_waitcnt vmcnt(8)
	s_waitcnt lgkmcnt(0)
	s_barrier
	s_waitcnt lgkmcnt(6)
	v_mfma_scale_f32_16x16x128_f8f6f4 v[126:129], v[2:9], v[18:25], v[126:129], v143, v143 op_sel:[0,1,0] op_sel_hi:[0,0,0]
	v_mfma_scale_f32_16x16x128_f8f6f4 v[122:125], v[10:17], v[18:25], v[122:125], v143, v143 op_sel:[0,1,0] op_sel_hi:[0,0,0]
	s_waitcnt lgkmcnt(4)
	v_mfma_scale_f32_16x16x128_f8f6f4 v[118:121], v[2:9], v[26:33], v[118:121], v143, v143 op_sel:[0,1,0] op_sel_hi:[0,0,0]
	v_mfma_scale_f32_16x16x128_f8f6f4 v[110:113], v[10:17], v[26:33], v[110:113], v143, v143 op_sel:[0,1,0] op_sel_hi:[0,0,0]
	s_waitcnt lgkmcnt(2)
	v_mfma_scale_f32_16x16x128_f8f6f4 v[102:105], v[2:9], v[34:41], v[102:105], v143, v143 op_sel:[0,1,0] op_sel_hi:[0,0,0]
	v_mfma_scale_f32_16x16x128_f8f6f4 v[94:97], v[10:17], v[34:41], v[136:139], v143, v143 op_sel:[0,1,0] op_sel_hi:[0,0,0]
	s_waitcnt lgkmcnt(0)
	v_mfma_scale_f32_16x16x128_f8f6f4 v[86:89], v[2:9], v[42:49], v[212:215], v143, v143 op_sel:[0,1,0] op_sel_hi:[0,0,0]
	v_mfma_scale_f32_16x16x128_f8f6f4 v[78:81], v[10:17], v[42:49], v[216:219], v143, v143 op_sel:[0,1,0] op_sel_hi:[0,0,0]
	v_mfma_scale_f32_16x16x128_f8f6f4 v[114:117], v[148:155], v[18:25], v[114:117], v143, v143 op_sel:[0,1,0] op_sel_hi:[0,0,0]
	v_mfma_scale_f32_16x16x128_f8f6f4 v[106:109], v[156:163], v[18:25], v[106:109], v143, v143 op_sel:[0,1,0] op_sel_hi:[0,0,0]
	v_mfma_scale_f32_16x16x128_f8f6f4 v[98:101], v[148:155], v[26:33], v[98:101], v143, v143 op_sel:[0,1,0] op_sel_hi:[0,0,0]
	v_mfma_scale_f32_16x16x128_f8f6f4 v[90:93], v[156:163], v[26:33], v[180:183], v143, v143 op_sel:[0,1,0] op_sel_hi:[0,0,0]
	v_mfma_scale_f32_16x16x128_f8f6f4 v[82:85], v[148:155], v[34:41], v[184:187], v143, v143 op_sel:[0,1,0] op_sel_hi:[0,0,0]
	v_mfma_scale_f32_16x16x128_f8f6f4 v[74:77], v[156:163], v[34:41], v[188:191], v143, v143 op_sel:[0,1,0] op_sel_hi:[0,0,0]
	v_mfma_scale_f32_16x16x128_f8f6f4 v[70:73], v[148:155], v[42:49], v[192:195], v143, v143 op_sel:[0,1,0] op_sel_hi:[0,0,0]
	v_mfma_scale_f32_16x16x128_f8f6f4 v[66:69], v[156:163], v[42:49], v[196:199], v143, v143 op_sel:[0,1,0] op_sel_hi:[0,0,0]
	s_barrier
	s_mov_b32 m0, s21
	s_add_i32 s42, s41, 0x80
	ds_read_b128 v[164:167], v142 offset:49152
	ds_read_b128 v[168:171], v142 offset:50176
	ds_read_b128 v[172:175], v142 offset:51200
	ds_read_b128 v[176:179], v142 offset:52224
	ds_read_b128 v[180:183], v142 offset:53248
	ds_read_b128 v[184:187], v142 offset:54272
	ds_read_b128 v[188:191], v142 offset:55296
	ds_read_b128 v[192:195], v142 offset:56320
	buffer_load_dwordx4 v135, s[80:83], s42 offen lds
	s_add_i32 s42, s41, 0x20080
	s_mov_b32 m0, s22
	s_add_i32 s39, s39, 0x20080
	buffer_load_dwordx4 v135, s[80:83], s42 offen lds
	s_add_i32 s42, s41, 0x40080
	s_mov_b32 m0, s25
	s_add_i32 s41, s41, 0x60080
	buffer_load_dwordx4 v135, s[80:83], s42 offen lds
	s_mov_b32 m0, s26
	s_nop 0
	buffer_load_dwordx4 v135, s[80:83], s41 offen lds
	s_mov_b32 m0, s23
	s_nop 0
	buffer_load_dwordx4 v1, s[80:83], s40 offen lds
	s_mov_b32 m0, s24
	s_nop 0
	buffer_load_dwordx4 v1, s[80:83], s39 offen lds
	s_waitcnt vmcnt(8)
	s_waitcnt lgkmcnt(0)
	s_barrier
	s_waitcnt lgkmcnt(6)
	v_mfma_scale_f32_16x16x128_f8f6f4 v[62:65], v[2:9], v[164:171], v[62:65], v143, v143 op_sel:[0,1,0] op_sel_hi:[0,0,0]
	v_mfma_scale_f32_16x16x128_f8f6f4 v[58:61], v[10:17], v[164:171], v[58:61], v143, v143 op_sel:[0,1,0] op_sel_hi:[0,0,0]
	s_waitcnt lgkmcnt(4)
	v_mfma_scale_f32_16x16x128_f8f6f4 v[54:57], v[2:9], v[172:179], v[54:57], v143, v143 op_sel:[0,1,0] op_sel_hi:[0,0,0]
	v_mfma_scale_f32_16x16x128_f8f6f4 v[46:49], v[10:17], v[172:179], v[200:203], v143, v143 op_sel:[0,1,0] op_sel_hi:[0,0,0]
	s_waitcnt lgkmcnt(2)
	v_mfma_scale_f32_16x16x128_f8f6f4 v[38:41], v[2:9], v[180:187], v[204:207], v143, v143 op_sel:[0,1,0] op_sel_hi:[0,0,0]
	v_mfma_scale_f32_16x16x128_f8f6f4 v[30:33], v[10:17], v[180:187], v[208:211], v143, v143 op_sel:[0,1,0] op_sel_hi:[0,0,0]
	s_waitcnt lgkmcnt(0)
	v_mfma_scale_f32_16x16x128_f8f6f4 v[22:25], v[2:9], v[188:195], v[220:223], v143, v143 op_sel:[0,1,0] op_sel_hi:[0,0,0]
	v_mfma_scale_f32_16x16x128_f8f6f4 v[14:17], v[10:17], v[188:195], v[224:227], v143, v143 op_sel:[0,1,0] op_sel_hi:[0,0,0]
	v_mfma_scale_f32_16x16x128_f8f6f4 v[50:53], v[148:155], v[164:171], v[50:53], v143, v143 op_sel:[0,1,0] op_sel_hi:[0,0,0]
	v_mfma_scale_f32_16x16x128_f8f6f4 v[42:45], v[156:163], v[164:171], v[228:231], v143, v143 op_sel:[0,1,0] op_sel_hi:[0,0,0]
	v_mfma_scale_f32_16x16x128_f8f6f4 v[34:37], v[148:155], v[172:179], v[232:235], v143, v143 op_sel:[0,1,0] op_sel_hi:[0,0,0]
	v_mfma_scale_f32_16x16x128_f8f6f4 v[26:29], v[156:163], v[172:179], v[236:239], v143, v143 op_sel:[0,1,0] op_sel_hi:[0,0,0]
	v_mfma_scale_f32_16x16x128_f8f6f4 v[18:21], v[148:155], v[180:187], v[240:243], v143, v143 op_sel:[0,1,0] op_sel_hi:[0,0,0]
	v_mfma_scale_f32_16x16x128_f8f6f4 v[10:13], v[156:163], v[180:187], v[244:247], v143, v143 op_sel:[0,1,0] op_sel_hi:[0,0,0]
	v_mfma_scale_f32_16x16x128_f8f6f4 v[6:9], v[148:155], v[188:195], v[248:251], v143, v143 op_sel:[0,1,0] op_sel_hi:[0,0,0]
	v_mfma_scale_f32_16x16x128_f8f6f4 v[2:5], v[156:163], v[188:195], v[130:133], v143, v143 op_sel:[0,1,0] op_sel_hi:[0,0,0]
	s_barrier
	s_add_i32 s38, s38, 2
	s_addk_i32 s36, 0x100
	s_addk_i32 s37, 0x100
	s_cmp_gt_u32 s38, 13
	s_cbranch_scc0 .LBB0_739
	s_and_b64 vcc, exec, s[6:7]
	s_cbranch_vccz .LBB0_742
	s_barrier

; #define PG8_STAGE(bufoff, goff, voff) do { _Pragma("unroll") for (int _i = 0; _i < 2; ++_i) \
;         __builtin_amdgcn_raw_ptr_buffer_load_lds(rsrc, (PG8_LAS void*)(lds + (bufoff) + ldsw + _i * 8192), 16, (int)(voff), (int)((goff) + _i * p1##voff), 0, 0); } while (0)
; #define PG8_LDA(dst, b, h) do { _Pragma("unroll") for (int m = 0; m < 4; ++m) dst[m] = PG8_LD8(lds + PG8_SA(b, h) + aoff + m * 2048); } while (0)
; #define PG8_LDB(dst, b, h) do { _Pragma("unroll") for (int n = 0; n < 2; ++n) dst[n] = PG8_LD8(lds + PG8_SB(b, h) + boff + n * 2048); } while (0)
; #define PG8_WAIT_V(n) asm volatile("s_waitcnt vmcnt(" #n ")" ::: "memory")
; #define PG8_WAIT_L(n) asm volatile("s_waitcnt lgkmcnt(" #n ")" ::: "memory")
; #define PG8_BAR __builtin_amdgcn_s_barrier()
; #define PG8_SCHED __builtin_amdgcn_sched_barrier(0)
; template <class Epi, class Sched, bool ALIGN_EPI, bool F8 = false, int F8SC = F8_SCALES>
; __device__ __forceinline__ void gemm_phase(PG8_LAS unsigned char* lds, const __amdgpu_buffer_rsrc_t rsrc, const int lda, const int ldb, const int K, const Sched& S, const Epi& E) {
;     ...
;             PG8_LDB(B0, 0, 0); PG8_LDB(B1, 0, 1); PG8_SCHED; PG8_LDA(At, 0, 0); PG8_STAGE(PG8_SA(1, 1), a1 + hsA, voffA);
;             PG8_WAIT_V(8); PG8_WAIT_L(0); PG8_BAR; PG8_MMA(0, 0, At, B0); PG8_MMA(0, 1, At, B1); PG8_BAR; PG8_SCHED;
;             PG8_LDA(At, 0, 1); PG8_STAGE(PG8_SB(0, 0), b2, voffB); PG8_STAGE(PG8_SB(0, 1), b2 + hsB, voffB); PG8_STAGE(PG8_SA(0, 0), a2, voffA);
;             PG8_WAIT_V(8); PG8_WAIT_L(0); PG8_BAR; PG8_MMA(1, 0, At, B0); PG8_MMA(1, 1, At, B1); PG8_BAR; PG8_SCHED;
.LBB0_765:
	ds_read_b128 v[146:149], v139
	ds_read_b128 v[150:153], v139 offset:1024
	ds_read_b128 v[154:157], v139 offset:2048
	ds_read_b128 v[158:161], v139 offset:3072
	ds_read_b128 v[162:165], v140
	ds_read_b128 v[166:169], v140 offset:1024
	ds_read_b128 v[170:173], v140 offset:2048
	ds_read_b128 v[174:177], v140 offset:3072
	s_add_i32 s38, s4, 0xfffa0080
	s_cmp_eq_u32 s37, 12
	s_cselect_b32 s38, s33, s38
	s_cselect_b32 s40, s34, s5
	s_add_i32 s39, s38, 0x80
	s_add_i32 s41, s4, 0xfffe0000
	s_mov_b32 s80, s96
	s_mov_b32 m0, s27
	ds_read_b128 v[178:181], v141
	ds_read_b128 v[182:185], v141 offset:1024
	ds_read_b128 v[186:189], v141 offset:2048
	ds_read_b128 v[190:193], v141 offset:3072
	ds_read_b128 v[194:197], v141 offset:4096
	ds_read_b128 v[198:201], v141 offset:5120
	ds_read_b128 v[202:205], v141 offset:6144
	ds_read_b128 v[206:209], v141 offset:7168
	buffer_load_dwordx4 v1, s[80:83], s41 offen lds
	s_mov_b32 m0, s28
	s_nop 0
	buffer_load_dwordx4 v1, s[80:83], s4 offen lds
	s_waitcnt vmcnt(8)
	s_waitcnt lgkmcnt(0)
	s_barrier
	s_waitcnt lgkmcnt(6)
	v_mfma_scale_f32_16x16x128_f8f6f4 v[126:129], v[146:153], v[178:185], v[126:129], v142, v142 op_sel:[0,1,0] op_sel_hi:[0,0,0]
	v_mfma_scale_f32_16x16x128_f8f6f4 v[118:121], v[154:161], v[178:185], v[118:121], v142, v142 op_sel:[0,1,0] op_sel_hi:[0,0,0]
	s_waitcnt lgkmcnt(4)
	v_mfma_scale_f32_16x16x128_f8f6f4 v[110:113], v[146:153], v[186:193], v[110:113], v142, v142 op_sel:[0,1,0] op_sel_hi:[0,0,0]
	v_mfma_scale_f32_16x16x128_f8f6f4 v[102:105], v[154:161], v[186:193], v[102:105], v142, v142 op_sel:[0,1,0] op_sel_hi:[0,0,0]
	s_waitcnt lgkmcnt(2)
	v_mfma_scale_f32_16x16x128_f8f6f4 v[210:213], v[146:153], v[194:201], v[94:97], v142, v142 op_sel:[0,1,0] op_sel_hi:[0,0,0]
	v_mfma_scale_f32_16x16x128_f8f6f4 v[214:217], v[154:161], v[194:201], v[86:89], v142, v142 op_sel:[0,1,0] op_sel_hi:[0,0,0]
	s_waitcnt lgkmcnt(0)
	v_mfma_scale_f32_16x16x128_f8f6f4 v[218:221], v[146:153], v[202:209], v[78:81], v142, v142 op_sel:[0,1,0] op_sel_hi:[0,0,0]
	v_mfma_scale_f32_16x16x128_f8f6f4 v[222:225], v[154:161], v[202:209], v[70:73], v142, v142 op_sel:[0,1,0] op_sel_hi:[0,0,0]
	v_mfma_scale_f32_16x16x128_f8f6f4 v[122:125], v[162:169], v[178:185], v[122:125], v142, v142 op_sel:[0,1,0] op_sel_hi:[0,0,0]
	v_mfma_scale_f32_16x16x128_f8f6f4 v[114:117], v[170:177], v[178:185], v[114:117], v142, v142 op_sel:[0,1,0] op_sel_hi:[0,0,0]
	v_mfma_scale_f32_16x16x128_f8f6f4 v[106:109], v[162:169], v[186:193], v[106:109], v142, v142 op_sel:[0,1,0] op_sel_hi:[0,0,0]
	v_mfma_scale_f32_16x16x128_f8f6f4 v[98:101], v[170:177], v[186:193], v[98:101], v142, v142 op_sel:[0,1,0] op_sel_hi:[0,0,0]
	v_mfma_scale_f32_16x16x128_f8f6f4 v[178:181], v[162:169], v[194:201], v[90:93], v142, v142 op_sel:[0,1,0] op_sel_hi:[0,0,0]
	v_mfma_scale_f32_16x16x128_f8f6f4 v[182:185], v[170:177], v[194:201], v[82:85], v142, v142 op_sel:[0,1,0] op_sel_hi:[0,0,0]
	v_mfma_scale_f32_16x16x128_f8f6f4 v[186:189], v[162:169], v[202:209], v[74:77], v142, v142 op_sel:[0,1,0] op_sel_hi:[0,0,0]
	v_mfma_scale_f32_16x16x128_f8f6f4 v[190:193], v[170:177], v[202:209], v[66:69], v142, v142 op_sel:[0,1,0] op_sel_hi:[0,0,0]
	s_barrier
	s_mov_b32 m0, s10
	s_nop 3
	ds_read_b128 v[66:69], v141 offset:16384
	ds_read_b128 v[70:73], v141 offset:17408
	ds_read_b128 v[74:77], v141 offset:18432
	ds_read_b128 v[78:81], v141 offset:19456
	ds_read_b128 v[82:85], v141 offset:20480
	ds_read_b128 v[86:89], v141 offset:21504
	ds_read_b128 v[90:93], v141 offset:22528
	ds_read_b128 v[94:97], v141 offset:23552
	buffer_load_dwordx4 v138, s[80:83], s40 offen lds
	s_add_i32 s41, s40, 0x20000
	s_mov_b32 m0, s11
	s_nop 0
	buffer_load_dwordx4 v138, s[80:83], s41 offen lds
	s_add_i32 s41, s40, 0x40000
	s_mov_b32 m0, s13
	s_nop 0
	buffer_load_dwordx4 v138, s[80:83], s41 offen lds
	s_add_i32 s41, s40, 0x60000
	s_mov_b32 m0, s16
	s_nop 0
	buffer_load_dwordx4 v138, s[80:83], s41 offen lds
	s_mov_b32 m0, s9
	s_add_i32 s41, s38, 0x20000
	buffer_load_dwordx4 v1, s[80:83], s38 offen lds
	s_mov_b32 m0, s17
	s_nop 0
	buffer_load_dwordx4 v1, s[80:83], s41 offen lds
	s_waitcnt vmcnt(8)
	s_waitcnt lgkmcnt(0)
	s_barrier
	s_waitcnt lgkmcnt(6)
	v_mfma_scale_f32_16x16x128_f8f6f4 v[62:65], v[146:153], v[66:73], v[62:65], v142, v142 op_sel:[0,1,0] op_sel_hi:[0,0,0]
	v_mfma_scale_f32_16x16x128_f8f6f4 v[54:57], v[154:161], v[66:73], v[54:57], v142, v142 op_sel:[0,1,0] op_sel_hi:[0,0,0]
	s_waitcnt lgkmcnt(4)
	v_mfma_scale_f32_16x16x128_f8f6f4 v[46:49], v[146:153], v[74:81], v[46:49], v142, v142 op_sel:[0,1,0] op_sel_hi:[0,0,0]
	v_mfma_scale_f32_16x16x128_f8f6f4 v[202:205], v[154:161], v[74:81], v[38:41], v142, v142 op_sel:[0,1,0] op_sel_hi:[0,0,0]
	s_waitcnt lgkmcnt(2)
	v_mfma_scale_f32_16x16x128_f8f6f4 v[206:209], v[146:153], v[82:89], v[30:33], v142, v142 op_sel:[0,1,0] op_sel_hi:[0,0,0]
	v_mfma_scale_f32_16x16x128_f8f6f4 v[226:229], v[154:161], v[82:89], v[22:25], v142, v142 op_sel:[0,1,0] op_sel_hi:[0,0,0]
	s_waitcnt lgkmcnt(0)
	v_mfma_scale_f32_16x16x128_f8f6f4 v[230:233], v[146:153], v[90:97], v[14:17], v142, v142 op_sel:[0,1,0] op_sel_hi:[0,0,0]
	v_mfma_scale_f32_16x16x128_f8f6f4 v[234:237], v[154:161], v[90:97], v[6:9], v142, v142 op_sel:[0,1,0] op_sel_hi:[0,0,0]
	v_mfma_scale_f32_16x16x128_f8f6f4 v[58:61], v[162:169], v[66:73], v[58:61], v142, v142 op_sel:[0,1,0] op_sel_hi:[0,0,0]
	v_mfma_scale_f32_16x16x128_f8f6f4 v[50:53], v[170:177], v[66:73], v[50:53], v142, v142 op_sel:[0,1,0] op_sel_hi:[0,0,0]
	v_mfma_scale_f32_16x16x128_f8f6f4 v[42:45], v[162:169], v[74:81], v[42:45], v142, v142 op_sel:[0,1,0] op_sel_hi:[0,0,0]
	v_mfma_scale_f32_16x16x128_f8f6f4 v[238:241], v[170:177], v[74:81], v[34:37], v142, v142 op_sel:[0,1,0] op_sel_hi:[0,0,0]
	v_mfma_scale_f32_16x16x128_f8f6f4 v[242:245], v[162:169], v[82:89], v[26:29], v142, v142 op_sel:[0,1,0] op_sel_hi:[0,0,0]
	v_mfma_scale_f32_16x16x128_f8f6f4 v[246:249], v[170:177], v[82:89], v[18:21], v142, v142 op_sel:[0,1,0] op_sel_hi:[0,0,0]
	v_mfma_scale_f32_16x16x128_f8f6f4 v[250:253], v[162:169], v[90:97], v[10:13], v142, v142 op_sel:[0,1,0] op_sel_hi:[0,0,0]
	v_mfma_scale_f32_16x16x128_f8f6f4 v[130:133], v[170:177], v[90:97], v[2:5], v142, v142 op_sel:[0,1,0] op_sel_hi:[0,0,0]
	s_barrier
; #define PG8_STAGE(bufoff, goff, voff) do { _Pragma("unroll") for (int _i = 0; _i < 2; ++_i) \
;         __builtin_amdgcn_raw_ptr_buffer_load_lds(rsrc, (PG8_LAS void*)(lds + (bufoff) + ldsw + _i * 8192), 16, (int)(voff), (int)((goff) + _i * p1##voff), 0, 0); } while (0)
; #define PG8_LDA(dst, b, h) do { _Pragma("unroll") for (int m = 0; m < 4; ++m) dst[m] = PG8_LD8(lds + PG8_SA(b, h) + aoff + m * 2048); } while (0)
; #define PG8_LDB(dst, b, h) do { _Pragma("unroll") for (int n = 0; n < 2; ++n) dst[n] = PG8_LD8(lds + PG8_SB(b, h) + boff + n * 2048); } while (0)
; #define PG8_WAIT_V(n) asm volatile("s_waitcnt vmcnt(" #n ")" ::: "memory")
; #define PG8_WAIT_L(n) asm volatile("s_waitcnt lgkmcnt(" #n ")" ::: "memory")
; #define PG8_BAR __builtin_amdgcn_s_barrier()
; #define PG8_SCHED __builtin_amdgcn_sched_barrier(0)
; template <class Epi, class Sched, bool ALIGN_EPI, bool F8 = false, int F8SC = F8_SCALES>
; __device__ __forceinline__ void gemm_phase(PG8_LAS unsigned char* lds, const __amdgpu_buffer_rsrc_t rsrc, const int lda, const int ldb, const int K, const Sched& S, const Epi& E) {
;     ...
;             PG8_LDB(B0, 1, 0); PG8_LDB(B1, 1, 1); PG8_SCHED; PG8_LDA(At, 1, 0); PG8_STAGE(PG8_SA(0, 1), a2 + hsA, voffA);
;             PG8_WAIT_V(8); PG8_WAIT_L(0); PG8_BAR; PG8_MMA(0, 0, At, B0); PG8_MMA(0, 1, At, B1); PG8_BAR; PG8_SCHED;
;             PG8_LDA(At, 1, 1); PG8_STAGE(PG8_SB(1, 0), b3, voffB); PG8_STAGE(PG8_SB(1, 1), b3 + hsB, voffB); PG8_STAGE(PG8_SA(1, 0), a3, voffA);
;             PG8_WAIT_V(8); PG8_WAIT_L(0); PG8_BAR; PG8_MMA(1, 0, At, B0); PG8_MMA(1, 1, At, B1); PG8_BAR; PG8_SCHED;
;         }
	s_nop 4
	ds_read_b128 v[2:5], v143
	ds_read_b128 v[6:9], v143 offset:1024
	ds_read_b128 v[146:149], v143 offset:2048
	ds_read_b128 v[150:153], v143 offset:3072
	ds_read_b128 v[154:157], v144
	ds_read_b128 v[158:161], v144 offset:1024
	ds_read_b128 v[162:165], v144 offset:2048
	ds_read_b128 v[166:169], v144 offset:3072
	s_mov_b32 m0, s18
	s_add_i32 s41, s38, 0x40000
	ds_read_b128 v[10:13], v141 offset:32768
	ds_read_b128 v[14:17], v141 offset:33792
	ds_read_b128 v[18:21], v141 offset:34816
	ds_read_b128 v[22:25], v141 offset:35840
	ds_read_b128 v[26:29], v141 offset:36864
	ds_read_b128 v[30:33], v141 offset:37888
	ds_read_b128 v[34:37], v141 offset:38912
	ds_read_b128 v[38:41], v141 offset:39936
	buffer_load_dwordx4 v1, s[80:83], s41 offen lds
	s_add_i32 s41, s38, 0x60000
	s_mov_b32 m0, s19
	s_nop 0
	buffer_load_dwordx4 v1, s[80:83], s41 offen lds
	s_waitcnt vmcnt(8)
	s_waitcnt lgkmcnt(0)
	s_barrier
	s_waitcnt lgkmcnt(6)
	v_mfma_scale_f32_16x16x128_f8f6f4 v[126:129], v[2:9], v[10:17], v[126:129], v142, v142 op_sel:[0,1,0] op_sel_hi:[0,0,0]
	v_mfma_scale_f32_16x16x128_f8f6f4 v[118:121], v[146:153], v[10:17], v[118:121], v142, v142 op_sel:[0,1,0] op_sel_hi:[0,0,0]
	s_waitcnt lgkmcnt(4)
	v_mfma_scale_f32_16x16x128_f8f6f4 v[110:113], v[2:9], v[18:25], v[110:113], v142, v142 op_sel:[0,1,0] op_sel_hi:[0,0,0]
	v_mfma_scale_f32_16x16x128_f8f6f4 v[102:105], v[146:153], v[18:25], v[102:105], v142, v142 op_sel:[0,1,0] op_sel_hi:[0,0,0]
	s_waitcnt lgkmcnt(2)
	v_mfma_scale_f32_16x16x128_f8f6f4 v[94:97], v[2:9], v[26:33], v[210:213], v142, v142 op_sel:[0,1,0] op_sel_hi:[0,0,0]
	v_mfma_scale_f32_16x16x128_f8f6f4 v[86:89], v[146:153], v[26:33], v[214:217], v142, v142 op_sel:[0,1,0] op_sel_hi:[0,0,0]
	s_waitcnt lgkmcnt(0)
	v_mfma_scale_f32_16x16x128_f8f6f4 v[78:81], v[2:9], v[34:41], v[218:221], v142, v142 op_sel:[0,1,0] op_sel_hi:[0,0,0]
	v_mfma_scale_f32_16x16x128_f8f6f4 v[70:73], v[146:153], v[34:41], v[222:225], v142, v142 op_sel:[0,1,0] op_sel_hi:[0,0,0]
	v_mfma_scale_f32_16x16x128_f8f6f4 v[122:125], v[154:161], v[10:17], v[122:125], v142, v142 op_sel:[0,1,0] op_sel_hi:[0,0,0]
	v_mfma_scale_f32_16x16x128_f8f6f4 v[114:117], v[162:169], v[10:17], v[114:117], v142, v142 op_sel:[0,1,0] op_sel_hi:[0,0,0]
	v_mfma_scale_f32_16x16x128_f8f6f4 v[106:109], v[154:161], v[18:25], v[106:109], v142, v142 op_sel:[0,1,0] op_sel_hi:[0,0,0]
	v_mfma_scale_f32_16x16x128_f8f6f4 v[98:101], v[162:169], v[18:25], v[98:101], v142, v142 op_sel:[0,1,0] op_sel_hi:[0,0,0]
	v_mfma_scale_f32_16x16x128_f8f6f4 v[90:93], v[154:161], v[26:33], v[178:181], v142, v142 op_sel:[0,1,0] op_sel_hi:[0,0,0]
	v_mfma_scale_f32_16x16x128_f8f6f4 v[82:85], v[162:169], v[26:33], v[182:185], v142, v142 op_sel:[0,1,0] op_sel_hi:[0,0,0]
	v_mfma_scale_f32_16x16x128_f8f6f4 v[74:77], v[154:161], v[34:41], v[186:189], v142, v142 op_sel:[0,1,0] op_sel_hi:[0,0,0]
	v_mfma_scale_f32_16x16x128_f8f6f4 v[66:69], v[162:169], v[34:41], v[190:193], v142, v142 op_sel:[0,1,0] op_sel_hi:[0,0,0]
	s_barrier
	s_mov_b32 m0, s21
	s_add_i32 s41, s40, 0x80
	ds_read_b128 v[170:173], v141 offset:49152
	ds_read_b128 v[174:177], v141 offset:50176
	ds_read_b128 v[178:181], v141 offset:51200
	ds_read_b128 v[182:185], v141 offset:52224
	ds_read_b128 v[186:189], v141 offset:53248
	ds_read_b128 v[190:193], v141 offset:54272
	ds_read_b128 v[194:197], v141 offset:55296
	ds_read_b128 v[198:201], v141 offset:56320
	buffer_load_dwordx4 v138, s[80:83], s41 offen lds
	s_add_i32 s41, s40, 0x20080
	s_mov_b32 m0, s22
	s_add_i32 s38, s38, 0x20080
	buffer_load_dwordx4 v138, s[80:83], s41 offen lds
	s_add_i32 s41, s40, 0x40080
	s_mov_b32 m0, s25
	s_add_i32 s40, s40, 0x60080
	buffer_load_dwordx4 v138, s[80:83], s41 offen lds
	s_mov_b32 m0, s26
	s_nop 0
	buffer_load_dwordx4 v138, s[80:83], s40 offen lds
	s_mov_b32 m0, s23
	s_nop 0
	buffer_load_dwordx4 v1, s[80:83], s39 offen lds
	s_mov_b32 m0, s24
	s_nop 0
	buffer_load_dwordx4 v1, s[80:83], s38 offen lds
	s_waitcnt vmcnt(8)
	s_waitcnt lgkmcnt(0)
	s_barrier
	s_waitcnt lgkmcnt(6)
	v_mfma_scale_f32_16x16x128_f8f6f4 v[62:65], v[2:9], v[170:177], v[62:65], v142, v142 op_sel:[0,1,0] op_sel_hi:[0,0,0]
	v_mfma_scale_f32_16x16x128_f8f6f4 v[54:57], v[146:153], v[170:177], v[54:57], v142, v142 op_sel:[0,1,0] op_sel_hi:[0,0,0]
	s_waitcnt lgkmcnt(4)
	v_mfma_scale_f32_16x16x128_f8f6f4 v[46:49], v[2:9], v[178:185], v[46:49], v142, v142 op_sel:[0,1,0] op_sel_hi:[0,0,0]
	v_mfma_scale_f32_16x16x128_f8f6f4 v[38:41], v[146:153], v[178:185], v[202:205], v142, v142 op_sel:[0,1,0] op_sel_hi:[0,0,0]
	s_waitcnt lgkmcnt(2)
	v_mfma_scale_f32_16x16x128_f8f6f4 v[30:33], v[2:9], v[186:193], v[206:209], v142, v142 op_sel:[0,1,0] op_sel_hi:[0,0,0]
	v_mfma_scale_f32_16x16x128_f8f6f4 v[22:25], v[146:153], v[186:193], v[226:229], v142, v142 op_sel:[0,1,0] op_sel_hi:[0,0,0]
	s_waitcnt lgkmcnt(0)
	v_mfma_scale_f32_16x16x128_f8f6f4 v[14:17], v[2:9], v[194:201], v[230:233], v142, v142 op_sel:[0,1,0] op_sel_hi:[0,0,0]
	v_mfma_scale_f32_16x16x128_f8f6f4 v[6:9], v[146:153], v[194:201], v[234:237], v142, v142 op_sel:[0,1,0] op_sel_hi:[0,0,0]
	v_mfma_scale_f32_16x16x128_f8f6f4 v[58:61], v[154:161], v[170:177], v[58:61], v142, v142 op_sel:[0,1,0] op_sel_hi:[0,0,0]
	v_mfma_scale_f32_16x16x128_f8f6f4 v[50:53], v[162:169], v[170:177], v[50:53], v142, v142 op_sel:[0,1,0] op_sel_hi:[0,0,0]
	v_mfma_scale_f32_16x16x128_f8f6f4 v[42:45], v[154:161], v[178:185], v[42:45], v142, v142 op_sel:[0,1,0] op_sel_hi:[0,0,0]
	v_mfma_scale_f32_16x16x128_f8f6f4 v[34:37], v[162:169], v[178:185], v[238:241], v142, v142 op_sel:[0,1,0] op_sel_hi:[0,0,0]
	v_mfma_scale_f32_16x16x128_f8f6f4 v[26:29], v[154:161], v[186:193], v[242:245], v142, v142 op_sel:[0,1,0] op_sel_hi:[0,0,0]
	v_mfma_scale_f32_16x16x128_f8f6f4 v[18:21], v[162:169], v[186:193], v[246:249], v142, v142 op_sel:[0,1,0] op_sel_hi:[0,0,0]
	v_mfma_scale_f32_16x16x128_f8f6f4 v[10:13], v[154:161], v[194:201], v[250:253], v142, v142 op_sel:[0,1,0] op_sel_hi:[0,0,0]
	v_mfma_scale_f32_16x16x128_f8f6f4 v[2:5], v[162:169], v[194:201], v[130:133], v142, v142 op_sel:[0,1,0] op_sel_hi:[0,0,0]
	s_barrier
	s_add_i32 s37, s37, 2
	s_addk_i32 s4, 0x100
	s_addk_i32 s5, 0x100
	s_cmp_gt_u32 s37, 13
	s_cbranch_scc0 .LBB0_765
	s_and_b64 vcc, exec, s[6:7]
	s_cbranch_vccz .LBB0_768
	s_barrier

; #define PG8_STAGE(bufoff, goff, voff) do { _Pragma("unroll") for (int _i = 0; _i < 2; ++_i) \
;         __builtin_amdgcn_raw_ptr_buffer_load_lds(rsrc, (PG8_LAS void*)(lds + (bufoff) + ldsw + _i * 8192), 16, (int)(voff), (int)((goff) + _i * p1##voff), 0, 0); } while (0)
; #define PG8_LDA(dst, b, h) do { _Pragma("unroll") for (int m = 0; m < 4; ++m) dst[m] = PG8_LD8(lds + PG8_SA(b, h) + aoff + m * 2048); } while (0)
; #define PG8_LDB(dst, b, h) do { _Pragma("unroll") for (int n = 0; n < 2; ++n) dst[n] = PG8_LD8(lds + PG8_SB(b, h) + boff + n * 2048); } while (0)
; #define PG8_WAIT_V(n) asm volatile("s_waitcnt vmcnt(" #n ")" ::: "memory")
; #define PG8_WAIT_L(n) asm volatile("s_waitcnt lgkmcnt(" #n ")" ::: "memory")
; #define PG8_BAR __builtin_amdgcn_s_barrier()
; #define PG8_SCHED __builtin_amdgcn_sched_barrier(0)
; template <class Epi, class Sched, bool ALIGN_EPI, bool F8 = false, int F8SC = F8_SCALES>
; __device__ __forceinline__ void gemm_phase(PG8_LAS unsigned char* lds, const __amdgpu_buffer_rsrc_t rsrc, const int lda, const int ldb, const int K, const Sched& S, const Epi& E) {
;     ...
;             PG8_LDB(B0, 0, 0); PG8_LDB(B1, 0, 1); PG8_SCHED; PG8_LDA(At, 0, 0); PG8_STAGE(PG8_SA(1, 1), a1 + hsA, voffA);
;             PG8_WAIT_V(8); PG8_WAIT_L(0); PG8_BAR; PG8_MMA(0, 0, At, B0); PG8_MMA(0, 1, At, B1); PG8_BAR; PG8_SCHED;
;             PG8_LDA(At, 0, 1); PG8_STAGE(PG8_SB(0, 0), b2, voffB); PG8_STAGE(PG8_SB(0, 1), b2 + hsB, voffB); PG8_STAGE(PG8_SA(0, 0), a2, voffA);
;             PG8_WAIT_V(8); PG8_WAIT_L(0); PG8_BAR; PG8_MMA(1, 0, At, B0); PG8_MMA(1, 1, At, B1); PG8_BAR; PG8_SCHED;
.LBB0_791:
	ds_read_b128 v[142:145], v135
	ds_read_b128 v[146:149], v135 offset:1024
	ds_read_b128 v[150:153], v135 offset:2048
	ds_read_b128 v[154:157], v135 offset:3072
	ds_read_b128 v[158:161], v136
	ds_read_b128 v[162:165], v136 offset:1024
	ds_read_b128 v[166:169], v136 offset:2048
	ds_read_b128 v[170:173], v136 offset:3072
	s_add_i32 s42, s39, 0xfffa0080
	s_cmp_eq_u32 s41, 12
	s_cselect_b32 s42, s4, s42
	s_cselect_b32 s44, s5, s40
	s_add_i32 s43, s42, 0x80
	s_add_i32 s45, s39, 0xfffe0000
	s_mov_b32 s80, s96
	s_mov_b32 m0, s31
	ds_read_b128 v[174:177], v137
	ds_read_b128 v[178:181], v137 offset:1024
	ds_read_b128 v[182:185], v137 offset:2048
	ds_read_b128 v[186:189], v137 offset:3072
	ds_read_b128 v[190:193], v137 offset:4096
	ds_read_b128 v[194:197], v137 offset:5120
	ds_read_b128 v[198:201], v137 offset:6144
	ds_read_b128 v[202:205], v137 offset:7168
	buffer_load_dwordx4 v1, s[80:83], s45 offen lds
	s_mov_b32 m0, s33
	s_nop 0
	buffer_load_dwordx4 v1, s[80:83], s39 offen lds
	s_waitcnt vmcnt(8)
	s_waitcnt lgkmcnt(0)
	s_barrier
	s_waitcnt lgkmcnt(6)
	v_mfma_scale_f32_16x16x128_f8f6f4 v[126:129], v[142:149], v[174:181], v[126:129], v138, v138 op_sel:[0,1,0] op_sel_hi:[0,0,0]
	v_mfma_scale_f32_16x16x128_f8f6f4 v[122:125], v[150:157], v[174:181], v[122:125], v138, v138 op_sel:[0,1,0] op_sel_hi:[0,0,0]
	s_waitcnt lgkmcnt(4)
	v_mfma_scale_f32_16x16x128_f8f6f4 v[118:121], v[142:149], v[182:189], v[118:121], v138, v138 op_sel:[0,1,0] op_sel_hi:[0,0,0]
	v_mfma_scale_f32_16x16x128_f8f6f4 v[114:117], v[150:157], v[182:189], v[114:117], v138, v138 op_sel:[0,1,0] op_sel_hi:[0,0,0]
	s_waitcnt lgkmcnt(2)
	v_mfma_scale_f32_16x16x128_f8f6f4 v[102:105], v[142:149], v[190:197], v[102:105], v138, v138 op_sel:[0,1,0] op_sel_hi:[0,0,0]
	v_mfma_scale_f32_16x16x128_f8f6f4 v[98:101], v[150:157], v[190:197], v[98:101], v138, v138 op_sel:[0,1,0] op_sel_hi:[0,0,0]
	s_waitcnt lgkmcnt(0)
	v_mfma_scale_f32_16x16x128_f8f6f4 v[206:209], v[142:149], v[198:205], v[86:89], v138, v138 op_sel:[0,1,0] op_sel_hi:[0,0,0]
	v_mfma_scale_f32_16x16x128_f8f6f4 v[210:213], v[150:157], v[198:205], v[82:85], v138, v138 op_sel:[0,1,0] op_sel_hi:[0,0,0]
	v_mfma_scale_f32_16x16x128_f8f6f4 v[110:113], v[158:165], v[174:181], v[110:113], v138, v138 op_sel:[0,1,0] op_sel_hi:[0,0,0]
	v_mfma_scale_f32_16x16x128_f8f6f4 v[106:109], v[166:173], v[174:181], v[106:109], v138, v138 op_sel:[0,1,0] op_sel_hi:[0,0,0]
	v_mfma_scale_f32_16x16x128_f8f6f4 v[174:177], v[158:165], v[182:189], v[94:97], v138, v138 op_sel:[0,1,0] op_sel_hi:[0,0,0]
	v_mfma_scale_f32_16x16x128_f8f6f4 v[178:181], v[166:173], v[182:189], v[90:93], v138, v138 op_sel:[0,1,0] op_sel_hi:[0,0,0]
	v_mfma_scale_f32_16x16x128_f8f6f4 v[182:185], v[158:165], v[190:197], v[78:81], v138, v138 op_sel:[0,1,0] op_sel_hi:[0,0,0]
	v_mfma_scale_f32_16x16x128_f8f6f4 v[186:189], v[166:173], v[190:197], v[74:77], v138, v138 op_sel:[0,1,0] op_sel_hi:[0,0,0]
	v_mfma_scale_f32_16x16x128_f8f6f4 v[190:193], v[158:165], v[198:205], v[70:73], v138, v138 op_sel:[0,1,0] op_sel_hi:[0,0,0]
	v_mfma_scale_f32_16x16x128_f8f6f4 v[194:197], v[166:173], v[198:205], v[66:69], v138, v138 op_sel:[0,1,0] op_sel_hi:[0,0,0]
	s_barrier
	s_mov_b32 m0, s17
	s_nop 3
	ds_read_b128 v[66:69], v137 offset:16384
	ds_read_b128 v[70:73], v137 offset:17408
	ds_read_b128 v[74:77], v137 offset:18432
	ds_read_b128 v[78:81], v137 offset:19456
	ds_read_b128 v[82:85], v137 offset:20480
	ds_read_b128 v[86:89], v137 offset:21504
	ds_read_b128 v[90:93], v137 offset:22528
	ds_read_b128 v[94:97], v137 offset:23552
	buffer_load_dwordx4 v134, s[80:83], s44 offen lds
	s_add_i32 s45, s44, 0x20000
	s_mov_b32 m0, s18
	s_nop 0
	buffer_load_dwordx4 v134, s[80:83], s45 offen lds
	s_add_i32 s45, s44, 0x40000
	s_mov_b32 m0, s19
	s_nop 0
	buffer_load_dwordx4 v134, s[80:83], s45 offen lds
	s_add_i32 s45, s44, 0x60000
	s_mov_b32 m0, s20
	s_nop 0
	buffer_load_dwordx4 v134, s[80:83], s45 offen lds
	s_mov_b32 m0, s16
	s_add_i32 s45, s42, 0x20000
	buffer_load_dwordx4 v1, s[80:83], s42 offen lds
	s_mov_b32 m0, s21
	s_nop 0
	buffer_load_dwordx4 v1, s[80:83], s45 offen lds
	s_waitcnt vmcnt(8)
	s_waitcnt lgkmcnt(0)
	s_barrier
	s_waitcnt lgkmcnt(6)
	v_mfma_scale_f32_16x16x128_f8f6f4 v[62:65], v[142:149], v[66:73], v[62:65], v138, v138 op_sel:[0,1,0] op_sel_hi:[0,0,0]
	v_mfma_scale_f32_16x16x128_f8f6f4 v[58:61], v[150:157], v[66:73], v[58:61], v138, v138 op_sel:[0,1,0] op_sel_hi:[0,0,0]
	s_waitcnt lgkmcnt(4)
	v_mfma_scale_f32_16x16x128_f8f6f4 v[54:57], v[142:149], v[74:81], v[54:57], v138, v138 op_sel:[0,1,0] op_sel_hi:[0,0,0]
	v_mfma_scale_f32_16x16x128_f8f6f4 v[50:53], v[150:157], v[74:81], v[50:53], v138, v138 op_sel:[0,1,0] op_sel_hi:[0,0,0]
	s_waitcnt lgkmcnt(2)
	v_mfma_scale_f32_16x16x128_f8f6f4 v[198:201], v[142:149], v[82:89], v[38:41], v138, v138 op_sel:[0,1,0] op_sel_hi:[0,0,0]
	v_mfma_scale_f32_16x16x128_f8f6f4 v[202:205], v[150:157], v[82:89], v[34:37], v138, v138 op_sel:[0,1,0] op_sel_hi:[0,0,0]
	s_waitcnt lgkmcnt(0)
	v_mfma_scale_f32_16x16x128_f8f6f4 v[214:217], v[142:149], v[90:97], v[22:25], v138, v138 op_sel:[0,1,0] op_sel_hi:[0,0,0]
	v_mfma_scale_f32_16x16x128_f8f6f4 v[218:221], v[150:157], v[90:97], v[18:21], v138, v138 op_sel:[0,1,0] op_sel_hi:[0,0,0]
	v_mfma_scale_f32_16x16x128_f8f6f4 v[222:225], v[158:165], v[66:73], v[46:49], v138, v138 op_sel:[0,1,0] op_sel_hi:[0,0,0]
	v_mfma_scale_f32_16x16x128_f8f6f4 v[226:229], v[166:173], v[66:73], v[42:45], v138, v138 op_sel:[0,1,0] op_sel_hi:[0,0,0]
	v_mfma_scale_f32_16x16x128_f8f6f4 v[230:233], v[158:165], v[74:81], v[30:33], v138, v138 op_sel:[0,1,0] op_sel_hi:[0,0,0]
	v_mfma_scale_f32_16x16x128_f8f6f4 v[234:237], v[166:173], v[74:81], v[26:29], v138, v138 op_sel:[0,1,0] op_sel_hi:[0,0,0]
	v_mfma_scale_f32_16x16x128_f8f6f4 v[238:241], v[158:165], v[82:89], v[14:17], v138, v138 op_sel:[0,1,0] op_sel_hi:[0,0,0]
	v_mfma_scale_f32_16x16x128_f8f6f4 v[242:245], v[166:173], v[82:89], v[10:13], v138, v138 op_sel:[0,1,0] op_sel_hi:[0,0,0]
	v_mfma_scale_f32_16x16x128_f8f6f4 v[246:249], v[158:165], v[90:97], v[6:9], v138, v138 op_sel:[0,1,0] op_sel_hi:[0,0,0]
	v_mfma_scale_f32_16x16x128_f8f6f4 v[250:253], v[166:173], v[90:97], v[2:5], v138, v138 op_sel:[0,1,0] op_sel_hi:[0,0,0]
	s_barrier
; #define PG8_STAGE(bufoff, goff, voff) do { _Pragma("unroll") for (int _i = 0; _i < 2; ++_i) \
;         __builtin_amdgcn_raw_ptr_buffer_load_lds(rsrc, (PG8_LAS void*)(lds + (bufoff) + ldsw + _i * 8192), 16, (int)(voff), (int)((goff) + _i * p1##voff), 0, 0); } while (0)
; #define PG8_LDA(dst, b, h) do { _Pragma("unroll") for (int m = 0; m < 4; ++m) dst[m] = PG8_LD8(lds + PG8_SA(b, h) + aoff + m * 2048); } while (0)
; #define PG8_LDB(dst, b, h) do { _Pragma("unroll") for (int n = 0; n < 2; ++n) dst[n] = PG8_LD8(lds + PG8_SB(b, h) + boff + n * 2048); } while (0)
; #define PG8_WAIT_V(n) asm volatile("s_waitcnt vmcnt(" #n ")" ::: "memory")
; #define PG8_WAIT_L(n) asm volatile("s_waitcnt lgkmcnt(" #n ")" ::: "memory")
; #define PG8_BAR __builtin_amdgcn_s_barrier()
; #define PG8_SCHED __builtin_amdgcn_sched_barrier(0)
; template <class Epi, class Sched, bool ALIGN_EPI, bool F8 = false, int F8SC = F8_SCALES>
; __device__ __forceinline__ void gemm_phase(PG8_LAS unsigned char* lds, const __amdgpu_buffer_rsrc_t rsrc, const int lda, const int ldb, const int K, const Sched& S, const Epi& E) {
;     ...
;             PG8_LDB(B0, 1, 0); PG8_LDB(B1, 1, 1); PG8_SCHED; PG8_LDA(At, 1, 0); PG8_STAGE(PG8_SA(0, 1), a2 + hsA, voffA);
;             PG8_WAIT_V(8); PG8_WAIT_L(0); PG8_BAR; PG8_MMA(0, 0, At, B0); PG8_MMA(0, 1, At, B1); PG8_BAR; PG8_SCHED;
;             PG8_LDA(At, 1, 1); PG8_STAGE(PG8_SB(1, 0), b3, voffB); PG8_STAGE(PG8_SB(1, 1), b3 + hsB, voffB); PG8_STAGE(PG8_SA(1, 0), a3, voffA);
;             PG8_WAIT_V(8); PG8_WAIT_L(0); PG8_BAR; PG8_MMA(1, 0, At, B0); PG8_MMA(1, 1, At, B1); PG8_BAR; PG8_SCHED;
;         }
	s_nop 4
	ds_read_b128 v[2:5], v139
	ds_read_b128 v[6:9], v139 offset:1024
	ds_read_b128 v[10:13], v139 offset:2048
	ds_read_b128 v[14:17], v139 offset:3072
	ds_read_b128 v[142:145], v140
	ds_read_b128 v[146:149], v140 offset:1024
	ds_read_b128 v[150:153], v140 offset:2048
	ds_read_b128 v[154:157], v140 offset:3072
	s_mov_b32 m0, s22
	s_add_i32 s45, s42, 0x40000
	ds_read_b128 v[18:21], v137 offset:32768
	ds_read_b128 v[22:25], v137 offset:33792
	ds_read_b128 v[26:29], v137 offset:34816
	ds_read_b128 v[30:33], v137 offset:35840
	ds_read_b128 v[34:37], v137 offset:36864
	ds_read_b128 v[38:41], v137 offset:37888
	ds_read_b128 v[42:45], v137 offset:38912
	ds_read_b128 v[46:49], v137 offset:39936
	buffer_load_dwordx4 v1, s[80:83], s45 offen lds
	s_add_i32 s45, s42, 0x60000
	s_mov_b32 m0, s23
	s_nop 0
	buffer_load_dwordx4 v1, s[80:83], s45 offen lds
	s_waitcnt vmcnt(8)
	s_waitcnt lgkmcnt(0)
	s_barrier
	s_waitcnt lgkmcnt(6)
	v_mfma_scale_f32_16x16x128_f8f6f4 v[126:129], v[2:9], v[18:25], v[126:129], v138, v138 op_sel:[0,1,0] op_sel_hi:[0,0,0]
	v_mfma_scale_f32_16x16x128_f8f6f4 v[122:125], v[10:17], v[18:25], v[122:125], v138, v138 op_sel:[0,1,0] op_sel_hi:[0,0,0]
	s_waitcnt lgkmcnt(4)
	v_mfma_scale_f32_16x16x128_f8f6f4 v[118:121], v[2:9], v[26:33], v[118:121], v138, v138 op_sel:[0,1,0] op_sel_hi:[0,0,0]
	v_mfma_scale_f32_16x16x128_f8f6f4 v[114:117], v[10:17], v[26:33], v[114:117], v138, v138 op_sel:[0,1,0] op_sel_hi:[0,0,0]
	s_waitcnt lgkmcnt(2)
	v_mfma_scale_f32_16x16x128_f8f6f4 v[102:105], v[2:9], v[34:41], v[102:105], v138, v138 op_sel:[0,1,0] op_sel_hi:[0,0,0]
	v_mfma_scale_f32_16x16x128_f8f6f4 v[98:101], v[10:17], v[34:41], v[98:101], v138, v138 op_sel:[0,1,0] op_sel_hi:[0,0,0]
	s_waitcnt lgkmcnt(0)
	v_mfma_scale_f32_16x16x128_f8f6f4 v[86:89], v[2:9], v[42:49], v[206:209], v138, v138 op_sel:[0,1,0] op_sel_hi:[0,0,0]
	v_mfma_scale_f32_16x16x128_f8f6f4 v[82:85], v[10:17], v[42:49], v[210:213], v138, v138 op_sel:[0,1,0] op_sel_hi:[0,0,0]
	v_mfma_scale_f32_16x16x128_f8f6f4 v[110:113], v[142:149], v[18:25], v[110:113], v138, v138 op_sel:[0,1,0] op_sel_hi:[0,0,0]
	v_mfma_scale_f32_16x16x128_f8f6f4 v[106:109], v[150:157], v[18:25], v[106:109], v138, v138 op_sel:[0,1,0] op_sel_hi:[0,0,0]
	v_mfma_scale_f32_16x16x128_f8f6f4 v[94:97], v[142:149], v[26:33], v[174:177], v138, v138 op_sel:[0,1,0] op_sel_hi:[0,0,0]
	v_mfma_scale_f32_16x16x128_f8f6f4 v[90:93], v[150:157], v[26:33], v[178:181], v138, v138 op_sel:[0,1,0] op_sel_hi:[0,0,0]
	v_mfma_scale_f32_16x16x128_f8f6f4 v[78:81], v[142:149], v[34:41], v[182:185], v138, v138 op_sel:[0,1,0] op_sel_hi:[0,0,0]
	v_mfma_scale_f32_16x16x128_f8f6f4 v[74:77], v[150:157], v[34:41], v[186:189], v138, v138 op_sel:[0,1,0] op_sel_hi:[0,0,0]
	v_mfma_scale_f32_16x16x128_f8f6f4 v[70:73], v[142:149], v[42:49], v[190:193], v138, v138 op_sel:[0,1,0] op_sel_hi:[0,0,0]
	v_mfma_scale_f32_16x16x128_f8f6f4 v[66:69], v[150:157], v[42:49], v[194:197], v138, v138 op_sel:[0,1,0] op_sel_hi:[0,0,0]
	s_barrier
	s_mov_b32 m0, s25
	s_add_i32 s45, s44, 0x80
	ds_read_b128 v[26:29], v137 offset:49152
	ds_read_b128 v[30:33], v137 offset:50176
	ds_read_b128 v[158:161], v137 offset:51200
	ds_read_b128 v[162:165], v137 offset:52224
	ds_read_b128 v[166:169], v137 offset:53248
	ds_read_b128 v[170:173], v137 offset:54272
	ds_read_b128 v[174:177], v137 offset:55296
	ds_read_b128 v[178:181], v137 offset:56320
	buffer_load_dwordx4 v134, s[80:83], s45 offen lds
	s_add_i32 s45, s44, 0x20080
	s_mov_b32 m0, s26
	s_add_i32 s42, s42, 0x20080
	buffer_load_dwordx4 v134, s[80:83], s45 offen lds
	s_add_i32 s45, s44, 0x40080
	s_mov_b32 m0, s29
	s_add_i32 s44, s44, 0x60080
	buffer_load_dwordx4 v134, s[80:83], s45 offen lds
	s_mov_b32 m0, s30
	s_nop 0
	buffer_load_dwordx4 v134, s[80:83], s44 offen lds
	s_mov_b32 m0, s27
	s_nop 0
	buffer_load_dwordx4 v1, s[80:83], s43 offen lds
	s_mov_b32 m0, s28
	s_nop 0
	buffer_load_dwordx4 v1, s[80:83], s42 offen lds
	s_waitcnt vmcnt(8)
	s_waitcnt lgkmcnt(0)
	s_barrier
	s_waitcnt lgkmcnt(6)
	v_mfma_scale_f32_16x16x128_f8f6f4 v[62:65], v[2:9], v[26:33], v[62:65], v138, v138 op_sel:[0,1,0] op_sel_hi:[0,0,0]
	v_mfma_scale_f32_16x16x128_f8f6f4 v[58:61], v[10:17], v[26:33], v[58:61], v138, v138 op_sel:[0,1,0] op_sel_hi:[0,0,0]
	s_waitcnt lgkmcnt(4)
	v_mfma_scale_f32_16x16x128_f8f6f4 v[54:57], v[2:9], v[158:165], v[54:57], v138, v138 op_sel:[0,1,0] op_sel_hi:[0,0,0]
	v_mfma_scale_f32_16x16x128_f8f6f4 v[50:53], v[10:17], v[158:165], v[50:53], v138, v138 op_sel:[0,1,0] op_sel_hi:[0,0,0]
	s_waitcnt lgkmcnt(2)
	v_mfma_scale_f32_16x16x128_f8f6f4 v[38:41], v[2:9], v[166:173], v[198:201], v138, v138 op_sel:[0,1,0] op_sel_hi:[0,0,0]
	v_mfma_scale_f32_16x16x128_f8f6f4 v[34:37], v[10:17], v[166:173], v[202:205], v138, v138 op_sel:[0,1,0] op_sel_hi:[0,0,0]
	s_waitcnt lgkmcnt(0)
	v_mfma_scale_f32_16x16x128_f8f6f4 v[22:25], v[2:9], v[174:181], v[214:217], v138, v138 op_sel:[0,1,0] op_sel_hi:[0,0,0]
	v_mfma_scale_f32_16x16x128_f8f6f4 v[18:21], v[10:17], v[174:181], v[218:221], v138, v138 op_sel:[0,1,0] op_sel_hi:[0,0,0]
	v_mfma_scale_f32_16x16x128_f8f6f4 v[46:49], v[142:149], v[26:33], v[222:225], v138, v138 op_sel:[0,1,0] op_sel_hi:[0,0,0]
	v_mfma_scale_f32_16x16x128_f8f6f4 v[42:45], v[150:157], v[26:33], v[226:229], v138, v138 op_sel:[0,1,0] op_sel_hi:[0,0,0]
	v_mfma_scale_f32_16x16x128_f8f6f4 v[30:33], v[142:149], v[158:165], v[230:233], v138, v138 op_sel:[0,1,0] op_sel_hi:[0,0,0]
	v_mfma_scale_f32_16x16x128_f8f6f4 v[26:29], v[150:157], v[158:165], v[234:237], v138, v138 op_sel:[0,1,0] op_sel_hi:[0,0,0]
	v_mfma_scale_f32_16x16x128_f8f6f4 v[14:17], v[142:149], v[166:173], v[238:241], v138, v138 op_sel:[0,1,0] op_sel_hi:[0,0,0]
	v_mfma_scale_f32_16x16x128_f8f6f4 v[10:13], v[150:157], v[166:173], v[242:245], v138, v138 op_sel:[0,1,0] op_sel_hi:[0,0,0]
	v_mfma_scale_f32_16x16x128_f8f6f4 v[6:9], v[142:149], v[174:181], v[246:249], v138, v138 op_sel:[0,1,0] op_sel_hi:[0,0,0]
	v_mfma_scale_f32_16x16x128_f8f6f4 v[2:5], v[150:157], v[174:181], v[250:253], v138, v138 op_sel:[0,1,0] op_sel_hi:[0,0,0]
	s_barrier
	s_add_i32 s41, s41, 2
	s_addk_i32 s39, 0x100
	s_addk_i32 s40, 0x100
	s_cmp_gt_u32 s41, 13
	s_cbranch_scc0 .LBB0_791
	s_and_b64 vcc, exec, s[10:11]
	s_cbranch_vccz .LBB0_794
	s_barrier

;     __device__ __forceinline__ bool next(int i, Unit& u) const { u.aux = 0; return t.map(i, u.pm, u.pn); }
;     __device__ __forceinline__ bool next(int i, Unit& u) const { u.aux = i & 1; return t.map(i >> 1, u.pm, u.pn); }
; #define PG8_STAGE(bufoff, goff, voff) do { _Pragma("unroll") for (int _i = 0; _i < 2; ++_i) \
;         __builtin_amdgcn_raw_ptr_buffer_load_lds(rsrc, (PG8_LAS void*)(lds + (bufoff) + ldsw + _i * 8192), 16, (int)(voff), (int)((goff) + _i * p1##voff), 0, 0); } while (0)
; #define PG8_LDA(dst, b, h) do { _Pragma("unroll") for (int m = 0; m < 4; ++m) dst[m] = PG8_LD8(lds + PG8_SA(b, h) + aoff + m * 2048); } while (0)
; #define PG8_LDB(dst, b, h) do { _Pragma("unroll") for (int n = 0; n < 2; ++n) dst[n] = PG8_LD8(lds + PG8_SB(b, h) + boff + n * 2048); } while (0)
; #define PG8_WAIT_V(n) asm volatile("s_waitcnt vmcnt(" #n ")" ::: "memory")
; #define PG8_WAIT_L(n) asm volatile("s_waitcnt lgkmcnt(" #n ")" ::: "memory")
; #define PG8_BAR __builtin_amdgcn_s_barrier()
; #define PG8_SCHED __builtin_amdgcn_sched_barrier(0)
; template <class Epi, class Sched, bool ALIGN_EPI, bool F8 = false, int F8SC = F8_SCALES>
; __device__ __forceinline__ void gemm_phase(PG8_LAS unsigned char* lds, const __amdgpu_buffer_rsrc_t rsrc, const int lda, const int ldb, const int K, const Sched& S, const Epi& E) {
;     ...
;     for (;;) {
;         const bool has_next = S.next(ui + 1, nxt);
;         unsigned nA = cA, nB = cB; if (has_next) { S.bases(nxt, nA, nB); nA = __builtin_amdgcn_readfirstlane(nA); nB = __builtin_amdgcn_readfirstlane(nB); }
; #pragma unroll 1
;         for (int t = 0; t < nt; t += 2) {
;             const bool last = (t == nt - 2);
;             const unsigned a1 = cA + (unsigned)(t + 1) * kstep;
;             const unsigned a2 = last ? nA : cA + (unsigned)(t + 2) * kstep, b2 = last ? nB : cB + (unsigned)(t + 2) * kstep;
;             const unsigned a3 = a2 + kstep, b3 = b2 + kstep;
;             PG8_LDB(B0, 0, 0); PG8_LDB(B1, 0, 1); PG8_SCHED; PG8_LDA(At, 0, 0); PG8_STAGE(PG8_SA(1, 1), a1 + hsA, voffA);
;             PG8_WAIT_V(8); PG8_WAIT_L(0); PG8_BAR; PG8_MMA(0, 0, At, B0); PG8_MMA(0, 1, At, B1); PG8_BAR; PG8_SCHED;
;             PG8_LDA(At, 0, 1); PG8_STAGE(PG8_SB(0, 0), b2, voffB); PG8_STAGE(PG8_SB(0, 1), b2 + hsB, voffB); PG8_STAGE(PG8_SA(0, 0), a2, voffA);
.LBB0_969:
	ds_read_b128 v[82:85], v157
	ds_read_b128 v[90:93], v157 offset:1024
	ds_read_b128 v[98:101], v157 offset:2048
	ds_read_b128 v[106:109], v157 offset:3072
	ds_read_b128 v[150:153], v158
	ds_read_b128 v[162:165], v158 offset:1024
	ds_read_b128 v[166:169], v158 offset:2048
	ds_read_b128 v[170:173], v158 offset:3072
	s_add_i32 s45, s44, 0x100
	s_add_i32 s48, s45, s42
	s_and_b64 s[46:47], s[14:15], exec
	s_cselect_b32 s50, s37, s48
	s_add_i32 s46, s45, s41
	s_add_i32 s45, s50, 0x80
	s_and_b64 s[14:15], s[14:15], exec
	s_cselect_b32 s53, s38, s46
	s_add_i32 s56, s43, s44
	s_add_i32 s44, s53, 0x10080
	s_add_i32 s15, s53, 0x18080
	s_add_i32 s14, s50, 0x10080
	s_add_i32 s57, s56, 0x10000
	s_add_i32 s55, s53, 0x8000
	s_add_i32 s54, s53, 0x10000
	s_add_i32 s52, s53, 0x18000
	s_add_i32 s51, s50, 0x10000
	s_add_i32 s49, s50, 0x20000
	s_add_i32 s48, s50, 0x30000
	s_add_i32 s47, s53, 0x80
	s_add_i32 s46, s53, 0x8080
	s_mov_b32 s80, s96
	s_mov_b32 m0, s31
	ds_read_b128 v[174:177], v159
	ds_read_b128 v[178:181], v159 offset:1024
	ds_read_b128 v[182:185], v159 offset:2048
	ds_read_b128 v[186:189], v159 offset:3072
	ds_read_b128 v[190:193], v159 offset:4096
	ds_read_b128 v[194:197], v159 offset:5120
	ds_read_b128 v[198:201], v159 offset:6144
	ds_read_b128 v[202:205], v159 offset:7168
	buffer_load_dwordx4 v1, s[80:83], s56 offen lds
	s_mov_b32 m0, s33
	s_nop 0
	buffer_load_dwordx4 v1, s[80:83], s57 offen lds
	s_waitcnt vmcnt(8)
	s_waitcnt lgkmcnt(0)
	s_barrier
	s_waitcnt lgkmcnt(7)
	v_mfma_f32_16x16x32_bf16 v[142:145], v[82:85], v[174:177], v[142:145]
	v_mfma_f32_16x16x32_bf16 v[138:141], v[98:101], v[174:177], v[138:141]
	s_waitcnt lgkmcnt(5)
	v_mfma_f32_16x16x32_bf16 v[126:129], v[82:85], v[182:185], v[126:129]
	v_mfma_f32_16x16x32_bf16 v[122:125], v[98:101], v[182:185], v[122:125]
	s_waitcnt lgkmcnt(3)
	v_mfma_f32_16x16x32_bf16 v[110:113], v[82:85], v[190:193], v[110:113]
	v_mfma_f32_16x16x32_bf16 v[102:105], v[98:101], v[190:193], v[102:105]
	s_waitcnt lgkmcnt(1)
	v_mfma_f32_16x16x32_bf16 v[78:81], v[82:85], v[198:201], v[78:81]
	v_mfma_f32_16x16x32_bf16 v[74:77], v[98:101], v[198:201], v[74:77]
	v_mfma_f32_16x16x32_bf16 v[142:145], v[90:93], v[178:181], v[142:145]
	v_mfma_f32_16x16x32_bf16 v[138:141], v[106:109], v[178:181], v[138:141]
	v_mfma_f32_16x16x32_bf16 v[126:129], v[90:93], v[186:189], v[126:129]
	v_mfma_f32_16x16x32_bf16 v[122:125], v[106:109], v[186:189], v[122:125]
	v_mfma_f32_16x16x32_bf16 v[110:113], v[90:93], v[194:197], v[110:113]
	v_mfma_f32_16x16x32_bf16 v[102:105], v[106:109], v[194:197], v[102:105]
	s_waitcnt lgkmcnt(0)
	v_mfma_f32_16x16x32_bf16 v[78:81], v[90:93], v[202:205], v[78:81]
	v_mfma_f32_16x16x32_bf16 v[74:77], v[106:109], v[202:205], v[74:77]
	v_mfma_f32_16x16x32_bf16 v[134:137], v[150:153], v[174:177], v[134:137]
	v_mfma_f32_16x16x32_bf16 v[130:133], v[166:169], v[174:177], v[130:133]
	v_mfma_f32_16x16x32_bf16 v[118:121], v[150:153], v[182:185], v[118:121]
	v_mfma_f32_16x16x32_bf16 v[114:117], v[166:169], v[182:185], v[114:117]
	v_mfma_f32_16x16x32_bf16 v[94:97], v[150:153], v[190:193], v[94:97]
	v_mfma_f32_16x16x32_bf16 v[86:89], v[166:169], v[190:193], v[86:89]
	v_mfma_f32_16x16x32_bf16 v[70:73], v[150:153], v[198:201], v[70:73]
	v_mfma_f32_16x16x32_bf16 v[66:69], v[166:169], v[198:201], v[66:69]
	v_mfma_f32_16x16x32_bf16 v[134:137], v[162:165], v[178:181], v[134:137]
	v_mfma_f32_16x16x32_bf16 v[130:133], v[170:173], v[178:181], v[130:133]
	v_mfma_f32_16x16x32_bf16 v[118:121], v[162:165], v[186:189], v[118:121]
	v_mfma_f32_16x16x32_bf16 v[114:117], v[170:173], v[186:189], v[114:117]
	v_mfma_f32_16x16x32_bf16 v[94:97], v[162:165], v[194:197], v[94:97]
	v_mfma_f32_16x16x32_bf16 v[86:89], v[170:173], v[194:197], v[86:89]
	v_mfma_f32_16x16x32_bf16 v[70:73], v[162:165], v[202:205], v[70:73]
	v_mfma_f32_16x16x32_bf16 v[66:69], v[170:173], v[202:205], v[66:69]
	s_barrier
	s_mov_b32 m0, s17
	ds_read_b128 v[174:177], v159 offset:16384
	ds_read_b128 v[178:181], v159 offset:17408
	ds_read_b128 v[182:185], v159 offset:18432
	ds_read_b128 v[186:189], v159 offset:19456
	ds_read_b128 v[190:193], v159 offset:20480
	ds_read_b128 v[194:197], v159 offset:21504
	ds_read_b128 v[198:201], v159 offset:22528
	ds_read_b128 v[202:205], v159 offset:23552
	buffer_load_dwordx4 v156, s[80:83], s53 offen lds
	s_mov_b32 m0, s18
	s_nop 0
	buffer_load_dwordx4 v156, s[80:83], s55 offen lds
	s_mov_b32 m0, s19
	s_nop 0
	buffer_load_dwordx4 v156, s[80:83], s54 offen lds
	s_mov_b32 m0, s20
	s_nop 0
	buffer_load_dwordx4 v156, s[80:83], s52 offen lds
	s_mov_b32 m0, s16
	s_nop 0
	buffer_load_dwordx4 v1, s[80:83], s50 offen lds
	s_mov_b32 m0, s21
	s_nop 0
	buffer_load_dwordx4 v1, s[80:83], s51 offen lds
	s_waitcnt vmcnt(8)
	s_waitcnt lgkmcnt(0)
	s_barrier
; #define PG8_STAGE(bufoff, goff, voff) do { _Pragma("unroll") for (int _i = 0; _i < 2; ++_i) \
;         __builtin_amdgcn_raw_ptr_buffer_load_lds(rsrc, (PG8_LAS void*)(lds + (bufoff) + ldsw + _i * 8192), 16, (int)(voff), (int)((goff) + _i * p1##voff), 0, 0); } while (0)
; #define PG8_LDA(dst, b, h) do { _Pragma("unroll") for (int m = 0; m < 4; ++m) dst[m] = PG8_LD8(lds + PG8_SA(b, h) + aoff + m * 2048); } while (0)
; #define PG8_LDB(dst, b, h) do { _Pragma("unroll") for (int n = 0; n < 2; ++n) dst[n] = PG8_LD8(lds + PG8_SB(b, h) + boff + n * 2048); } while (0)
; #define PG8_WAIT_V(n) asm volatile("s_waitcnt vmcnt(" #n ")" ::: "memory")
; #define PG8_WAIT_L(n) asm volatile("s_waitcnt lgkmcnt(" #n ")" ::: "memory")
; #define PG8_BAR __builtin_amdgcn_s_barrier()
; #define PG8_SCHED __builtin_amdgcn_sched_barrier(0)
; template <class Epi, class Sched, bool ALIGN_EPI, bool F8 = false, int F8SC = F8_SCALES>
; __device__ __forceinline__ void gemm_phase(PG8_LAS unsigned char* lds, const __amdgpu_buffer_rsrc_t rsrc, const int lda, const int ldb, const int K, const Sched& S, const Epi& E) {
;     ...
;             PG8_WAIT_V(8); PG8_WAIT_L(0); PG8_BAR; PG8_MMA(1, 0, At, B0); PG8_MMA(1, 1, At, B1); PG8_BAR; PG8_SCHED;
;             PG8_LDB(B0, 1, 0); PG8_LDB(B1, 1, 1); PG8_SCHED; PG8_LDA(At, 1, 0); PG8_STAGE(PG8_SA(0, 1), a2 + hsA, voffA);
;             PG8_WAIT_V(8); PG8_WAIT_L(0); PG8_BAR; PG8_MMA(0, 0, At, B0); PG8_MMA(0, 1, At, B1); PG8_BAR; PG8_SCHED;
	s_waitcnt lgkmcnt(7)
	v_mfma_f32_16x16x32_bf16 v[62:65], v[82:85], v[174:177], v[62:65]
	v_mfma_f32_16x16x32_bf16 v[58:61], v[98:101], v[174:177], v[58:61]
	s_waitcnt lgkmcnt(5)
	v_mfma_f32_16x16x32_bf16 v[46:49], v[82:85], v[182:185], v[46:49]
	v_mfma_f32_16x16x32_bf16 v[42:45], v[98:101], v[182:185], v[42:45]
	s_waitcnt lgkmcnt(3)
	v_mfma_f32_16x16x32_bf16 v[30:33], v[82:85], v[190:193], v[30:33]
	v_mfma_f32_16x16x32_bf16 v[26:29], v[98:101], v[190:193], v[26:29]
	s_waitcnt lgkmcnt(1)
	v_mfma_f32_16x16x32_bf16 v[14:17], v[82:85], v[198:201], v[14:17]
	v_mfma_f32_16x16x32_bf16 v[10:13], v[98:101], v[198:201], v[10:13]
	v_mfma_f32_16x16x32_bf16 v[62:65], v[90:93], v[178:181], v[62:65]
	v_mfma_f32_16x16x32_bf16 v[58:61], v[106:109], v[178:181], v[58:61]
	v_mfma_f32_16x16x32_bf16 v[46:49], v[90:93], v[186:189], v[46:49]
	v_mfma_f32_16x16x32_bf16 v[42:45], v[106:109], v[186:189], v[42:45]
	v_mfma_f32_16x16x32_bf16 v[30:33], v[90:93], v[194:197], v[30:33]
	v_mfma_f32_16x16x32_bf16 v[26:29], v[106:109], v[194:197], v[26:29]
	s_waitcnt lgkmcnt(0)
	v_mfma_f32_16x16x32_bf16 v[14:17], v[90:93], v[202:205], v[14:17]
	v_mfma_f32_16x16x32_bf16 v[10:13], v[106:109], v[202:205], v[10:13]
	v_mfma_f32_16x16x32_bf16 v[54:57], v[150:153], v[174:177], v[54:57]
	v_mfma_f32_16x16x32_bf16 v[50:53], v[166:169], v[174:177], v[50:53]
	v_mfma_f32_16x16x32_bf16 v[38:41], v[150:153], v[182:185], v[38:41]
	v_mfma_f32_16x16x32_bf16 v[34:37], v[166:169], v[182:185], v[34:37]
	v_mfma_f32_16x16x32_bf16 v[22:25], v[150:153], v[190:193], v[22:25]
	v_mfma_f32_16x16x32_bf16 v[18:21], v[166:169], v[190:193], v[18:21]
	v_mfma_f32_16x16x32_bf16 v[6:9], v[150:153], v[198:201], v[6:9]
	v_mfma_f32_16x16x32_bf16 v[2:5], v[166:169], v[198:201], v[2:5]
	v_mfma_f32_16x16x32_bf16 v[54:57], v[162:165], v[178:181], v[54:57]
	v_mfma_f32_16x16x32_bf16 v[50:53], v[170:173], v[178:181], v[50:53]
	v_mfma_f32_16x16x32_bf16 v[38:41], v[162:165], v[186:189], v[38:41]
	v_mfma_f32_16x16x32_bf16 v[34:37], v[170:173], v[186:189], v[34:37]
	v_mfma_f32_16x16x32_bf16 v[22:25], v[162:165], v[194:197], v[22:25]
	v_mfma_f32_16x16x32_bf16 v[18:21], v[170:173], v[194:197], v[18:21]
	v_mfma_f32_16x16x32_bf16 v[6:9], v[162:165], v[202:205], v[6:9]
	v_mfma_f32_16x16x32_bf16 v[2:5], v[170:173], v[202:205], v[2:5]
	s_barrier
	ds_read_b128 v[82:85], v160
	ds_read_b128 v[90:93], v160 offset:1024
	ds_read_b128 v[98:101], v160 offset:2048
	ds_read_b128 v[106:109], v160 offset:3072
	ds_read_b128 v[150:153], v161
	ds_read_b128 v[162:165], v161 offset:1024
	ds_read_b128 v[166:169], v161 offset:2048
	ds_read_b128 v[170:173], v161 offset:3072
	s_mov_b32 m0, s22
	ds_read_b128 v[174:177], v159 offset:32768
	ds_read_b128 v[178:181], v159 offset:33792
	ds_read_b128 v[182:185], v159 offset:34816
	ds_read_b128 v[186:189], v159 offset:35840
	ds_read_b128 v[190:193], v159 offset:36864
	ds_read_b128 v[194:197], v159 offset:37888
	ds_read_b128 v[198:201], v159 offset:38912
	ds_read_b128 v[202:205], v159 offset:39936
	buffer_load_dwordx4 v1, s[80:83], s49 offen lds
	s_mov_b32 m0, s23
	s_nop 0
	buffer_load_dwordx4 v1, s[80:83], s48 offen lds
	s_waitcnt vmcnt(8)
	s_waitcnt lgkmcnt(0)
	s_barrier
	s_waitcnt lgkmcnt(7)
	v_mfma_f32_16x16x32_bf16 v[142:145], v[82:85], v[174:177], v[142:145]
	v_mfma_f32_16x16x32_bf16 v[138:141], v[98:101], v[174:177], v[138:141]
	s_waitcnt lgkmcnt(5)
	v_mfma_f32_16x16x32_bf16 v[126:129], v[82:85], v[182:185], v[126:129]
	v_mfma_f32_16x16x32_bf16 v[122:125], v[98:101], v[182:185], v[122:125]
	s_waitcnt lgkmcnt(3)
	v_mfma_f32_16x16x32_bf16 v[110:113], v[82:85], v[190:193], v[110:113]
	v_mfma_f32_16x16x32_bf16 v[102:105], v[98:101], v[190:193], v[102:105]
	s_waitcnt lgkmcnt(1)
	v_mfma_f32_16x16x32_bf16 v[78:81], v[82:85], v[198:201], v[78:81]
	v_mfma_f32_16x16x32_bf16 v[74:77], v[98:101], v[198:201], v[74:77]
	v_mfma_f32_16x16x32_bf16 v[142:145], v[90:93], v[178:181], v[142:145]
	v_mfma_f32_16x16x32_bf16 v[138:141], v[106:109], v[178:181], v[138:141]
	v_mfma_f32_16x16x32_bf16 v[126:129], v[90:93], v[186:189], v[126:129]
	v_mfma_f32_16x16x32_bf16 v[122:125], v[106:109], v[186:189], v[122:125]
	v_mfma_f32_16x16x32_bf16 v[110:113], v[90:93], v[194:197], v[110:113]
	v_mfma_f32_16x16x32_bf16 v[102:105], v[106:109], v[194:197], v[102:105]
	s_waitcnt lgkmcnt(0)
	v_mfma_f32_16x16x32_bf16 v[78:81], v[90:93], v[202:205], v[78:81]
	v_mfma_f32_16x16x32_bf16 v[74:77], v[106:109], v[202:205], v[74:77]
	v_mfma_f32_16x16x32_bf16 v[134:137], v[150:153], v[174:177], v[134:137]
	v_mfma_f32_16x16x32_bf16 v[130:133], v[166:169], v[174:177], v[130:133]
	v_mfma_f32_16x16x32_bf16 v[118:121], v[150:153], v[182:185], v[118:121]
	v_mfma_f32_16x16x32_bf16 v[114:117], v[166:169], v[182:185], v[114:117]
	v_mfma_f32_16x16x32_bf16 v[94:97], v[150:153], v[190:193], v[94:97]
	v_mfma_f32_16x16x32_bf16 v[86:89], v[166:169], v[190:193], v[86:89]
	v_mfma_f32_16x16x32_bf16 v[70:73], v[150:153], v[198:201], v[70:73]
	v_mfma_f32_16x16x32_bf16 v[66:69], v[166:169], v[198:201], v[66:69]
	v_mfma_f32_16x16x32_bf16 v[134:137], v[162:165], v[178:181], v[134:137]
	v_mfma_f32_16x16x32_bf16 v[130:133], v[170:173], v[178:181], v[130:133]
	v_mfma_f32_16x16x32_bf16 v[118:121], v[162:165], v[186:189], v[118:121]
	v_mfma_f32_16x16x32_bf16 v[114:117], v[170:173], v[186:189], v[114:117]
	v_mfma_f32_16x16x32_bf16 v[94:97], v[162:165], v[194:197], v[94:97]
	v_mfma_f32_16x16x32_bf16 v[86:89], v[170:173], v[194:197], v[86:89]
	v_mfma_f32_16x16x32_bf16 v[70:73], v[162:165], v[202:205], v[70:73]
	v_mfma_f32_16x16x32_bf16 v[66:69], v[170:173], v[202:205], v[66:69]
	s_barrier
; #define PG8_STAGE(bufoff, goff, voff) do { _Pragma("unroll") for (int _i = 0; _i < 2; ++_i) \
;         __builtin_amdgcn_raw_ptr_buffer_load_lds(rsrc, (PG8_LAS void*)(lds + (bufoff) + ldsw + _i * 8192), 16, (int)(voff), (int)((goff) + _i * p1##voff), 0, 0); } while (0)
; #define PG8_LDA(dst, b, h) do { _Pragma("unroll") for (int m = 0; m < 4; ++m) dst[m] = PG8_LD8(lds + PG8_SA(b, h) + aoff + m * 2048); } while (0)
; #define PG8_WAIT_V(n) asm volatile("s_waitcnt vmcnt(" #n ")" ::: "memory")
; #define PG8_WAIT_L(n) asm volatile("s_waitcnt lgkmcnt(" #n ")" ::: "memory")
; #define PG8_BAR __builtin_amdgcn_s_barrier()
; #define PG8_SCHED __builtin_amdgcn_sched_barrier(0)
; #define PG8_ZERO() do { _Pragma("unroll") for (int a = 0; a < 2; ++a) _Pragma("unroll") for (int b = 0; b < 2; ++b) _Pragma("unroll") for (int m = 0; m < 4; ++m) _Pragma("unroll") for (int n = 0; n < 2; ++n) acc[a][b][m][n] = (f32x4){0.f, 0.f, 0.f, 0.f}; } while (0)
; template <class Epi, class Sched, bool ALIGN_EPI, bool F8 = false, int F8SC = F8_SCALES>
; __device__ __forceinline__ void gemm_phase(PG8_LAS unsigned char* lds, const __amdgpu_buffer_rsrc_t rsrc, const int lda, const int ldb, const int K, const Sched& S, const Epi& E) {
;     ...
;             PG8_LDA(At, 1, 1); PG8_STAGE(PG8_SB(1, 0), b3, voffB); PG8_STAGE(PG8_SB(1, 1), b3 + hsB, voffB); PG8_STAGE(PG8_SA(1, 0), a3, voffA);
;             PG8_WAIT_V(8); PG8_WAIT_L(0); PG8_BAR; PG8_MMA(1, 0, At, B0); PG8_MMA(1, 1, At, B1); PG8_BAR; PG8_SCHED;
;         }
;         if constexpr (ALIGN_EPI) { if (wr == 0) PG8_BAR; }
;         bool keep; { int t2 = threadIdx.x; asm volatile("" : "+v"(t2)); const int w2 = __builtin_amdgcn_readfirstlane(t2 >> 6), l2 = t2 & 63; keep = E(acc, cur, w2 >> 2, w2 & 3, l2 & 15, l2 >> 4); }
;         if (!has_next) break;
;         if (!keep) PG8_ZERO();
	s_mov_b32 m0, s25
	ds_read_b128 v[174:177], v159 offset:49152
	ds_read_b128 v[178:181], v159 offset:50176
	ds_read_b128 v[182:185], v159 offset:51200
	ds_read_b128 v[186:189], v159 offset:52224
	ds_read_b128 v[190:193], v159 offset:53248
	ds_read_b128 v[194:197], v159 offset:54272
	ds_read_b128 v[198:201], v159 offset:55296
	ds_read_b128 v[202:205], v159 offset:56320
	buffer_load_dwordx4 v156, s[80:83], s47 offen lds
	s_mov_b32 m0, s26
	s_nop 0
	buffer_load_dwordx4 v156, s[80:83], s46 offen lds
	s_mov_b32 m0, s29
	s_nop 0
	buffer_load_dwordx4 v156, s[80:83], s44 offen lds
	s_mov_b32 m0, s30
	s_nop 0
	buffer_load_dwordx4 v156, s[80:83], s15 offen lds
	s_mov_b32 m0, s27
	s_nop 0
	buffer_load_dwordx4 v1, s[80:83], s45 offen lds
	s_mov_b32 m0, s28
	s_nop 0
	buffer_load_dwordx4 v1, s[80:83], s14 offen lds
	s_waitcnt vmcnt(8)
	s_waitcnt lgkmcnt(0)
	s_barrier
	s_waitcnt lgkmcnt(7)
	v_mfma_f32_16x16x32_bf16 v[62:65], v[82:85], v[174:177], v[62:65]
	v_mfma_f32_16x16x32_bf16 v[58:61], v[98:101], v[174:177], v[58:61]
	s_waitcnt lgkmcnt(5)
	v_mfma_f32_16x16x32_bf16 v[46:49], v[82:85], v[182:185], v[46:49]
	v_mfma_f32_16x16x32_bf16 v[42:45], v[98:101], v[182:185], v[42:45]
	s_waitcnt lgkmcnt(3)
	v_mfma_f32_16x16x32_bf16 v[30:33], v[82:85], v[190:193], v[30:33]
	v_mfma_f32_16x16x32_bf16 v[26:29], v[98:101], v[190:193], v[26:29]
	s_waitcnt lgkmcnt(1)
	v_mfma_f32_16x16x32_bf16 v[14:17], v[82:85], v[198:201], v[14:17]
	v_mfma_f32_16x16x32_bf16 v[10:13], v[98:101], v[198:201], v[10:13]
	v_mfma_f32_16x16x32_bf16 v[62:65], v[90:93], v[178:181], v[62:65]
	v_mfma_f32_16x16x32_bf16 v[58:61], v[106:109], v[178:181], v[58:61]
	v_mfma_f32_16x16x32_bf16 v[46:49], v[90:93], v[186:189], v[46:49]
	v_mfma_f32_16x16x32_bf16 v[42:45], v[106:109], v[186:189], v[42:45]
	v_mfma_f32_16x16x32_bf16 v[30:33], v[90:93], v[194:197], v[30:33]
	v_mfma_f32_16x16x32_bf16 v[26:29], v[106:109], v[194:197], v[26:29]
	s_waitcnt lgkmcnt(0)
	v_mfma_f32_16x16x32_bf16 v[14:17], v[90:93], v[202:205], v[14:17]
	v_mfma_f32_16x16x32_bf16 v[10:13], v[106:109], v[202:205], v[10:13]
	v_mfma_f32_16x16x32_bf16 v[54:57], v[150:153], v[174:177], v[54:57]
	v_mfma_f32_16x16x32_bf16 v[50:53], v[166:169], v[174:177], v[50:53]
	v_mfma_f32_16x16x32_bf16 v[38:41], v[150:153], v[182:185], v[38:41]
	v_mfma_f32_16x16x32_bf16 v[34:37], v[166:169], v[182:185], v[34:37]
	v_mfma_f32_16x16x32_bf16 v[22:25], v[150:153], v[190:193], v[22:25]
	v_mfma_f32_16x16x32_bf16 v[18:21], v[166:169], v[190:193], v[18:21]
	v_mfma_f32_16x16x32_bf16 v[6:9], v[150:153], v[198:201], v[6:9]
	v_mfma_f32_16x16x32_bf16 v[2:5], v[166:169], v[198:201], v[2:5]
	v_mfma_f32_16x16x32_bf16 v[54:57], v[162:165], v[178:181], v[54:57]
	v_mfma_f32_16x16x32_bf16 v[50:53], v[170:173], v[178:181], v[50:53]
	v_mfma_f32_16x16x32_bf16 v[38:41], v[162:165], v[186:189], v[38:41]
	v_mfma_f32_16x16x32_bf16 v[34:37], v[170:173], v[186:189], v[34:37]
	v_mfma_f32_16x16x32_bf16 v[22:25], v[162:165], v[194:197], v[22:25]
	v_mfma_f32_16x16x32_bf16 v[18:21], v[170:173], v[194:197], v[18:21]
	v_mfma_f32_16x16x32_bf16 v[6:9], v[162:165], v[202:205], v[6:9]
	v_mfma_f32_16x16x32_bf16 v[2:5], v[170:173], v[202:205], v[2:5]
	s_barrier
	s_andn2_b64 vcc, exec, s[6:7]
	s_mov_b64 s[14:15], -1
	s_mov_b64 s[6:7], 0
	s_movk_i32 s44, 0x100
	s_cbranch_vccz .LBB0_969
	s_and_b64 vcc, exec, s[10:11]
	s_cbranch_vccz .LBB0_972
	s_barrier

;     __device__ __forceinline__ bool next(int i, Unit& u) const { u.aux = 0; return t.map(i, u.pm, u.pn); }
;     __device__ __forceinline__ bool next(int i, Unit& u) const { u.aux = i & 1; return t.map(i >> 1, u.pm, u.pn); }
; #define PG8_STAGE(bufoff, goff, voff) do { _Pragma("unroll") for (int _i = 0; _i < 2; ++_i) \
;         __builtin_amdgcn_raw_ptr_buffer_load_lds(rsrc, (PG8_LAS void*)(lds + (bufoff) + ldsw + _i * 8192), 16, (int)(voff), (int)((goff) + _i * p1##voff), 0, 0); } while (0)
; #define PG8_LDA(dst, b, h) do { _Pragma("unroll") for (int m = 0; m < 4; ++m) dst[m] = PG8_LD8(lds + PG8_SA(b, h) + aoff + m * 2048); } while (0)
; #define PG8_LDB(dst, b, h) do { _Pragma("unroll") for (int n = 0; n < 2; ++n) dst[n] = PG8_LD8(lds + PG8_SB(b, h) + boff + n * 2048); } while (0)
; #define PG8_WAIT_V(n) asm volatile("s_waitcnt vmcnt(" #n ")" ::: "memory")
; #define PG8_WAIT_L(n) asm volatile("s_waitcnt lgkmcnt(" #n ")" ::: "memory")
; #define PG8_BAR __builtin_amdgcn_s_barrier()
; #define PG8_SCHED __builtin_amdgcn_sched_barrier(0)
; template <class Epi, class Sched, bool ALIGN_EPI, bool F8 = false, int F8SC = F8_SCALES>
; __device__ __forceinline__ void gemm_phase(PG8_LAS unsigned char* lds, const __amdgpu_buffer_rsrc_t rsrc, const int lda, const int ldb, const int K, const Sched& S, const Epi& E) {
;     ...
;     for (;;) {
;         const bool has_next = S.next(ui + 1, nxt);
;         unsigned nA = cA, nB = cB; if (has_next) { S.bases(nxt, nA, nB); nA = __builtin_amdgcn_readfirstlane(nA); nB = __builtin_amdgcn_readfirstlane(nB); }
; #pragma unroll 1
;         for (int t = 0; t < nt; t += 2) {
;             const bool last = (t == nt - 2);
;             const unsigned a1 = cA + (unsigned)(t + 1) * kstep;
;             const unsigned a2 = last ? nA : cA + (unsigned)(t + 2) * kstep, b2 = last ? nB : cB + (unsigned)(t + 2) * kstep;
;             const unsigned a3 = a2 + kstep, b3 = b2 + kstep;
;             PG8_LDB(B0, 0, 0); PG8_LDB(B1, 0, 1); PG8_SCHED; PG8_LDA(At, 0, 0); PG8_STAGE(PG8_SA(1, 1), a1 + hsA, voffA);
;             PG8_WAIT_V(8); PG8_WAIT_L(0); PG8_BAR; PG8_MMA(0, 0, At, B0); PG8_MMA(0, 1, At, B1); PG8_BAR; PG8_SCHED;
;             PG8_LDA(At, 0, 1); PG8_STAGE(PG8_SB(0, 0), b2, voffB); PG8_STAGE(PG8_SB(0, 1), b2 + hsB, voffB); PG8_STAGE(PG8_SA(0, 0), a2, voffA);
.LBB0_995:
	ds_read_b128 v[106:109], v157
	ds_read_b128 v[110:113], v157 offset:1024
	ds_read_b128 v[114:117], v157 offset:2048
	ds_read_b128 v[122:125], v157 offset:3072
	ds_read_b128 v[150:153], v158
	ds_read_b128 v[162:165], v158 offset:1024
	ds_read_b128 v[166:169], v158 offset:2048
	ds_read_b128 v[170:173], v158 offset:3072
	s_add_i32 s46, s43, 0x100
	s_add_i32 s47, s46, s41
	s_and_b64 s[44:45], s[12:13], exec
	s_cselect_b32 s49, s36, s47
	s_add_i32 s46, s46, s40
	s_add_i32 s44, s49, 0x80
	s_and_b64 s[12:13], s[12:13], exec
	s_cselect_b32 s52, s37, s46
	s_add_i32 s55, s42, s43
	s_add_i32 s43, s52, 0x10080
	s_add_i32 s13, s52, 0x18080
	s_add_i32 s12, s49, 0x10080
	s_add_i32 s56, s55, 0x10000
	s_add_i32 s54, s52, 0x8000
	s_add_i32 s53, s52, 0x10000
	s_add_i32 s51, s52, 0x18000
	s_add_i32 s50, s49, 0x10000
	s_add_i32 s48, s49, 0x20000
	s_add_i32 s47, s49, 0x30000
	s_add_i32 s46, s52, 0x80
	s_add_i32 s45, s52, 0x8080
	s_mov_b32 s80, s96
	s_mov_b32 m0, s30
	ds_read_b128 v[174:177], v159
	ds_read_b128 v[178:181], v159 offset:1024
	ds_read_b128 v[182:185], v159 offset:2048
	ds_read_b128 v[186:189], v159 offset:3072
	ds_read_b128 v[190:193], v159 offset:4096
	ds_read_b128 v[194:197], v159 offset:5120
	ds_read_b128 v[198:201], v159 offset:6144
	ds_read_b128 v[202:205], v159 offset:7168
	buffer_load_dwordx4 v1, s[80:83], s55 offen lds
	s_mov_b32 m0, s31
	s_nop 0
	buffer_load_dwordx4 v1, s[80:83], s56 offen lds
	s_waitcnt vmcnt(8)
	s_waitcnt lgkmcnt(0)
	s_barrier
	s_waitcnt lgkmcnt(7)
	v_mfma_f32_16x16x32_bf16 v[142:145], v[106:109], v[174:177], v[142:145]
	v_mfma_f32_16x16x32_bf16 v[138:141], v[114:117], v[174:177], v[138:141]
	s_waitcnt lgkmcnt(5)
	v_mfma_f32_16x16x32_bf16 v[126:129], v[106:109], v[182:185], v[126:129]
	v_mfma_f32_16x16x32_bf16 v[118:121], v[114:117], v[182:185], v[118:121]
	s_waitcnt lgkmcnt(3)
	v_mfma_f32_16x16x32_bf16 v[94:97], v[106:109], v[190:193], v[94:97]
	v_mfma_f32_16x16x32_bf16 v[90:93], v[114:117], v[190:193], v[90:93]
	s_waitcnt lgkmcnt(1)
	v_mfma_f32_16x16x32_bf16 v[78:81], v[106:109], v[198:201], v[78:81]
	v_mfma_f32_16x16x32_bf16 v[74:77], v[114:117], v[198:201], v[74:77]
	v_mfma_f32_16x16x32_bf16 v[142:145], v[110:113], v[178:181], v[142:145]
	v_mfma_f32_16x16x32_bf16 v[138:141], v[122:125], v[178:181], v[138:141]
	v_mfma_f32_16x16x32_bf16 v[126:129], v[110:113], v[186:189], v[126:129]
	v_mfma_f32_16x16x32_bf16 v[118:121], v[122:125], v[186:189], v[118:121]
	v_mfma_f32_16x16x32_bf16 v[94:97], v[110:113], v[194:197], v[94:97]
	v_mfma_f32_16x16x32_bf16 v[90:93], v[122:125], v[194:197], v[90:93]
	s_waitcnt lgkmcnt(0)
	v_mfma_f32_16x16x32_bf16 v[78:81], v[110:113], v[202:205], v[78:81]
	v_mfma_f32_16x16x32_bf16 v[74:77], v[122:125], v[202:205], v[74:77]
	v_mfma_f32_16x16x32_bf16 v[134:137], v[150:153], v[174:177], v[134:137]
	v_mfma_f32_16x16x32_bf16 v[130:133], v[166:169], v[174:177], v[130:133]
	v_mfma_f32_16x16x32_bf16 v[102:105], v[150:153], v[182:185], v[102:105]
	v_mfma_f32_16x16x32_bf16 v[98:101], v[166:169], v[182:185], v[98:101]
	v_mfma_f32_16x16x32_bf16 v[86:89], v[150:153], v[190:193], v[86:89]
	v_mfma_f32_16x16x32_bf16 v[82:85], v[166:169], v[190:193], v[82:85]
	v_mfma_f32_16x16x32_bf16 v[70:73], v[150:153], v[198:201], v[70:73]
	v_mfma_f32_16x16x32_bf16 v[66:69], v[166:169], v[198:201], v[66:69]
	v_mfma_f32_16x16x32_bf16 v[134:137], v[162:165], v[178:181], v[134:137]
	v_mfma_f32_16x16x32_bf16 v[130:133], v[170:173], v[178:181], v[130:133]
	v_mfma_f32_16x16x32_bf16 v[102:105], v[162:165], v[186:189], v[102:105]
	v_mfma_f32_16x16x32_bf16 v[98:101], v[170:173], v[186:189], v[98:101]
	v_mfma_f32_16x16x32_bf16 v[86:89], v[162:165], v[194:197], v[86:89]
	v_mfma_f32_16x16x32_bf16 v[82:85], v[170:173], v[194:197], v[82:85]
	v_mfma_f32_16x16x32_bf16 v[70:73], v[162:165], v[202:205], v[70:73]
	v_mfma_f32_16x16x32_bf16 v[66:69], v[170:173], v[202:205], v[66:69]
	s_barrier
	s_mov_b32 m0, s16
	ds_read_b128 v[174:177], v159 offset:16384
	ds_read_b128 v[178:181], v159 offset:17408
	ds_read_b128 v[182:185], v159 offset:18432
	ds_read_b128 v[186:189], v159 offset:19456
	ds_read_b128 v[190:193], v159 offset:20480
	ds_read_b128 v[194:197], v159 offset:21504
	ds_read_b128 v[198:201], v159 offset:22528
	ds_read_b128 v[202:205], v159 offset:23552
	buffer_load_dwordx4 v156, s[80:83], s52 offen lds
	s_mov_b32 m0, s17
	s_nop 0
	buffer_load_dwordx4 v156, s[80:83], s54 offen lds
	s_mov_b32 m0, s18
	s_nop 0
	buffer_load_dwordx4 v156, s[80:83], s53 offen lds
	s_mov_b32 m0, s19
	s_nop 0
	buffer_load_dwordx4 v156, s[80:83], s51 offen lds
	s_mov_b32 m0, s15
	s_nop 0
	buffer_load_dwordx4 v1, s[80:83], s49 offen lds
	s_mov_b32 m0, s20
	s_nop 0
	buffer_load_dwordx4 v1, s[80:83], s50 offen lds
	s_waitcnt vmcnt(8)
	s_waitcnt lgkmcnt(0)
	s_barrier
; #define PG8_STAGE(bufoff, goff, voff) do { _Pragma("unroll") for (int _i = 0; _i < 2; ++_i) \
;         __builtin_amdgcn_raw_ptr_buffer_load_lds(rsrc, (PG8_LAS void*)(lds + (bufoff) + ldsw + _i * 8192), 16, (int)(voff), (int)((goff) + _i * p1##voff), 0, 0); } while (0)
; #define PG8_LDA(dst, b, h) do { _Pragma("unroll") for (int m = 0; m < 4; ++m) dst[m] = PG8_LD8(lds + PG8_SA(b, h) + aoff + m * 2048); } while (0)
; #define PG8_LDB(dst, b, h) do { _Pragma("unroll") for (int n = 0; n < 2; ++n) dst[n] = PG8_LD8(lds + PG8_SB(b, h) + boff + n * 2048); } while (0)
; #define PG8_WAIT_V(n) asm volatile("s_waitcnt vmcnt(" #n ")" ::: "memory")
; #define PG8_WAIT_L(n) asm volatile("s_waitcnt lgkmcnt(" #n ")" ::: "memory")
; #define PG8_BAR __builtin_amdgcn_s_barrier()
; #define PG8_SCHED __builtin_amdgcn_sched_barrier(0)
; template <class Epi, class Sched, bool ALIGN_EPI, bool F8 = false, int F8SC = F8_SCALES>
; __device__ __forceinline__ void gemm_phase(PG8_LAS unsigned char* lds, const __amdgpu_buffer_rsrc_t rsrc, const int lda, const int ldb, const int K, const Sched& S, const Epi& E) {
;     ...
;             PG8_WAIT_V(8); PG8_WAIT_L(0); PG8_BAR; PG8_MMA(1, 0, At, B0); PG8_MMA(1, 1, At, B1); PG8_BAR; PG8_SCHED;
;             PG8_LDB(B0, 1, 0); PG8_LDB(B1, 1, 1); PG8_SCHED; PG8_LDA(At, 1, 0); PG8_STAGE(PG8_SA(0, 1), a2 + hsA, voffA);
;             PG8_WAIT_V(8); PG8_WAIT_L(0); PG8_BAR; PG8_MMA(0, 0, At, B0); PG8_MMA(0, 1, At, B1); PG8_BAR; PG8_SCHED;
	s_waitcnt lgkmcnt(7)
	v_mfma_f32_16x16x32_bf16 v[62:65], v[106:109], v[174:177], v[62:65]
	v_mfma_f32_16x16x32_bf16 v[58:61], v[114:117], v[174:177], v[58:61]
	s_waitcnt lgkmcnt(5)
	v_mfma_f32_16x16x32_bf16 v[46:49], v[106:109], v[182:185], v[46:49]
	v_mfma_f32_16x16x32_bf16 v[42:45], v[114:117], v[182:185], v[42:45]
	s_waitcnt lgkmcnt(3)
	v_mfma_f32_16x16x32_bf16 v[30:33], v[106:109], v[190:193], v[30:33]
	v_mfma_f32_16x16x32_bf16 v[26:29], v[114:117], v[190:193], v[26:29]
	s_waitcnt lgkmcnt(1)
	v_mfma_f32_16x16x32_bf16 v[14:17], v[106:109], v[198:201], v[14:17]
	v_mfma_f32_16x16x32_bf16 v[10:13], v[114:117], v[198:201], v[10:13]
	v_mfma_f32_16x16x32_bf16 v[62:65], v[110:113], v[178:181], v[62:65]
	v_mfma_f32_16x16x32_bf16 v[58:61], v[122:125], v[178:181], v[58:61]
	v_mfma_f32_16x16x32_bf16 v[46:49], v[110:113], v[186:189], v[46:49]
	v_mfma_f32_16x16x32_bf16 v[42:45], v[122:125], v[186:189], v[42:45]
	v_mfma_f32_16x16x32_bf16 v[30:33], v[110:113], v[194:197], v[30:33]
	v_mfma_f32_16x16x32_bf16 v[26:29], v[122:125], v[194:197], v[26:29]
	s_waitcnt lgkmcnt(0)
	v_mfma_f32_16x16x32_bf16 v[14:17], v[110:113], v[202:205], v[14:17]
	v_mfma_f32_16x16x32_bf16 v[10:13], v[122:125], v[202:205], v[10:13]
	v_mfma_f32_16x16x32_bf16 v[54:57], v[150:153], v[174:177], v[54:57]
	v_mfma_f32_16x16x32_bf16 v[50:53], v[166:169], v[174:177], v[50:53]
	v_mfma_f32_16x16x32_bf16 v[38:41], v[150:153], v[182:185], v[38:41]
	v_mfma_f32_16x16x32_bf16 v[34:37], v[166:169], v[182:185], v[34:37]
	v_mfma_f32_16x16x32_bf16 v[22:25], v[150:153], v[190:193], v[22:25]
	v_mfma_f32_16x16x32_bf16 v[18:21], v[166:169], v[190:193], v[18:21]
	v_mfma_f32_16x16x32_bf16 v[6:9], v[150:153], v[198:201], v[6:9]
	v_mfma_f32_16x16x32_bf16 v[2:5], v[166:169], v[198:201], v[2:5]
	v_mfma_f32_16x16x32_bf16 v[54:57], v[162:165], v[178:181], v[54:57]
	v_mfma_f32_16x16x32_bf16 v[50:53], v[170:173], v[178:181], v[50:53]
	v_mfma_f32_16x16x32_bf16 v[38:41], v[162:165], v[186:189], v[38:41]
	v_mfma_f32_16x16x32_bf16 v[34:37], v[170:173], v[186:189], v[34:37]
	v_mfma_f32_16x16x32_bf16 v[22:25], v[162:165], v[194:197], v[22:25]
	v_mfma_f32_16x16x32_bf16 v[18:21], v[170:173], v[194:197], v[18:21]
	v_mfma_f32_16x16x32_bf16 v[6:9], v[162:165], v[202:205], v[6:9]
	v_mfma_f32_16x16x32_bf16 v[2:5], v[170:173], v[202:205], v[2:5]
	s_barrier
	ds_read_b128 v[106:109], v160
	ds_read_b128 v[110:113], v160 offset:1024
	ds_read_b128 v[114:117], v160 offset:2048
	ds_read_b128 v[122:125], v160 offset:3072
	ds_read_b128 v[150:153], v161
	ds_read_b128 v[162:165], v161 offset:1024
	ds_read_b128 v[166:169], v161 offset:2048
	ds_read_b128 v[170:173], v161 offset:3072
	s_mov_b32 m0, s21
	ds_read_b128 v[174:177], v159 offset:32768
	ds_read_b128 v[178:181], v159 offset:33792
	ds_read_b128 v[182:185], v159 offset:34816
	ds_read_b128 v[186:189], v159 offset:35840
	ds_read_b128 v[190:193], v159 offset:36864
	ds_read_b128 v[194:197], v159 offset:37888
	ds_read_b128 v[198:201], v159 offset:38912
	ds_read_b128 v[202:205], v159 offset:39936
	buffer_load_dwordx4 v1, s[80:83], s48 offen lds
	s_mov_b32 m0, s22
	s_nop 0
	buffer_load_dwordx4 v1, s[80:83], s47 offen lds
	s_waitcnt vmcnt(8)
	s_waitcnt lgkmcnt(0)
	s_barrier
	s_waitcnt lgkmcnt(7)
	v_mfma_f32_16x16x32_bf16 v[142:145], v[106:109], v[174:177], v[142:145]
	v_mfma_f32_16x16x32_bf16 v[138:141], v[114:117], v[174:177], v[138:141]
	s_waitcnt lgkmcnt(5)
	v_mfma_f32_16x16x32_bf16 v[126:129], v[106:109], v[182:185], v[126:129]
	v_mfma_f32_16x16x32_bf16 v[118:121], v[114:117], v[182:185], v[118:121]
	s_waitcnt lgkmcnt(3)
	v_mfma_f32_16x16x32_bf16 v[94:97], v[106:109], v[190:193], v[94:97]
	v_mfma_f32_16x16x32_bf16 v[90:93], v[114:117], v[190:193], v[90:93]
	s_waitcnt lgkmcnt(1)
	v_mfma_f32_16x16x32_bf16 v[78:81], v[106:109], v[198:201], v[78:81]
	v_mfma_f32_16x16x32_bf16 v[74:77], v[114:117], v[198:201], v[74:77]
	v_mfma_f32_16x16x32_bf16 v[142:145], v[110:113], v[178:181], v[142:145]
	v_mfma_f32_16x16x32_bf16 v[138:141], v[122:125], v[178:181], v[138:141]
	v_mfma_f32_16x16x32_bf16 v[126:129], v[110:113], v[186:189], v[126:129]
	v_mfma_f32_16x16x32_bf16 v[118:121], v[122:125], v[186:189], v[118:121]
	v_mfma_f32_16x16x32_bf16 v[94:97], v[110:113], v[194:197], v[94:97]
	v_mfma_f32_16x16x32_bf16 v[90:93], v[122:125], v[194:197], v[90:93]
	s_waitcnt lgkmcnt(0)
	v_mfma_f32_16x16x32_bf16 v[78:81], v[110:113], v[202:205], v[78:81]
	v_mfma_f32_16x16x32_bf16 v[74:77], v[122:125], v[202:205], v[74:77]
	v_mfma_f32_16x16x32_bf16 v[134:137], v[150:153], v[174:177], v[134:137]
	v_mfma_f32_16x16x32_bf16 v[130:133], v[166:169], v[174:177], v[130:133]
	v_mfma_f32_16x16x32_bf16 v[102:105], v[150:153], v[182:185], v[102:105]
	v_mfma_f32_16x16x32_bf16 v[98:101], v[166:169], v[182:185], v[98:101]
	v_mfma_f32_16x16x32_bf16 v[86:89], v[150:153], v[190:193], v[86:89]
	v_mfma_f32_16x16x32_bf16 v[82:85], v[166:169], v[190:193], v[82:85]
	v_mfma_f32_16x16x32_bf16 v[70:73], v[150:153], v[198:201], v[70:73]
	v_mfma_f32_16x16x32_bf16 v[66:69], v[166:169], v[198:201], v[66:69]
	v_mfma_f32_16x16x32_bf16 v[134:137], v[162:165], v[178:181], v[134:137]
	v_mfma_f32_16x16x32_bf16 v[130:133], v[170:173], v[178:181], v[130:133]
	v_mfma_f32_16x16x32_bf16 v[102:105], v[162:165], v[186:189], v[102:105]
	v_mfma_f32_16x16x32_bf16 v[98:101], v[170:173], v[186:189], v[98:101]
	v_mfma_f32_16x16x32_bf16 v[86:89], v[162:165], v[194:197], v[86:89]
	v_mfma_f32_16x16x32_bf16 v[82:85], v[170:173], v[194:197], v[82:85]
	v_mfma_f32_16x16x32_bf16 v[70:73], v[162:165], v[202:205], v[70:73]
	v_mfma_f32_16x16x32_bf16 v[66:69], v[170:173], v[202:205], v[66:69]
	s_barrier
; #define PG8_STAGE(bufoff, goff, voff) do { _Pragma("unroll") for (int _i = 0; _i < 2; ++_i) \
;         __builtin_amdgcn_raw_ptr_buffer_load_lds(rsrc, (PG8_LAS void*)(lds + (bufoff) + ldsw + _i * 8192), 16, (int)(voff), (int)((goff) + _i * p1##voff), 0, 0); } while (0)
; #define PG8_LDA(dst, b, h) do { _Pragma("unroll") for (int m = 0; m < 4; ++m) dst[m] = PG8_LD8(lds + PG8_SA(b, h) + aoff + m * 2048); } while (0)
; #define PG8_WAIT_V(n) asm volatile("s_waitcnt vmcnt(" #n ")" ::: "memory")
; #define PG8_WAIT_L(n) asm volatile("s_waitcnt lgkmcnt(" #n ")" ::: "memory")
; #define PG8_BAR __builtin_amdgcn_s_barrier()
; #define PG8_SCHED __builtin_amdgcn_sched_barrier(0)
; #define PG8_ZERO() do { _Pragma("unroll") for (int a = 0; a < 2; ++a) _Pragma("unroll") for (int b = 0; b < 2; ++b) _Pragma("unroll") for (int m = 0; m < 4; ++m) _Pragma("unroll") for (int n = 0; n < 2; ++n) acc[a][b][m][n] = (f32x4){0.f, 0.f, 0.f, 0.f}; } while (0)
; template <class Epi, class Sched, bool ALIGN_EPI, bool F8 = false, int F8SC = F8_SCALES>
; __device__ __forceinline__ void gemm_phase(PG8_LAS unsigned char* lds, const __amdgpu_buffer_rsrc_t rsrc, const int lda, const int ldb, const int K, const Sched& S, const Epi& E) {
;     ...
;             PG8_LDA(At, 1, 1); PG8_STAGE(PG8_SB(1, 0), b3, voffB); PG8_STAGE(PG8_SB(1, 1), b3 + hsB, voffB); PG8_STAGE(PG8_SA(1, 0), a3, voffA);
;             PG8_WAIT_V(8); PG8_WAIT_L(0); PG8_BAR; PG8_MMA(1, 0, At, B0); PG8_MMA(1, 1, At, B1); PG8_BAR; PG8_SCHED;
;         }
;         if constexpr (ALIGN_EPI) { if (wr == 0) PG8_BAR; }
;         bool keep; { int t2 = threadIdx.x; asm volatile("" : "+v"(t2)); const int w2 = __builtin_amdgcn_readfirstlane(t2 >> 6), l2 = t2 & 63; keep = E(acc, cur, w2 >> 2, w2 & 3, l2 & 15, l2 >> 4); }
;         if (!has_next) break;
;         if (!keep) PG8_ZERO();
	s_mov_b32 m0, s24
	ds_read_b128 v[174:177], v159 offset:49152
	ds_read_b128 v[178:181], v159 offset:50176
	ds_read_b128 v[182:185], v159 offset:51200
	ds_read_b128 v[186:189], v159 offset:52224
	ds_read_b128 v[190:193], v159 offset:53248
	ds_read_b128 v[194:197], v159 offset:54272
	ds_read_b128 v[198:201], v159 offset:55296
	ds_read_b128 v[202:205], v159 offset:56320
	buffer_load_dwordx4 v156, s[80:83], s46 offen lds
	s_mov_b32 m0, s25
	s_nop 0
	buffer_load_dwordx4 v156, s[80:83], s45 offen lds
	s_mov_b32 m0, s28
	s_nop 0
	buffer_load_dwordx4 v156, s[80:83], s43 offen lds
	s_mov_b32 m0, s29
	s_nop 0
	buffer_load_dwordx4 v156, s[80:83], s13 offen lds
	s_mov_b32 m0, s26
	s_nop 0
	buffer_load_dwordx4 v1, s[80:83], s44 offen lds
	s_mov_b32 m0, s27
	s_nop 0
	buffer_load_dwordx4 v1, s[80:83], s12 offen lds
	s_waitcnt vmcnt(8)
	s_waitcnt lgkmcnt(0)
	s_barrier
	s_waitcnt lgkmcnt(7)
	v_mfma_f32_16x16x32_bf16 v[62:65], v[106:109], v[174:177], v[62:65]
	v_mfma_f32_16x16x32_bf16 v[58:61], v[114:117], v[174:177], v[58:61]
	s_waitcnt lgkmcnt(5)
	v_mfma_f32_16x16x32_bf16 v[46:49], v[106:109], v[182:185], v[46:49]
	v_mfma_f32_16x16x32_bf16 v[42:45], v[114:117], v[182:185], v[42:45]
	s_waitcnt lgkmcnt(3)
	v_mfma_f32_16x16x32_bf16 v[30:33], v[106:109], v[190:193], v[30:33]
	v_mfma_f32_16x16x32_bf16 v[26:29], v[114:117], v[190:193], v[26:29]
	s_waitcnt lgkmcnt(1)
	v_mfma_f32_16x16x32_bf16 v[14:17], v[106:109], v[198:201], v[14:17]
	v_mfma_f32_16x16x32_bf16 v[10:13], v[114:117], v[198:201], v[10:13]
	v_mfma_f32_16x16x32_bf16 v[62:65], v[110:113], v[178:181], v[62:65]
	v_mfma_f32_16x16x32_bf16 v[58:61], v[122:125], v[178:181], v[58:61]
	v_mfma_f32_16x16x32_bf16 v[46:49], v[110:113], v[186:189], v[46:49]
	v_mfma_f32_16x16x32_bf16 v[42:45], v[122:125], v[186:189], v[42:45]
	v_mfma_f32_16x16x32_bf16 v[30:33], v[110:113], v[194:197], v[30:33]
	v_mfma_f32_16x16x32_bf16 v[26:29], v[122:125], v[194:197], v[26:29]
	s_waitcnt lgkmcnt(0)
	v_mfma_f32_16x16x32_bf16 v[14:17], v[110:113], v[202:205], v[14:17]
	v_mfma_f32_16x16x32_bf16 v[10:13], v[122:125], v[202:205], v[10:13]
	v_mfma_f32_16x16x32_bf16 v[54:57], v[150:153], v[174:177], v[54:57]
	v_mfma_f32_16x16x32_bf16 v[50:53], v[166:169], v[174:177], v[50:53]
	v_mfma_f32_16x16x32_bf16 v[38:41], v[150:153], v[182:185], v[38:41]
	v_mfma_f32_16x16x32_bf16 v[34:37], v[166:169], v[182:185], v[34:37]
	v_mfma_f32_16x16x32_bf16 v[22:25], v[150:153], v[190:193], v[22:25]
	v_mfma_f32_16x16x32_bf16 v[18:21], v[166:169], v[190:193], v[18:21]
	v_mfma_f32_16x16x32_bf16 v[6:9], v[150:153], v[198:201], v[6:9]
	v_mfma_f32_16x16x32_bf16 v[2:5], v[166:169], v[198:201], v[2:5]
	v_mfma_f32_16x16x32_bf16 v[54:57], v[162:165], v[178:181], v[54:57]
	v_mfma_f32_16x16x32_bf16 v[50:53], v[170:173], v[178:181], v[50:53]
	v_mfma_f32_16x16x32_bf16 v[38:41], v[162:165], v[186:189], v[38:41]
	v_mfma_f32_16x16x32_bf16 v[34:37], v[170:173], v[186:189], v[34:37]
	v_mfma_f32_16x16x32_bf16 v[22:25], v[162:165], v[194:197], v[22:25]
	v_mfma_f32_16x16x32_bf16 v[18:21], v[170:173], v[194:197], v[18:21]
	v_mfma_f32_16x16x32_bf16 v[6:9], v[162:165], v[202:205], v[6:9]
	v_mfma_f32_16x16x32_bf16 v[2:5], v[170:173], v[202:205], v[2:5]
	s_barrier
	s_andn2_b64 vcc, exec, s[6:7]
	s_mov_b64 s[12:13], -1
	s_mov_b64 s[6:7], 0
	s_movk_i32 s43, 0x100
	s_cbranch_vccz .LBB0_995
	s_and_b64 vcc, exec, s[10:11]
	s_cbranch_vccz .LBB0_998
	s_barrier

;     __device__ __forceinline__ bool next(int i, Unit& u) const { u.aux = 0; return t.map(i, u.pm, u.pn); }
;     __device__ __forceinline__ bool next(int i, Unit& u) const { u.aux = i & 1; return t.map(i >> 1, u.pm, u.pn); }
; #define PG8_STAGE(bufoff, goff, voff) do { _Pragma("unroll") for (int _i = 0; _i < 2; ++_i) \
;         __builtin_amdgcn_raw_ptr_buffer_load_lds(rsrc, (PG8_LAS void*)(lds + (bufoff) + ldsw + _i * 8192), 16, (int)(voff), (int)((goff) + _i * p1##voff), 0, 0); } while (0)
; #define PG8_LDA(dst, b, h) do { _Pragma("unroll") for (int m = 0; m < 4; ++m) dst[m] = PG8_LD8(lds + PG8_SA(b, h) + aoff + m * 2048); } while (0)
; #define PG8_LDB(dst, b, h) do { _Pragma("unroll") for (int n = 0; n < 2; ++n) dst[n] = PG8_LD8(lds + PG8_SB(b, h) + boff + n * 2048); } while (0)
; #define PG8_WAIT_V(n) asm volatile("s_waitcnt vmcnt(" #n ")" ::: "memory")
; #define PG8_WAIT_L(n) asm volatile("s_waitcnt lgkmcnt(" #n ")" ::: "memory")
; #define PG8_BAR __builtin_amdgcn_s_barrier()
; #define PG8_SCHED __builtin_amdgcn_sched_barrier(0)
; template <class Epi, class Sched, bool ALIGN_EPI, bool F8 = false, int F8SC = F8_SCALES>
; __device__ __forceinline__ void gemm_phase(PG8_LAS unsigned char* lds, const __amdgpu_buffer_rsrc_t rsrc, const int lda, const int ldb, const int K, const Sched& S, const Epi& E) {
;     ...
;     for (;;) {
;         const bool has_next = S.next(ui + 1, nxt);
;         unsigned nA = cA, nB = cB; if (has_next) { S.bases(nxt, nA, nB); nA = __builtin_amdgcn_readfirstlane(nA); nB = __builtin_amdgcn_readfirstlane(nB); }
; #pragma unroll 1
;         for (int t = 0; t < nt; t += 2) {
;             const bool last = (t == nt - 2);
;             const unsigned a1 = cA + (unsigned)(t + 1) * kstep;
;             const unsigned a2 = last ? nA : cA + (unsigned)(t + 2) * kstep, b2 = last ? nB : cB + (unsigned)(t + 2) * kstep;
;             const unsigned a3 = a2 + kstep, b3 = b2 + kstep;
;             PG8_LDB(B0, 0, 0); PG8_LDB(B1, 0, 1); PG8_SCHED; PG8_LDA(At, 0, 0); PG8_STAGE(PG8_SA(1, 1), a1 + hsA, voffA);
;             PG8_WAIT_V(8); PG8_WAIT_L(0); PG8_BAR; PG8_MMA(0, 0, At, B0); PG8_MMA(0, 1, At, B1); PG8_BAR; PG8_SCHED;
;             PG8_LDA(At, 0, 1); PG8_STAGE(PG8_SB(0, 0), b2, voffB); PG8_STAGE(PG8_SB(0, 1), b2 + hsB, voffB); PG8_STAGE(PG8_SA(0, 0), a2, voffA);
.LBB0_1021:
	ds_read_b128 v[140:143], v135
	ds_read_b128 v[144:147], v135 offset:1024
	ds_read_b128 v[148:151], v135 offset:2048
	ds_read_b128 v[152:155], v135 offset:3072
	ds_read_b128 v[156:159], v136
	ds_read_b128 v[160:163], v136 offset:1024
	ds_read_b128 v[164:167], v136 offset:2048
	ds_read_b128 v[168:171], v136 offset:3072
	s_add_i32 s44, s41, 0x100
	s_add_i32 s45, s44, s39
	s_and_b64 s[42:43], s[10:11], exec
	s_cselect_b32 s47, s37, s45
	s_add_i32 s44, s44, s36
	s_add_i32 s42, s47, 0x80
	s_and_b64 s[10:11], s[10:11], exec
	s_cselect_b32 s50, s38, s44
	s_add_i32 s53, s40, s41
	s_add_i32 s41, s50, 0x10080
	s_add_i32 s11, s50, 0x18080
	s_add_i32 s10, s47, 0x10080
	s_add_i32 s54, s53, 0x10000
	s_add_i32 s52, s50, 0x8000
	s_add_i32 s51, s50, 0x10000
	s_add_i32 s49, s50, 0x18000
	s_add_i32 s48, s47, 0x10000
	s_add_i32 s46, s47, 0x20000
	s_add_i32 s45, s47, 0x30000
	s_add_i32 s44, s50, 0x80
	s_add_i32 s43, s50, 0x8080
	s_mov_b32 s80, s96
	s_mov_b32 m0, s28
	ds_read_b128 v[172:175], v137
	ds_read_b128 v[176:179], v137 offset:1024
	ds_read_b128 v[180:183], v137 offset:2048
	ds_read_b128 v[184:187], v137 offset:3072
	ds_read_b128 v[188:191], v137 offset:4096
	ds_read_b128 v[192:195], v137 offset:5120
	ds_read_b128 v[196:199], v137 offset:6144
	ds_read_b128 v[200:203], v137 offset:7168
	buffer_load_dwordx4 v1, s[80:83], s53 offen lds
	s_mov_b32 m0, s29
	s_nop 0
	buffer_load_dwordx4 v1, s[80:83], s54 offen lds
	s_waitcnt vmcnt(8)
	s_waitcnt lgkmcnt(0)
	s_barrier
	s_waitcnt lgkmcnt(7)
	v_mfma_f32_16x16x32_bf16 v[126:129], v[140:143], v[172:175], v[126:129]
	v_mfma_f32_16x16x32_bf16 v[122:125], v[148:151], v[172:175], v[122:125]
	s_waitcnt lgkmcnt(5)
	v_mfma_f32_16x16x32_bf16 v[118:121], v[140:143], v[180:183], v[118:121]
	v_mfma_f32_16x16x32_bf16 v[114:117], v[148:151], v[180:183], v[114:117]
	s_waitcnt lgkmcnt(3)
	v_mfma_f32_16x16x32_bf16 v[102:105], v[140:143], v[188:191], v[102:105]
	v_mfma_f32_16x16x32_bf16 v[98:101], v[148:151], v[188:191], v[98:101]
	s_waitcnt lgkmcnt(1)
	v_mfma_f32_16x16x32_bf16 v[86:89], v[140:143], v[196:199], v[86:89]
	v_mfma_f32_16x16x32_bf16 v[82:85], v[148:151], v[196:199], v[82:85]
	v_mfma_f32_16x16x32_bf16 v[126:129], v[144:147], v[176:179], v[126:129]
	v_mfma_f32_16x16x32_bf16 v[122:125], v[152:155], v[176:179], v[122:125]
	v_mfma_f32_16x16x32_bf16 v[118:121], v[144:147], v[184:187], v[118:121]
	v_mfma_f32_16x16x32_bf16 v[114:117], v[152:155], v[184:187], v[114:117]
	v_mfma_f32_16x16x32_bf16 v[102:105], v[144:147], v[192:195], v[102:105]
	v_mfma_f32_16x16x32_bf16 v[98:101], v[152:155], v[192:195], v[98:101]
	s_waitcnt lgkmcnt(0)
	v_mfma_f32_16x16x32_bf16 v[86:89], v[144:147], v[200:203], v[86:89]
	v_mfma_f32_16x16x32_bf16 v[82:85], v[152:155], v[200:203], v[82:85]
	v_mfma_f32_16x16x32_bf16 v[110:113], v[156:159], v[172:175], v[110:113]
	v_mfma_f32_16x16x32_bf16 v[106:109], v[164:167], v[172:175], v[106:109]
	v_mfma_f32_16x16x32_bf16 v[94:97], v[156:159], v[180:183], v[94:97]
	v_mfma_f32_16x16x32_bf16 v[90:93], v[164:167], v[180:183], v[90:93]
	v_mfma_f32_16x16x32_bf16 v[78:81], v[156:159], v[188:191], v[78:81]
	v_mfma_f32_16x16x32_bf16 v[74:77], v[164:167], v[188:191], v[74:77]
	v_mfma_f32_16x16x32_bf16 v[70:73], v[156:159], v[196:199], v[70:73]
	v_mfma_f32_16x16x32_bf16 v[66:69], v[164:167], v[196:199], v[66:69]
	v_mfma_f32_16x16x32_bf16 v[110:113], v[160:163], v[176:179], v[110:113]
	v_mfma_f32_16x16x32_bf16 v[106:109], v[168:171], v[176:179], v[106:109]
	v_mfma_f32_16x16x32_bf16 v[94:97], v[160:163], v[184:187], v[94:97]
	v_mfma_f32_16x16x32_bf16 v[90:93], v[168:171], v[184:187], v[90:93]
	v_mfma_f32_16x16x32_bf16 v[78:81], v[160:163], v[192:195], v[78:81]
	v_mfma_f32_16x16x32_bf16 v[74:77], v[168:171], v[192:195], v[74:77]
	v_mfma_f32_16x16x32_bf16 v[70:73], v[160:163], v[200:203], v[70:73]
	v_mfma_f32_16x16x32_bf16 v[66:69], v[168:171], v[200:203], v[66:69]
	s_barrier
	s_mov_b32 m0, s14
	ds_read_b128 v[172:175], v137 offset:16384
	ds_read_b128 v[176:179], v137 offset:17408
	ds_read_b128 v[180:183], v137 offset:18432
	ds_read_b128 v[184:187], v137 offset:19456
	ds_read_b128 v[188:191], v137 offset:20480
	ds_read_b128 v[192:195], v137 offset:21504
	ds_read_b128 v[196:199], v137 offset:22528
	ds_read_b128 v[200:203], v137 offset:23552
	buffer_load_dwordx4 v134, s[80:83], s50 offen lds
	s_mov_b32 m0, s15
	s_nop 0
	buffer_load_dwordx4 v134, s[80:83], s52 offen lds
	s_mov_b32 m0, s16
	s_nop 0
	buffer_load_dwordx4 v134, s[80:83], s51 offen lds
	s_mov_b32 m0, s17
	s_nop 0
	buffer_load_dwordx4 v134, s[80:83], s49 offen lds
	s_mov_b32 m0, s13
	s_nop 0
	buffer_load_dwordx4 v1, s[80:83], s47 offen lds
	s_mov_b32 m0, s18
	s_nop 0
	buffer_load_dwordx4 v1, s[80:83], s48 offen lds
	s_waitcnt vmcnt(8)
	s_waitcnt lgkmcnt(0)
	s_barrier
; #define PG8_STAGE(bufoff, goff, voff) do { _Pragma("unroll") for (int _i = 0; _i < 2; ++_i) \
;         __builtin_amdgcn_raw_ptr_buffer_load_lds(rsrc, (PG8_LAS void*)(lds + (bufoff) + ldsw + _i * 8192), 16, (int)(voff), (int)((goff) + _i * p1##voff), 0, 0); } while (0)
; #define PG8_LDA(dst, b, h) do { _Pragma("unroll") for (int m = 0; m < 4; ++m) dst[m] = PG8_LD8(lds + PG8_SA(b, h) + aoff + m * 2048); } while (0)
; #define PG8_LDB(dst, b, h) do { _Pragma("unroll") for (int n = 0; n < 2; ++n) dst[n] = PG8_LD8(lds + PG8_SB(b, h) + boff + n * 2048); } while (0)
; #define PG8_WAIT_V(n) asm volatile("s_waitcnt vmcnt(" #n ")" ::: "memory")
; #define PG8_WAIT_L(n) asm volatile("s_waitcnt lgkmcnt(" #n ")" ::: "memory")
; #define PG8_BAR __builtin_amdgcn_s_barrier()
; #define PG8_SCHED __builtin_amdgcn_sched_barrier(0)
; template <class Epi, class Sched, bool ALIGN_EPI, bool F8 = false, int F8SC = F8_SCALES>
; __device__ __forceinline__ void gemm_phase(PG8_LAS unsigned char* lds, const __amdgpu_buffer_rsrc_t rsrc, const int lda, const int ldb, const int K, const Sched& S, const Epi& E) {
;     ...
;             PG8_WAIT_V(8); PG8_WAIT_L(0); PG8_BAR; PG8_MMA(1, 0, At, B0); PG8_MMA(1, 1, At, B1); PG8_BAR; PG8_SCHED;
;             PG8_LDB(B0, 1, 0); PG8_LDB(B1, 1, 1); PG8_SCHED; PG8_LDA(At, 1, 0); PG8_STAGE(PG8_SA(0, 1), a2 + hsA, voffA);
;             PG8_WAIT_V(8); PG8_WAIT_L(0); PG8_BAR; PG8_MMA(0, 0, At, B0); PG8_MMA(0, 1, At, B1); PG8_BAR; PG8_SCHED;
	s_waitcnt lgkmcnt(7)
	v_mfma_f32_16x16x32_bf16 v[62:65], v[140:143], v[172:175], v[62:65]
	v_mfma_f32_16x16x32_bf16 v[58:61], v[148:151], v[172:175], v[58:61]
	s_waitcnt lgkmcnt(5)
	v_mfma_f32_16x16x32_bf16 v[54:57], v[140:143], v[180:183], v[54:57]
	v_mfma_f32_16x16x32_bf16 v[50:53], v[148:151], v[180:183], v[50:53]
	s_waitcnt lgkmcnt(3)
	v_mfma_f32_16x16x32_bf16 v[38:41], v[140:143], v[188:191], v[38:41]
	v_mfma_f32_16x16x32_bf16 v[34:37], v[148:151], v[188:191], v[34:37]
	s_waitcnt lgkmcnt(1)
	v_mfma_f32_16x16x32_bf16 v[22:25], v[140:143], v[196:199], v[22:25]
	v_mfma_f32_16x16x32_bf16 v[18:21], v[148:151], v[196:199], v[18:21]
	v_mfma_f32_16x16x32_bf16 v[62:65], v[144:147], v[176:179], v[62:65]
	v_mfma_f32_16x16x32_bf16 v[58:61], v[152:155], v[176:179], v[58:61]
	v_mfma_f32_16x16x32_bf16 v[54:57], v[144:147], v[184:187], v[54:57]
	v_mfma_f32_16x16x32_bf16 v[50:53], v[152:155], v[184:187], v[50:53]
	v_mfma_f32_16x16x32_bf16 v[38:41], v[144:147], v[192:195], v[38:41]
	v_mfma_f32_16x16x32_bf16 v[34:37], v[152:155], v[192:195], v[34:37]
	s_waitcnt lgkmcnt(0)
	v_mfma_f32_16x16x32_bf16 v[22:25], v[144:147], v[200:203], v[22:25]
	v_mfma_f32_16x16x32_bf16 v[18:21], v[152:155], v[200:203], v[18:21]
	v_mfma_f32_16x16x32_bf16 v[46:49], v[156:159], v[172:175], v[46:49]
	v_mfma_f32_16x16x32_bf16 v[42:45], v[164:167], v[172:175], v[42:45]
	v_mfma_f32_16x16x32_bf16 v[30:33], v[156:159], v[180:183], v[30:33]
	v_mfma_f32_16x16x32_bf16 v[26:29], v[164:167], v[180:183], v[26:29]
	v_mfma_f32_16x16x32_bf16 v[14:17], v[156:159], v[188:191], v[14:17]
	v_mfma_f32_16x16x32_bf16 v[10:13], v[164:167], v[188:191], v[10:13]
	v_mfma_f32_16x16x32_bf16 v[6:9], v[156:159], v[196:199], v[6:9]
	v_mfma_f32_16x16x32_bf16 v[2:5], v[164:167], v[196:199], v[2:5]
	v_mfma_f32_16x16x32_bf16 v[46:49], v[160:163], v[176:179], v[46:49]
	v_mfma_f32_16x16x32_bf16 v[42:45], v[168:171], v[176:179], v[42:45]
	v_mfma_f32_16x16x32_bf16 v[30:33], v[160:163], v[184:187], v[30:33]
	v_mfma_f32_16x16x32_bf16 v[26:29], v[168:171], v[184:187], v[26:29]
	v_mfma_f32_16x16x32_bf16 v[14:17], v[160:163], v[192:195], v[14:17]
	v_mfma_f32_16x16x32_bf16 v[10:13], v[168:171], v[192:195], v[10:13]
	v_mfma_f32_16x16x32_bf16 v[6:9], v[160:163], v[200:203], v[6:9]
	v_mfma_f32_16x16x32_bf16 v[2:5], v[168:171], v[200:203], v[2:5]
	s_barrier
	ds_read_b128 v[140:143], v138
	ds_read_b128 v[144:147], v138 offset:1024
	ds_read_b128 v[148:151], v138 offset:2048
	ds_read_b128 v[152:155], v138 offset:3072
	ds_read_b128 v[156:159], v139
	ds_read_b128 v[160:163], v139 offset:1024
	ds_read_b128 v[164:167], v139 offset:2048
	ds_read_b128 v[168:171], v139 offset:3072
	s_mov_b32 m0, s19
	ds_read_b128 v[172:175], v137 offset:32768
	ds_read_b128 v[176:179], v137 offset:33792
	ds_read_b128 v[180:183], v137 offset:34816
	ds_read_b128 v[184:187], v137 offset:35840
	ds_read_b128 v[188:191], v137 offset:36864
	ds_read_b128 v[192:195], v137 offset:37888
	ds_read_b128 v[196:199], v137 offset:38912
	ds_read_b128 v[200:203], v137 offset:39936
	buffer_load_dwordx4 v1, s[80:83], s46 offen lds
	s_mov_b32 m0, s20
	s_nop 0
	buffer_load_dwordx4 v1, s[80:83], s45 offen lds
	s_waitcnt vmcnt(8)
	s_waitcnt lgkmcnt(0)
	s_barrier
	s_waitcnt lgkmcnt(7)
	v_mfma_f32_16x16x32_bf16 v[126:129], v[140:143], v[172:175], v[126:129]
	v_mfma_f32_16x16x32_bf16 v[122:125], v[148:151], v[172:175], v[122:125]
	s_waitcnt lgkmcnt(5)
	v_mfma_f32_16x16x32_bf16 v[118:121], v[140:143], v[180:183], v[118:121]
	v_mfma_f32_16x16x32_bf16 v[114:117], v[148:151], v[180:183], v[114:117]
	s_waitcnt lgkmcnt(3)
	v_mfma_f32_16x16x32_bf16 v[102:105], v[140:143], v[188:191], v[102:105]
	v_mfma_f32_16x16x32_bf16 v[98:101], v[148:151], v[188:191], v[98:101]
	s_waitcnt lgkmcnt(1)
	v_mfma_f32_16x16x32_bf16 v[86:89], v[140:143], v[196:199], v[86:89]
	v_mfma_f32_16x16x32_bf16 v[82:85], v[148:151], v[196:199], v[82:85]
	v_mfma_f32_16x16x32_bf16 v[126:129], v[144:147], v[176:179], v[126:129]
	v_mfma_f32_16x16x32_bf16 v[122:125], v[152:155], v[176:179], v[122:125]
	v_mfma_f32_16x16x32_bf16 v[118:121], v[144:147], v[184:187], v[118:121]
	v_mfma_f32_16x16x32_bf16 v[114:117], v[152:155], v[184:187], v[114:117]
	v_mfma_f32_16x16x32_bf16 v[102:105], v[144:147], v[192:195], v[102:105]
	v_mfma_f32_16x16x32_bf16 v[98:101], v[152:155], v[192:195], v[98:101]
	s_waitcnt lgkmcnt(0)
	v_mfma_f32_16x16x32_bf16 v[86:89], v[144:147], v[200:203], v[86:89]
	v_mfma_f32_16x16x32_bf16 v[82:85], v[152:155], v[200:203], v[82:85]
	v_mfma_f32_16x16x32_bf16 v[110:113], v[156:159], v[172:175], v[110:113]
	v_mfma_f32_16x16x32_bf16 v[106:109], v[164:167], v[172:175], v[106:109]
	v_mfma_f32_16x16x32_bf16 v[94:97], v[156:159], v[180:183], v[94:97]
	v_mfma_f32_16x16x32_bf16 v[90:93], v[164:167], v[180:183], v[90:93]
	v_mfma_f32_16x16x32_bf16 v[78:81], v[156:159], v[188:191], v[78:81]
	v_mfma_f32_16x16x32_bf16 v[74:77], v[164:167], v[188:191], v[74:77]
	v_mfma_f32_16x16x32_bf16 v[70:73], v[156:159], v[196:199], v[70:73]
	v_mfma_f32_16x16x32_bf16 v[66:69], v[164:167], v[196:199], v[66:69]
	v_mfma_f32_16x16x32_bf16 v[110:113], v[160:163], v[176:179], v[110:113]
	v_mfma_f32_16x16x32_bf16 v[106:109], v[168:171], v[176:179], v[106:109]
	v_mfma_f32_16x16x32_bf16 v[94:97], v[160:163], v[184:187], v[94:97]
	v_mfma_f32_16x16x32_bf16 v[90:93], v[168:171], v[184:187], v[90:93]
	v_mfma_f32_16x16x32_bf16 v[78:81], v[160:163], v[192:195], v[78:81]
	v_mfma_f32_16x16x32_bf16 v[74:77], v[168:171], v[192:195], v[74:77]
	v_mfma_f32_16x16x32_bf16 v[70:73], v[160:163], v[200:203], v[70:73]
	v_mfma_f32_16x16x32_bf16 v[66:69], v[168:171], v[200:203], v[66:69]
	s_barrier
; #define PG8_STAGE(bufoff, goff, voff) do { _Pragma("unroll") for (int _i = 0; _i < 2; ++_i) \
;         __builtin_amdgcn_raw_ptr_buffer_load_lds(rsrc, (PG8_LAS void*)(lds + (bufoff) + ldsw + _i * 8192), 16, (int)(voff), (int)((goff) + _i * p1##voff), 0, 0); } while (0)
; #define PG8_LDA(dst, b, h) do { _Pragma("unroll") for (int m = 0; m < 4; ++m) dst[m] = PG8_LD8(lds + PG8_SA(b, h) + aoff + m * 2048); } while (0)
; #define PG8_WAIT_V(n) asm volatile("s_waitcnt vmcnt(" #n ")" ::: "memory")
; #define PG8_WAIT_L(n) asm volatile("s_waitcnt lgkmcnt(" #n ")" ::: "memory")
; #define PG8_BAR __builtin_amdgcn_s_barrier()
; #define PG8_SCHED __builtin_amdgcn_sched_barrier(0)
; #define PG8_ZERO() do { _Pragma("unroll") for (int a = 0; a < 2; ++a) _Pragma("unroll") for (int b = 0; b < 2; ++b) _Pragma("unroll") for (int m = 0; m < 4; ++m) _Pragma("unroll") for (int n = 0; n < 2; ++n) acc[a][b][m][n] = (f32x4){0.f, 0.f, 0.f, 0.f}; } while (0)
; template <class Epi, class Sched, bool ALIGN_EPI, bool F8 = false, int F8SC = F8_SCALES>
; __device__ __forceinline__ void gemm_phase(PG8_LAS unsigned char* lds, const __amdgpu_buffer_rsrc_t rsrc, const int lda, const int ldb, const int K, const Sched& S, const Epi& E) {
;     ...
;             PG8_LDA(At, 1, 1); PG8_STAGE(PG8_SB(1, 0), b3, voffB); PG8_STAGE(PG8_SB(1, 1), b3 + hsB, voffB); PG8_STAGE(PG8_SA(1, 0), a3, voffA);
;             PG8_WAIT_V(8); PG8_WAIT_L(0); PG8_BAR; PG8_MMA(1, 0, At, B0); PG8_MMA(1, 1, At, B1); PG8_BAR; PG8_SCHED;
;         }
;         if constexpr (ALIGN_EPI) { if (wr == 0) PG8_BAR; }
;         bool keep; { int t2 = threadIdx.x; asm volatile("" : "+v"(t2)); const int w2 = __builtin_amdgcn_readfirstlane(t2 >> 6), l2 = t2 & 63; keep = E(acc, cur, w2 >> 2, w2 & 3, l2 & 15, l2 >> 4); }
;         if (!has_next) break;
;         if (!keep) PG8_ZERO();
	s_mov_b32 m0, s22
	ds_read_b128 v[172:175], v137 offset:49152
	ds_read_b128 v[176:179], v137 offset:50176
	ds_read_b128 v[180:183], v137 offset:51200
	ds_read_b128 v[184:187], v137 offset:52224
	ds_read_b128 v[188:191], v137 offset:53248
	ds_read_b128 v[192:195], v137 offset:54272
	ds_read_b128 v[196:199], v137 offset:55296
	ds_read_b128 v[200:203], v137 offset:56320
	buffer_load_dwordx4 v134, s[80:83], s44 offen lds
	s_mov_b32 m0, s23
	s_nop 0
	buffer_load_dwordx4 v134, s[80:83], s43 offen lds
	s_mov_b32 m0, s26
	s_nop 0
	buffer_load_dwordx4 v134, s[80:83], s41 offen lds
	s_mov_b32 m0, s27
	s_nop 0
	buffer_load_dwordx4 v134, s[80:83], s11 offen lds
	s_mov_b32 m0, s24
	s_nop 0
	buffer_load_dwordx4 v1, s[80:83], s42 offen lds
	s_mov_b32 m0, s25
	s_nop 0
	buffer_load_dwordx4 v1, s[80:83], s10 offen lds
	s_waitcnt vmcnt(8)
	s_waitcnt lgkmcnt(0)
	s_barrier
	s_waitcnt lgkmcnt(7)
	v_mfma_f32_16x16x32_bf16 v[62:65], v[140:143], v[172:175], v[62:65]
	v_mfma_f32_16x16x32_bf16 v[58:61], v[148:151], v[172:175], v[58:61]
	s_waitcnt lgkmcnt(5)
	v_mfma_f32_16x16x32_bf16 v[54:57], v[140:143], v[180:183], v[54:57]
	v_mfma_f32_16x16x32_bf16 v[50:53], v[148:151], v[180:183], v[50:53]
	s_waitcnt lgkmcnt(3)
	v_mfma_f32_16x16x32_bf16 v[38:41], v[140:143], v[188:191], v[38:41]
	v_mfma_f32_16x16x32_bf16 v[34:37], v[148:151], v[188:191], v[34:37]
	s_waitcnt lgkmcnt(1)
	v_mfma_f32_16x16x32_bf16 v[22:25], v[140:143], v[196:199], v[22:25]
	v_mfma_f32_16x16x32_bf16 v[18:21], v[148:151], v[196:199], v[18:21]
	v_mfma_f32_16x16x32_bf16 v[62:65], v[144:147], v[176:179], v[62:65]
	v_mfma_f32_16x16x32_bf16 v[58:61], v[152:155], v[176:179], v[58:61]
	v_mfma_f32_16x16x32_bf16 v[54:57], v[144:147], v[184:187], v[54:57]
	v_mfma_f32_16x16x32_bf16 v[50:53], v[152:155], v[184:187], v[50:53]
	v_mfma_f32_16x16x32_bf16 v[38:41], v[144:147], v[192:195], v[38:41]
	v_mfma_f32_16x16x32_bf16 v[34:37], v[152:155], v[192:195], v[34:37]
	s_waitcnt lgkmcnt(0)
	v_mfma_f32_16x16x32_bf16 v[22:25], v[144:147], v[200:203], v[22:25]
	v_mfma_f32_16x16x32_bf16 v[18:21], v[152:155], v[200:203], v[18:21]
	v_mfma_f32_16x16x32_bf16 v[46:49], v[156:159], v[172:175], v[46:49]
	v_mfma_f32_16x16x32_bf16 v[42:45], v[164:167], v[172:175], v[42:45]
	v_mfma_f32_16x16x32_bf16 v[30:33], v[156:159], v[180:183], v[30:33]
	v_mfma_f32_16x16x32_bf16 v[26:29], v[164:167], v[180:183], v[26:29]
	v_mfma_f32_16x16x32_bf16 v[14:17], v[156:159], v[188:191], v[14:17]
	v_mfma_f32_16x16x32_bf16 v[10:13], v[164:167], v[188:191], v[10:13]
	v_mfma_f32_16x16x32_bf16 v[6:9], v[156:159], v[196:199], v[6:9]
	v_mfma_f32_16x16x32_bf16 v[2:5], v[164:167], v[196:199], v[2:5]
	v_mfma_f32_16x16x32_bf16 v[46:49], v[160:163], v[176:179], v[46:49]
	v_mfma_f32_16x16x32_bf16 v[42:45], v[168:171], v[176:179], v[42:45]
	v_mfma_f32_16x16x32_bf16 v[30:33], v[160:163], v[184:187], v[30:33]
	v_mfma_f32_16x16x32_bf16 v[26:29], v[168:171], v[184:187], v[26:29]
	v_mfma_f32_16x16x32_bf16 v[14:17], v[160:163], v[192:195], v[14:17]
	v_mfma_f32_16x16x32_bf16 v[10:13], v[168:171], v[192:195], v[10:13]
	v_mfma_f32_16x16x32_bf16 v[6:9], v[160:163], v[200:203], v[6:9]
	v_mfma_f32_16x16x32_bf16 v[2:5], v[168:171], v[200:203], v[2:5]
	s_barrier
	s_andn2_b64 vcc, exec, s[4:5]
	s_mov_b64 s[10:11], -1
	s_mov_b64 s[4:5], 0
	s_movk_i32 s41, 0x100
	s_cbranch_vccz .LBB0_1021
	s_and_b64 vcc, exec, s[8:9]
	s_cbranch_vccz .LBB0_1024
	s_barrier

; #define PG8_STAGE(bufoff, goff, voff) do { _Pragma("unroll") for (int _i = 0; _i < 2; ++_i) \
;         __builtin_amdgcn_raw_ptr_buffer_load_lds(rsrc, (PG8_LAS void*)(lds + (bufoff) + ldsw + _i * 8192), 16, (int)(voff), (int)((goff) + _i * p1##voff), 0, 0); } while (0)
; #define PG8_LDA(dst, b, h) do { _Pragma("unroll") for (int m = 0; m < 4; ++m) dst[m] = PG8_LD8(lds + PG8_SA(b, h) + aoff + m * 2048); } while (0)
; #define PG8_LDB(dst, b, h) do { _Pragma("unroll") for (int n = 0; n < 2; ++n) dst[n] = PG8_LD8(lds + PG8_SB(b, h) + boff + n * 2048); } while (0)
; #define PG8_WAIT_V(n) asm volatile("s_waitcnt vmcnt(" #n ")" ::: "memory")
; #define PG8_WAIT_L(n) asm volatile("s_waitcnt lgkmcnt(" #n ")" ::: "memory")
; #define PG8_BAR __builtin_amdgcn_s_barrier()
; #define PG8_SCHED __builtin_amdgcn_sched_barrier(0)
; template <class Epi, class Sched, bool ALIGN_EPI, bool F8 = false, int F8SC = F8_SCALES>
; __device__ __forceinline__ void gemm_phase(PG8_LAS unsigned char* lds, const __amdgpu_buffer_rsrc_t rsrc, const int lda, const int ldb, const int K, const Sched& S, const Epi& E) {
;     ...
;             PG8_LDB(B0, 0, 0); PG8_LDB(B1, 0, 1); PG8_SCHED; PG8_LDA(At, 0, 0); PG8_STAGE(PG8_SA(1, 1), a1 + hsA, voffA);
;             PG8_WAIT_V(8); PG8_WAIT_L(0); PG8_BAR; PG8_MMA(0, 0, At, B0); PG8_MMA(0, 1, At, B1); PG8_BAR; PG8_SCHED;
;             PG8_LDA(At, 0, 1); PG8_STAGE(PG8_SB(0, 0), b2, voffB); PG8_STAGE(PG8_SB(0, 1), b2 + hsB, voffB); PG8_STAGE(PG8_SA(0, 0), a2, voffA);
;             PG8_WAIT_V(8); PG8_WAIT_L(0); PG8_BAR; PG8_MMA(1, 0, At, B0); PG8_MMA(1, 1, At, B1); PG8_BAR; PG8_SCHED;
.LBB0_1289:
	v_add_u32_e32 v2, 0x10000, v181
	ds_read_b128 v[150:153], v2
	ds_read_b128 v[154:157], v2 offset:1024
	ds_read_b128 v[158:161], v2 offset:2048
	ds_read_b128 v[162:165], v2 offset:3072
	v_add_u32_e32 v2, 0x14000, v181
	ds_read_b128 v[184:187], v2
	ds_read_b128 v[188:191], v2 offset:1024
	ds_read_b128 v[192:195], v2 offset:2048
	ds_read_b128 v[196:199], v2 offset:3072
	s_add_i32 s25, s6, 0xfffd0080
	s_cmp_eq_u32 s24, 4
	s_cselect_b32 s25, s52, s25
	s_cselect_b32 s53, s51, s7
	s_add_i32 s27, s25, 0x80
	s_add_i32 s54, s6, 0xffff0000
	s_mov_b32 s80, s96
	s_mov_b32 m0, s42
	ds_read_b128 v[200:203], v182
	ds_read_b128 v[204:207], v182 offset:1024
	ds_read_b128 v[208:211], v182 offset:2048
	ds_read_b128 v[212:215], v182 offset:3072
	ds_read_b128 v[216:219], v182 offset:4096
	ds_read_b128 v[220:223], v182 offset:5120
	ds_read_b128 v[224:227], v182 offset:6144
	ds_read_b128 v[228:231], v182 offset:7168
	buffer_load_dwordx4 v1, s[80:83], s54 offen lds
	s_mov_b32 m0, s43
	s_nop 0
	buffer_load_dwordx4 v1, s[80:83], s6 offen lds
	s_waitcnt vmcnt(8)
	s_waitcnt lgkmcnt(0)
	s_barrier
	s_waitcnt lgkmcnt(4)
	v_mfma_scale_f32_16x16x128_f8f6f4 v[122:125], v[150:157], v[208:215], v[122:125], v183, v183 op_sel:[0,1,0] op_sel_hi:[0,0,0]
	s_waitcnt lgkmcnt(2)
	v_mfma_scale_f32_16x16x128_f8f6f4 v[134:137], v[150:157], v[216:223], v[134:137], v183, v183 op_sel:[0,1,0] op_sel_hi:[0,0,0]
	s_waitcnt lgkmcnt(0)
	v_mfma_scale_f32_16x16x128_f8f6f4 v[118:121], v[150:157], v[224:231], v[118:121], v183, v183 op_sel:[0,1,0] op_sel_hi:[0,0,0]
	v_mfma_scale_f32_16x16x128_f8f6f4 v[94:97], v[150:157], v[200:207], v[106:109], v183, v183 op_sel:[0,1,0] op_sel_hi:[0,0,0]
	v_mfma_scale_f32_16x16x128_f8f6f4 v[114:117], v[158:165], v[200:207], v[66:69], v183, v183 op_sel:[0,1,0] op_sel_hi:[0,0,0]
	v_mfma_scale_f32_16x16x128_f8f6f4 v[130:133], v[158:165], v[208:215], v[62:65], v183, v183 op_sel:[0,1,0] op_sel_hi:[0,0,0]
	v_mfma_scale_f32_16x16x128_f8f6f4 v[142:145], v[158:165], v[216:223], v[58:61], v183, v183 op_sel:[0,1,0] op_sel_hi:[0,0,0]
	v_mfma_scale_f32_16x16x128_f8f6f4 v[166:169], v[158:165], v[224:231], v[54:57], v183, v183 op_sel:[0,1,0] op_sel_hi:[0,0,0]
	v_mfma_scale_f32_16x16x128_f8f6f4 v[146:149], v[184:191], v[200:207], v[146:149], v183, v183 op_sel:[0,1,0] op_sel_hi:[0,0,0]
	v_mfma_scale_f32_16x16x128_f8f6f4 v[138:141], v[184:191], v[208:215], v[138:141], v183, v183 op_sel:[0,1,0] op_sel_hi:[0,0,0]
	v_mfma_scale_f32_16x16x128_f8f6f4 v[126:129], v[184:191], v[216:223], v[126:129], v183, v183 op_sel:[0,1,0] op_sel_hi:[0,0,0]
	v_mfma_scale_f32_16x16x128_f8f6f4 v[110:113], v[184:191], v[224:231], v[110:113], v183, v183 op_sel:[0,1,0] op_sel_hi:[0,0,0]
	v_mfma_scale_f32_16x16x128_f8f6f4 v[174:177], v[192:199], v[200:207], v[50:53], v183, v183 op_sel:[0,1,0] op_sel_hi:[0,0,0]
	v_mfma_scale_f32_16x16x128_f8f6f4 v[200:203], v[192:199], v[208:215], v[46:49], v183, v183 op_sel:[0,1,0] op_sel_hi:[0,0,0]
	v_mfma_scale_f32_16x16x128_f8f6f4 v[204:207], v[192:199], v[216:223], v[42:45], v183, v183 op_sel:[0,1,0] op_sel_hi:[0,0,0]
	v_mfma_scale_f32_16x16x128_f8f6f4 v[208:211], v[192:199], v[224:231], v[38:41], v183, v183 op_sel:[0,1,0] op_sel_hi:[0,0,0]
	s_barrier
	s_mov_b32 m0, s28
	s_nop 3
	ds_read_b128 v[38:41], v182 offset:16384
	ds_read_b128 v[42:45], v182 offset:17408
	ds_read_b128 v[46:49], v182 offset:18432
	ds_read_b128 v[50:53], v182 offset:19456
	ds_read_b128 v[54:57], v182 offset:20480
	ds_read_b128 v[58:61], v182 offset:21504
	ds_read_b128 v[62:65], v182 offset:22528
	ds_read_b128 v[66:69], v182 offset:23552
	buffer_load_dwordx4 v180, s[80:83], s53 offen lds
	s_add_i32 s54, s53, 0x10000
	s_mov_b32 m0, s29
	s_nop 0
	buffer_load_dwordx4 v180, s[80:83], s54 offen lds
	s_add_i32 s54, s53, 0x20000
	s_mov_b32 m0, s30
	s_nop 0
	buffer_load_dwordx4 v180, s[80:83], s54 offen lds
	s_add_i32 s54, s53, 0x30000
	s_mov_b32 m0, s31
	s_nop 0
	buffer_load_dwordx4 v180, s[80:83], s54 offen lds
	s_mov_b32 m0, s15
	s_add_i32 s54, s25, 0x10000
	buffer_load_dwordx4 v1, s[80:83], s25 offen lds
	s_mov_b32 m0, s33
	s_nop 0
	buffer_load_dwordx4 v1, s[80:83], s54 offen lds
	s_waitcnt vmcnt(8)
	s_waitcnt lgkmcnt(0)
	s_barrier
	s_waitcnt lgkmcnt(6)
	v_mfma_scale_f32_16x16x128_f8f6f4 v[102:105], v[150:157], v[38:45], v[102:105], v183, v183 op_sel:[0,1,0] op_sel_hi:[0,0,0]
	s_waitcnt lgkmcnt(4)
	v_mfma_scale_f32_16x16x128_f8f6f4 v[90:93], v[150:157], v[46:53], v[90:93], v183, v183 op_sel:[0,1,0] op_sel_hi:[0,0,0]
	s_waitcnt lgkmcnt(2)
	v_mfma_scale_f32_16x16x128_f8f6f4 v[82:85], v[150:157], v[54:61], v[82:85], v183, v183 op_sel:[0,1,0] op_sel_hi:[0,0,0]
	v_mfma_scale_f32_16x16x128_f8f6f4 v[216:219], v[158:165], v[38:45], v[34:37], v183, v183 op_sel:[0,1,0] op_sel_hi:[0,0,0]
	v_mfma_scale_f32_16x16x128_f8f6f4 v[220:223], v[158:165], v[46:53], v[30:33], v183, v183 op_sel:[0,1,0] op_sel_hi:[0,0,0]
	v_mfma_scale_f32_16x16x128_f8f6f4 v[224:227], v[158:165], v[54:61], v[26:29], v183, v183 op_sel:[0,1,0] op_sel_hi:[0,0,0]
	s_waitcnt lgkmcnt(0)
	v_mfma_scale_f32_16x16x128_f8f6f4 v[228:231], v[150:157], v[62:69], v[74:77], v183, v183 op_sel:[0,1,0] op_sel_hi:[0,0,0]
	v_mfma_scale_f32_16x16x128_f8f6f4 v[232:235], v[158:165], v[62:69], v[22:25], v183, v183 op_sel:[0,1,0] op_sel_hi:[0,0,0]
	v_mfma_scale_f32_16x16x128_f8f6f4 v[98:101], v[184:191], v[38:45], v[98:101], v183, v183 op_sel:[0,1,0] op_sel_hi:[0,0,0]
	v_mfma_scale_f32_16x16x128_f8f6f4 v[86:89], v[184:191], v[46:53], v[86:89], v183, v183 op_sel:[0,1,0] op_sel_hi:[0,0,0]
	v_mfma_scale_f32_16x16x128_f8f6f4 v[78:81], v[184:191], v[54:61], v[78:81], v183, v183 op_sel:[0,1,0] op_sel_hi:[0,0,0]
	v_mfma_scale_f32_16x16x128_f8f6f4 v[236:239], v[192:199], v[38:45], v[18:21], v183, v183 op_sel:[0,1,0] op_sel_hi:[0,0,0]
	v_mfma_scale_f32_16x16x128_f8f6f4 v[240:243], v[192:199], v[46:53], v[14:17], v183, v183 op_sel:[0,1,0] op_sel_hi:[0,0,0]
	v_mfma_scale_f32_16x16x128_f8f6f4 v[244:247], v[192:199], v[54:61], v[10:13], v183, v183 op_sel:[0,1,0] op_sel_hi:[0,0,0]
	v_mfma_scale_f32_16x16x128_f8f6f4 v[248:251], v[184:191], v[62:69], v[70:73], v183, v183 op_sel:[0,1,0] op_sel_hi:[0,0,0]
	v_mfma_scale_f32_16x16x128_f8f6f4 v[170:173], v[192:199], v[62:69], v[6:9], v183, v183 op_sel:[0,1,0] op_sel_hi:[0,0,0]
	s_barrier
; #define PG8_STAGE(bufoff, goff, voff) do { _Pragma("unroll") for (int _i = 0; _i < 2; ++_i) \
;         __builtin_amdgcn_raw_ptr_buffer_load_lds(rsrc, (PG8_LAS void*)(lds + (bufoff) + ldsw + _i * 8192), 16, (int)(voff), (int)((goff) + _i * p1##voff), 0, 0); } while (0)
; #define PG8_LDA(dst, b, h) do { _Pragma("unroll") for (int m = 0; m < 4; ++m) dst[m] = PG8_LD8(lds + PG8_SA(b, h) + aoff + m * 2048); } while (0)
; #define PG8_LDB(dst, b, h) do { _Pragma("unroll") for (int n = 0; n < 2; ++n) dst[n] = PG8_LD8(lds + PG8_SB(b, h) + boff + n * 2048); } while (0)
; #define PG8_WAIT_V(n) asm volatile("s_waitcnt vmcnt(" #n ")" ::: "memory")
; #define PG8_WAIT_L(n) asm volatile("s_waitcnt lgkmcnt(" #n ")" ::: "memory")
; #define PG8_BAR __builtin_amdgcn_s_barrier()
; #define PG8_SCHED __builtin_amdgcn_sched_barrier(0)
; template <class Epi, class Sched, bool ALIGN_EPI, bool F8 = false, int F8SC = F8_SCALES>
; __device__ __forceinline__ void gemm_phase(PG8_LAS unsigned char* lds, const __amdgpu_buffer_rsrc_t rsrc, const int lda, const int ldb, const int K, const Sched& S, const Epi& E) {
;     ...
;             PG8_LDB(B0, 1, 0); PG8_LDB(B1, 1, 1); PG8_SCHED; PG8_LDA(At, 1, 0); PG8_STAGE(PG8_SA(0, 1), a2 + hsA, voffA);
;             PG8_WAIT_V(8); PG8_WAIT_L(0); PG8_BAR; PG8_MMA(0, 0, At, B0); PG8_MMA(0, 1, At, B1); PG8_BAR; PG8_SCHED;
;             PG8_LDA(At, 1, 1); PG8_STAGE(PG8_SB(1, 0), b3, voffB); PG8_STAGE(PG8_SB(1, 1), b3 + hsB, voffB); PG8_STAGE(PG8_SA(1, 0), a3, voffA);
;             PG8_WAIT_V(8); PG8_WAIT_L(0); PG8_BAR; PG8_MMA(1, 0, At, B0); PG8_MMA(1, 1, At, B1); PG8_BAR; PG8_SCHED;
;         }
	v_add_u32_e32 v2, 0x18000, v181
	s_nop 3
	ds_read_b128 v[4:7], v2
	ds_read_b128 v[8:11], v2 offset:1024
	ds_read_b128 v[12:15], v2 offset:2048
	ds_read_b128 v[16:19], v2 offset:3072
	v_add_u32_e32 v2, 0x1c000, v181
	ds_read_b128 v[150:153], v2
	ds_read_b128 v[154:157], v2 offset:1024
	ds_read_b128 v[158:161], v2 offset:2048
	ds_read_b128 v[162:165], v2 offset:3072
	s_mov_b32 m0, s34
	s_add_i32 s54, s25, 0x20000
	ds_read_b128 v[20:23], v182 offset:32768
	ds_read_b128 v[24:27], v182 offset:33792
	ds_read_b128 v[28:31], v182 offset:34816
	ds_read_b128 v[32:35], v182 offset:35840
	ds_read_b128 v[36:39], v182 offset:36864
	ds_read_b128 v[40:43], v182 offset:37888
	ds_read_b128 v[70:73], v182 offset:38912
	ds_read_b128 v[74:77], v182 offset:39936
	buffer_load_dwordx4 v1, s[80:83], s54 offen lds
	s_add_i32 s54, s25, 0x30000
	s_mov_b32 m0, s35
	s_nop 0
	buffer_load_dwordx4 v1, s[80:83], s54 offen lds
	s_waitcnt vmcnt(8)
	s_waitcnt lgkmcnt(0)
	s_barrier
	s_waitcnt lgkmcnt(6)
	v_mfma_scale_f32_16x16x128_f8f6f4 v[106:109], v[4:11], v[20:27], v[94:97], v183, v183 op_sel:[0,1,0] op_sel_hi:[0,0,0]
	v_mfma_scale_f32_16x16x128_f8f6f4 v[66:69], v[12:19], v[20:27], v[114:117], v183, v183 op_sel:[0,1,0] op_sel_hi:[0,0,0]
	s_waitcnt lgkmcnt(4)
	v_mfma_scale_f32_16x16x128_f8f6f4 v[122:125], v[4:11], v[28:35], v[122:125], v183, v183 op_sel:[0,1,0] op_sel_hi:[0,0,0]
	v_mfma_scale_f32_16x16x128_f8f6f4 v[62:65], v[12:19], v[28:35], v[130:133], v183, v183 op_sel:[0,1,0] op_sel_hi:[0,0,0]
	s_waitcnt lgkmcnt(2)
	v_mfma_scale_f32_16x16x128_f8f6f4 v[134:137], v[4:11], v[36:43], v[134:137], v183, v183 op_sel:[0,1,0] op_sel_hi:[0,0,0]
	v_mfma_scale_f32_16x16x128_f8f6f4 v[58:61], v[12:19], v[36:43], v[142:145], v183, v183 op_sel:[0,1,0] op_sel_hi:[0,0,0]
	s_waitcnt lgkmcnt(0)
	v_mfma_scale_f32_16x16x128_f8f6f4 v[118:121], v[4:11], v[70:77], v[118:121], v183, v183 op_sel:[0,1,0] op_sel_hi:[0,0,0]
	v_mfma_scale_f32_16x16x128_f8f6f4 v[54:57], v[12:19], v[70:77], v[166:169], v183, v183 op_sel:[0,1,0] op_sel_hi:[0,0,0]
	v_mfma_scale_f32_16x16x128_f8f6f4 v[146:149], v[150:157], v[20:27], v[146:149], v183, v183 op_sel:[0,1,0] op_sel_hi:[0,0,0]
	v_mfma_scale_f32_16x16x128_f8f6f4 v[50:53], v[158:165], v[20:27], v[174:177], v183, v183 op_sel:[0,1,0] op_sel_hi:[0,0,0]
	v_mfma_scale_f32_16x16x128_f8f6f4 v[138:141], v[150:157], v[28:35], v[138:141], v183, v183 op_sel:[0,1,0] op_sel_hi:[0,0,0]
	v_mfma_scale_f32_16x16x128_f8f6f4 v[46:49], v[158:165], v[28:35], v[200:203], v183, v183 op_sel:[0,1,0] op_sel_hi:[0,0,0]
	v_mfma_scale_f32_16x16x128_f8f6f4 v[126:129], v[150:157], v[36:43], v[126:129], v183, v183 op_sel:[0,1,0] op_sel_hi:[0,0,0]
	v_mfma_scale_f32_16x16x128_f8f6f4 v[42:45], v[158:165], v[36:43], v[204:207], v183, v183 op_sel:[0,1,0] op_sel_hi:[0,0,0]
	v_mfma_scale_f32_16x16x128_f8f6f4 v[110:113], v[150:157], v[70:77], v[110:113], v183, v183 op_sel:[0,1,0] op_sel_hi:[0,0,0]
	v_mfma_scale_f32_16x16x128_f8f6f4 v[38:41], v[158:165], v[70:77], v[208:211], v183, v183 op_sel:[0,1,0] op_sel_hi:[0,0,0]
	s_barrier
	s_mov_b32 m0, s36
	s_add_i32 s54, s53, 0x80
	ds_read_b128 v[184:187], v182 offset:49152
	ds_read_b128 v[188:191], v182 offset:50176
	ds_read_b128 v[192:195], v182 offset:51200
	ds_read_b128 v[196:199], v182 offset:52224
	ds_read_b128 v[200:203], v182 offset:53248
	ds_read_b128 v[204:207], v182 offset:54272
	ds_read_b128 v[208:211], v182 offset:55296
	ds_read_b128 v[212:215], v182 offset:56320
	buffer_load_dwordx4 v180, s[80:83], s54 offen lds
	s_add_i32 s54, s53, 0x10080
	s_mov_b32 m0, s37
	s_add_i32 s25, s25, 0x10080
	buffer_load_dwordx4 v180, s[80:83], s54 offen lds
	s_add_i32 s54, s53, 0x20080
	s_mov_b32 m0, s40
	s_add_i32 s53, s53, 0x30080
	buffer_load_dwordx4 v180, s[80:83], s54 offen lds
	s_mov_b32 m0, s41
	s_nop 0
	buffer_load_dwordx4 v180, s[80:83], s53 offen lds
	s_mov_b32 m0, s38
	s_nop 0
	buffer_load_dwordx4 v1, s[80:83], s27 offen lds
	s_mov_b32 m0, s39
	s_nop 0
	buffer_load_dwordx4 v1, s[80:83], s25 offen lds
	s_waitcnt vmcnt(8)
	s_waitcnt lgkmcnt(0)
	s_barrier
	s_waitcnt lgkmcnt(6)
	v_mfma_scale_f32_16x16x128_f8f6f4 v[102:105], v[4:11], v[184:191], v[102:105], v183, v183 op_sel:[0,1,0] op_sel_hi:[0,0,0]
	v_mfma_scale_f32_16x16x128_f8f6f4 v[34:37], v[12:19], v[184:191], v[216:219], v183, v183 op_sel:[0,1,0] op_sel_hi:[0,0,0]
	s_waitcnt lgkmcnt(4)
	v_mfma_scale_f32_16x16x128_f8f6f4 v[90:93], v[4:11], v[192:199], v[90:93], v183, v183 op_sel:[0,1,0] op_sel_hi:[0,0,0]
	v_mfma_scale_f32_16x16x128_f8f6f4 v[30:33], v[12:19], v[192:199], v[220:223], v183, v183 op_sel:[0,1,0] op_sel_hi:[0,0,0]
	s_waitcnt lgkmcnt(2)
	v_mfma_scale_f32_16x16x128_f8f6f4 v[82:85], v[4:11], v[200:207], v[82:85], v183, v183 op_sel:[0,1,0] op_sel_hi:[0,0,0]
	v_mfma_scale_f32_16x16x128_f8f6f4 v[26:29], v[12:19], v[200:207], v[224:227], v183, v183 op_sel:[0,1,0] op_sel_hi:[0,0,0]
	s_waitcnt lgkmcnt(0)
	v_mfma_scale_f32_16x16x128_f8f6f4 v[74:77], v[4:11], v[208:215], v[228:231], v183, v183 op_sel:[0,1,0] op_sel_hi:[0,0,0]
	v_mfma_scale_f32_16x16x128_f8f6f4 v[22:25], v[12:19], v[208:215], v[232:235], v183, v183 op_sel:[0,1,0] op_sel_hi:[0,0,0]
	v_mfma_scale_f32_16x16x128_f8f6f4 v[98:101], v[150:157], v[184:191], v[98:101], v183, v183 op_sel:[0,1,0] op_sel_hi:[0,0,0]
	v_mfma_scale_f32_16x16x128_f8f6f4 v[18:21], v[158:165], v[184:191], v[236:239], v183, v183 op_sel:[0,1,0] op_sel_hi:[0,0,0]
	v_mfma_scale_f32_16x16x128_f8f6f4 v[86:89], v[150:157], v[192:199], v[86:89], v183, v183 op_sel:[0,1,0] op_sel_hi:[0,0,0]
	v_mfma_scale_f32_16x16x128_f8f6f4 v[14:17], v[158:165], v[192:199], v[240:243], v183, v183 op_sel:[0,1,0] op_sel_hi:[0,0,0]
	v_mfma_scale_f32_16x16x128_f8f6f4 v[78:81], v[150:157], v[200:207], v[78:81], v183, v183 op_sel:[0,1,0] op_sel_hi:[0,0,0]
	v_mfma_scale_f32_16x16x128_f8f6f4 v[10:13], v[158:165], v[200:207], v[244:247], v183, v183 op_sel:[0,1,0] op_sel_hi:[0,0,0]
	v_mfma_scale_f32_16x16x128_f8f6f4 v[70:73], v[150:157], v[208:215], v[248:251], v183, v183 op_sel:[0,1,0] op_sel_hi:[0,0,0]
	v_mfma_scale_f32_16x16x128_f8f6f4 v[6:9], v[158:165], v[208:215], v[170:173], v183, v183 op_sel:[0,1,0] op_sel_hi:[0,0,0]
	s_barrier
	s_add_i32 s24, s24, 2
	s_addk_i32 s6, 0x100
	s_addk_i32 s7, 0x100
	s_cmp_gt_u32 s24, 5
	s_cbranch_scc0 .LBB0_1289
	s_and_b64 vcc, exec, s[12:13]
	s_cbranch_vccz .LBB0_1292
	s_barrier

; #define PG8_STAGE(bufoff, goff, voff) do { _Pragma("unroll") for (int _i = 0; _i < 2; ++_i) \
;         __builtin_amdgcn_raw_ptr_buffer_load_lds(rsrc, (PG8_LAS void*)(lds + (bufoff) + ldsw + _i * 8192), 16, (int)(voff), (int)((goff) + _i * p1##voff), 0, 0); } while (0)
; #define PG8_LDA(dst, b, h) do { _Pragma("unroll") for (int m = 0; m < 4; ++m) dst[m] = PG8_LD8(lds + PG8_SA(b, h) + aoff + m * 2048); } while (0)
; #define PG8_LDB(dst, b, h) do { _Pragma("unroll") for (int n = 0; n < 2; ++n) dst[n] = PG8_LD8(lds + PG8_SB(b, h) + boff + n * 2048); } while (0)
; #define PG8_WAIT_V(n) asm volatile("s_waitcnt vmcnt(" #n ")" ::: "memory")
; #define PG8_WAIT_L(n) asm volatile("s_waitcnt lgkmcnt(" #n ")" ::: "memory")
; #define PG8_BAR __builtin_amdgcn_s_barrier()
; #define PG8_SCHED __builtin_amdgcn_sched_barrier(0)
; template <class Epi, class Sched, bool ALIGN_EPI, bool F8 = false, int F8SC = F8_SCALES>
; __device__ __forceinline__ void gemm_phase(PG8_LAS unsigned char* lds, const __amdgpu_buffer_rsrc_t rsrc, const int lda, const int ldb, const int K, const Sched& S, const Epi& E) {
;     ...
;             PG8_LDB(B0, 0, 0); PG8_LDB(B1, 0, 1); PG8_SCHED; PG8_LDA(At, 0, 0); PG8_STAGE(PG8_SA(1, 1), a1 + hsA, voffA);
;             PG8_WAIT_V(8); PG8_WAIT_L(0); PG8_BAR; PG8_MMA(0, 0, At, B0); PG8_MMA(0, 1, At, B1); PG8_BAR; PG8_SCHED;
;             PG8_LDA(At, 0, 1); PG8_STAGE(PG8_SB(0, 0), b2, voffB); PG8_STAGE(PG8_SB(0, 1), b2 + hsB, voffB); PG8_STAGE(PG8_SA(0, 0), a2, voffA);
;             PG8_WAIT_V(8); PG8_WAIT_L(0); PG8_BAR; PG8_MMA(1, 0, At, B0); PG8_MMA(1, 1, At, B1); PG8_BAR; PG8_SCHED;
.LBB0_1448:
	ds_read_b128 v[142:145], v135
	ds_read_b128 v[146:149], v135 offset:1024
	ds_read_b128 v[150:153], v135 offset:2048
	ds_read_b128 v[154:157], v135 offset:3072
	ds_read_b128 v[158:161], v136
	ds_read_b128 v[162:165], v136 offset:1024
	ds_read_b128 v[166:169], v136 offset:2048
	ds_read_b128 v[170:173], v136 offset:3072
	s_add_i32 s47, s44, 0xfffa0080
	s_cmp_eq_u32 s46, 12
	s_cselect_b32 s47, s4, s47
	s_cselect_b32 s49, s5, s45
	s_add_i32 s48, s47, 0x80
	s_add_i32 s50, s44, 0xfffe0000
	s_mov_b32 s80, s96
	s_mov_b32 m0, s33
	ds_read_b128 v[174:177], v137
	ds_read_b128 v[178:181], v137 offset:1024
	ds_read_b128 v[182:185], v137 offset:2048
	ds_read_b128 v[186:189], v137 offset:3072
	ds_read_b128 v[190:193], v137 offset:4096
	ds_read_b128 v[194:197], v137 offset:5120
	ds_read_b128 v[198:201], v137 offset:6144
	ds_read_b128 v[202:205], v137 offset:7168
	buffer_load_dwordx4 v1, s[80:83], s50 offen lds
	s_mov_b32 m0, s34
	s_nop 0
	buffer_load_dwordx4 v1, s[80:83], s44 offen lds
	s_waitcnt vmcnt(8)
	s_waitcnt lgkmcnt(0)
	s_barrier
	s_waitcnt lgkmcnt(6)
	v_mfma_scale_f32_16x16x128_f8f6f4 v[126:129], v[142:149], v[174:181], v[126:129], v138, v138 op_sel:[0,1,0] op_sel_hi:[0,0,0]
	v_mfma_scale_f32_16x16x128_f8f6f4 v[122:125], v[150:157], v[174:181], v[122:125], v138, v138 op_sel:[0,1,0] op_sel_hi:[0,0,0]
	s_waitcnt lgkmcnt(4)
	v_mfma_scale_f32_16x16x128_f8f6f4 v[118:121], v[142:149], v[182:189], v[118:121], v138, v138 op_sel:[0,1,0] op_sel_hi:[0,0,0]
	v_mfma_scale_f32_16x16x128_f8f6f4 v[114:117], v[150:157], v[182:189], v[114:117], v138, v138 op_sel:[0,1,0] op_sel_hi:[0,0,0]
	s_waitcnt lgkmcnt(2)
	v_mfma_scale_f32_16x16x128_f8f6f4 v[102:105], v[142:149], v[190:197], v[102:105], v138, v138 op_sel:[0,1,0] op_sel_hi:[0,0,0]
	v_mfma_scale_f32_16x16x128_f8f6f4 v[98:101], v[150:157], v[190:197], v[98:101], v138, v138 op_sel:[0,1,0] op_sel_hi:[0,0,0]
	s_waitcnt lgkmcnt(0)
	v_mfma_scale_f32_16x16x128_f8f6f4 v[206:209], v[142:149], v[198:205], v[86:89], v138, v138 op_sel:[0,1,0] op_sel_hi:[0,0,0]
	v_mfma_scale_f32_16x16x128_f8f6f4 v[210:213], v[150:157], v[198:205], v[82:85], v138, v138 op_sel:[0,1,0] op_sel_hi:[0,0,0]
	v_mfma_scale_f32_16x16x128_f8f6f4 v[110:113], v[158:165], v[174:181], v[110:113], v138, v138 op_sel:[0,1,0] op_sel_hi:[0,0,0]
	v_mfma_scale_f32_16x16x128_f8f6f4 v[106:109], v[166:173], v[174:181], v[106:109], v138, v138 op_sel:[0,1,0] op_sel_hi:[0,0,0]
	v_mfma_scale_f32_16x16x128_f8f6f4 v[174:177], v[158:165], v[182:189], v[94:97], v138, v138 op_sel:[0,1,0] op_sel_hi:[0,0,0]
	v_mfma_scale_f32_16x16x128_f8f6f4 v[178:181], v[166:173], v[182:189], v[90:93], v138, v138 op_sel:[0,1,0] op_sel_hi:[0,0,0]
	v_mfma_scale_f32_16x16x128_f8f6f4 v[182:185], v[158:165], v[190:197], v[78:81], v138, v138 op_sel:[0,1,0] op_sel_hi:[0,0,0]
	v_mfma_scale_f32_16x16x128_f8f6f4 v[186:189], v[166:173], v[190:197], v[74:77], v138, v138 op_sel:[0,1,0] op_sel_hi:[0,0,0]
	v_mfma_scale_f32_16x16x128_f8f6f4 v[190:193], v[158:165], v[198:205], v[70:73], v138, v138 op_sel:[0,1,0] op_sel_hi:[0,0,0]
	v_mfma_scale_f32_16x16x128_f8f6f4 v[194:197], v[166:173], v[198:205], v[66:69], v138, v138 op_sel:[0,1,0] op_sel_hi:[0,0,0]
	s_barrier
	s_mov_b32 m0, s18
	s_nop 3
	ds_read_b128 v[66:69], v137 offset:16384
	ds_read_b128 v[70:73], v137 offset:17408
	ds_read_b128 v[74:77], v137 offset:18432
	ds_read_b128 v[78:81], v137 offset:19456
	ds_read_b128 v[82:85], v137 offset:20480
	ds_read_b128 v[86:89], v137 offset:21504
	ds_read_b128 v[90:93], v137 offset:22528
	ds_read_b128 v[94:97], v137 offset:23552
	buffer_load_dwordx4 v134, s[80:83], s49 offen lds
	s_add_i32 s50, s49, 0x20000
	s_mov_b32 m0, s19
	s_nop 0
	buffer_load_dwordx4 v134, s[80:83], s50 offen lds
	s_add_i32 s50, s49, 0x40000
	s_mov_b32 m0, s20
	s_nop 0
	buffer_load_dwordx4 v134, s[80:83], s50 offen lds
	s_add_i32 s50, s49, 0x60000
	s_mov_b32 m0, s21
	s_nop 0
	buffer_load_dwordx4 v134, s[80:83], s50 offen lds
	s_mov_b32 m0, s9
	s_add_i32 s50, s47, 0x20000
	buffer_load_dwordx4 v1, s[80:83], s47 offen lds
	s_mov_b32 m0, s22
	s_nop 0
	buffer_load_dwordx4 v1, s[80:83], s50 offen lds
	s_waitcnt vmcnt(8)
	s_waitcnt lgkmcnt(0)
	s_barrier
	s_waitcnt lgkmcnt(6)
	v_mfma_scale_f32_16x16x128_f8f6f4 v[62:65], v[142:149], v[66:73], v[62:65], v138, v138 op_sel:[0,1,0] op_sel_hi:[0,0,0]
	v_mfma_scale_f32_16x16x128_f8f6f4 v[58:61], v[150:157], v[66:73], v[58:61], v138, v138 op_sel:[0,1,0] op_sel_hi:[0,0,0]
	s_waitcnt lgkmcnt(4)
	v_mfma_scale_f32_16x16x128_f8f6f4 v[54:57], v[142:149], v[74:81], v[54:57], v138, v138 op_sel:[0,1,0] op_sel_hi:[0,0,0]
	v_mfma_scale_f32_16x16x128_f8f6f4 v[50:53], v[150:157], v[74:81], v[50:53], v138, v138 op_sel:[0,1,0] op_sel_hi:[0,0,0]
	s_waitcnt lgkmcnt(2)
	v_mfma_scale_f32_16x16x128_f8f6f4 v[198:201], v[142:149], v[82:89], v[38:41], v138, v138 op_sel:[0,1,0] op_sel_hi:[0,0,0]
	v_mfma_scale_f32_16x16x128_f8f6f4 v[202:205], v[150:157], v[82:89], v[34:37], v138, v138 op_sel:[0,1,0] op_sel_hi:[0,0,0]
	s_waitcnt lgkmcnt(0)
	v_mfma_scale_f32_16x16x128_f8f6f4 v[214:217], v[142:149], v[90:97], v[22:25], v138, v138 op_sel:[0,1,0] op_sel_hi:[0,0,0]
	v_mfma_scale_f32_16x16x128_f8f6f4 v[218:221], v[150:157], v[90:97], v[18:21], v138, v138 op_sel:[0,1,0] op_sel_hi:[0,0,0]
	v_mfma_scale_f32_16x16x128_f8f6f4 v[222:225], v[158:165], v[66:73], v[46:49], v138, v138 op_sel:[0,1,0] op_sel_hi:[0,0,0]
	v_mfma_scale_f32_16x16x128_f8f6f4 v[226:229], v[166:173], v[66:73], v[42:45], v138, v138 op_sel:[0,1,0] op_sel_hi:[0,0,0]
	v_mfma_scale_f32_16x16x128_f8f6f4 v[230:233], v[158:165], v[74:81], v[30:33], v138, v138 op_sel:[0,1,0] op_sel_hi:[0,0,0]
	v_mfma_scale_f32_16x16x128_f8f6f4 v[234:237], v[166:173], v[74:81], v[26:29], v138, v138 op_sel:[0,1,0] op_sel_hi:[0,0,0]
	v_mfma_scale_f32_16x16x128_f8f6f4 v[238:241], v[158:165], v[82:89], v[14:17], v138, v138 op_sel:[0,1,0] op_sel_hi:[0,0,0]
	v_mfma_scale_f32_16x16x128_f8f6f4 v[242:245], v[166:173], v[82:89], v[10:13], v138, v138 op_sel:[0,1,0] op_sel_hi:[0,0,0]
	v_mfma_scale_f32_16x16x128_f8f6f4 v[246:249], v[158:165], v[90:97], v[6:9], v138, v138 op_sel:[0,1,0] op_sel_hi:[0,0,0]
	v_mfma_scale_f32_16x16x128_f8f6f4 v[250:253], v[166:173], v[90:97], v[2:5], v138, v138 op_sel:[0,1,0] op_sel_hi:[0,0,0]
	s_barrier
; #define PG8_STAGE(bufoff, goff, voff) do { _Pragma("unroll") for (int _i = 0; _i < 2; ++_i) \
;         __builtin_amdgcn_raw_ptr_buffer_load_lds(rsrc, (PG8_LAS void*)(lds + (bufoff) + ldsw + _i * 8192), 16, (int)(voff), (int)((goff) + _i * p1##voff), 0, 0); } while (0)
; #define PG8_LDA(dst, b, h) do { _Pragma("unroll") for (int m = 0; m < 4; ++m) dst[m] = PG8_LD8(lds + PG8_SA(b, h) + aoff + m * 2048); } while (0)
; #define PG8_LDB(dst, b, h) do { _Pragma("unroll") for (int n = 0; n < 2; ++n) dst[n] = PG8_LD8(lds + PG8_SB(b, h) + boff + n * 2048); } while (0)
; #define PG8_WAIT_V(n) asm volatile("s_waitcnt vmcnt(" #n ")" ::: "memory")
; #define PG8_WAIT_L(n) asm volatile("s_waitcnt lgkmcnt(" #n ")" ::: "memory")
; #define PG8_BAR __builtin_amdgcn_s_barrier()
; #define PG8_SCHED __builtin_amdgcn_sched_barrier(0)
; template <class Epi, class Sched, bool ALIGN_EPI, bool F8 = false, int F8SC = F8_SCALES>
; __device__ __forceinline__ void gemm_phase(PG8_LAS unsigned char* lds, const __amdgpu_buffer_rsrc_t rsrc, const int lda, const int ldb, const int K, const Sched& S, const Epi& E) {
;     ...
;             PG8_LDB(B0, 1, 0); PG8_LDB(B1, 1, 1); PG8_SCHED; PG8_LDA(At, 1, 0); PG8_STAGE(PG8_SA(0, 1), a2 + hsA, voffA);
;             PG8_WAIT_V(8); PG8_WAIT_L(0); PG8_BAR; PG8_MMA(0, 0, At, B0); PG8_MMA(0, 1, At, B1); PG8_BAR; PG8_SCHED;
;             PG8_LDA(At, 1, 1); PG8_STAGE(PG8_SB(1, 0), b3, voffB); PG8_STAGE(PG8_SB(1, 1), b3 + hsB, voffB); PG8_STAGE(PG8_SA(1, 0), a3, voffA);
;             PG8_WAIT_V(8); PG8_WAIT_L(0); PG8_BAR; PG8_MMA(1, 0, At, B0); PG8_MMA(1, 1, At, B1); PG8_BAR; PG8_SCHED;
;         }
	s_nop 4
	ds_read_b128 v[2:5], v139
	ds_read_b128 v[6:9], v139 offset:1024
	ds_read_b128 v[10:13], v139 offset:2048
	ds_read_b128 v[14:17], v139 offset:3072
	ds_read_b128 v[142:145], v140
	ds_read_b128 v[146:149], v140 offset:1024
	ds_read_b128 v[150:153], v140 offset:2048
	ds_read_b128 v[154:157], v140 offset:3072
	s_mov_b32 m0, s23
	s_add_i32 s50, s47, 0x40000
	ds_read_b128 v[18:21], v137 offset:32768
	ds_read_b128 v[22:25], v137 offset:33792
	ds_read_b128 v[26:29], v137 offset:34816
	ds_read_b128 v[30:33], v137 offset:35840
	ds_read_b128 v[34:37], v137 offset:36864
	ds_read_b128 v[38:41], v137 offset:37888
	ds_read_b128 v[42:45], v137 offset:38912
	ds_read_b128 v[46:49], v137 offset:39936
	buffer_load_dwordx4 v1, s[80:83], s50 offen lds
	s_add_i32 s50, s47, 0x60000
	s_mov_b32 m0, s24
	s_nop 0
	buffer_load_dwordx4 v1, s[80:83], s50 offen lds
	s_waitcnt vmcnt(8)
	s_waitcnt lgkmcnt(0)
	s_barrier
	s_waitcnt lgkmcnt(6)
	v_mfma_scale_f32_16x16x128_f8f6f4 v[126:129], v[2:9], v[18:25], v[126:129], v138, v138 op_sel:[0,1,0] op_sel_hi:[0,0,0]
	v_mfma_scale_f32_16x16x128_f8f6f4 v[122:125], v[10:17], v[18:25], v[122:125], v138, v138 op_sel:[0,1,0] op_sel_hi:[0,0,0]
	s_waitcnt lgkmcnt(4)
	v_mfma_scale_f32_16x16x128_f8f6f4 v[118:121], v[2:9], v[26:33], v[118:121], v138, v138 op_sel:[0,1,0] op_sel_hi:[0,0,0]
	v_mfma_scale_f32_16x16x128_f8f6f4 v[114:117], v[10:17], v[26:33], v[114:117], v138, v138 op_sel:[0,1,0] op_sel_hi:[0,0,0]
	s_waitcnt lgkmcnt(2)
	v_mfma_scale_f32_16x16x128_f8f6f4 v[102:105], v[2:9], v[34:41], v[102:105], v138, v138 op_sel:[0,1,0] op_sel_hi:[0,0,0]
	v_mfma_scale_f32_16x16x128_f8f6f4 v[98:101], v[10:17], v[34:41], v[98:101], v138, v138 op_sel:[0,1,0] op_sel_hi:[0,0,0]
	s_waitcnt lgkmcnt(0)
	v_mfma_scale_f32_16x16x128_f8f6f4 v[86:89], v[2:9], v[42:49], v[206:209], v138, v138 op_sel:[0,1,0] op_sel_hi:[0,0,0]
	v_mfma_scale_f32_16x16x128_f8f6f4 v[82:85], v[10:17], v[42:49], v[210:213], v138, v138 op_sel:[0,1,0] op_sel_hi:[0,0,0]
	v_mfma_scale_f32_16x16x128_f8f6f4 v[110:113], v[142:149], v[18:25], v[110:113], v138, v138 op_sel:[0,1,0] op_sel_hi:[0,0,0]
	v_mfma_scale_f32_16x16x128_f8f6f4 v[106:109], v[150:157], v[18:25], v[106:109], v138, v138 op_sel:[0,1,0] op_sel_hi:[0,0,0]
	v_mfma_scale_f32_16x16x128_f8f6f4 v[94:97], v[142:149], v[26:33], v[174:177], v138, v138 op_sel:[0,1,0] op_sel_hi:[0,0,0]
	v_mfma_scale_f32_16x16x128_f8f6f4 v[90:93], v[150:157], v[26:33], v[178:181], v138, v138 op_sel:[0,1,0] op_sel_hi:[0,0,0]
	v_mfma_scale_f32_16x16x128_f8f6f4 v[78:81], v[142:149], v[34:41], v[182:185], v138, v138 op_sel:[0,1,0] op_sel_hi:[0,0,0]
	v_mfma_scale_f32_16x16x128_f8f6f4 v[74:77], v[150:157], v[34:41], v[186:189], v138, v138 op_sel:[0,1,0] op_sel_hi:[0,0,0]
	v_mfma_scale_f32_16x16x128_f8f6f4 v[70:73], v[142:149], v[42:49], v[190:193], v138, v138 op_sel:[0,1,0] op_sel_hi:[0,0,0]
	v_mfma_scale_f32_16x16x128_f8f6f4 v[66:69], v[150:157], v[42:49], v[194:197], v138, v138 op_sel:[0,1,0] op_sel_hi:[0,0,0]
	s_barrier
	s_mov_b32 m0, s26
	s_add_i32 s50, s49, 0x80
	ds_read_b128 v[26:29], v137 offset:49152
	ds_read_b128 v[30:33], v137 offset:50176
	ds_read_b128 v[158:161], v137 offset:51200
	ds_read_b128 v[162:165], v137 offset:52224
	ds_read_b128 v[166:169], v137 offset:53248
	ds_read_b128 v[170:173], v137 offset:54272
	ds_read_b128 v[174:177], v137 offset:55296
	ds_read_b128 v[178:181], v137 offset:56320
	buffer_load_dwordx4 v134, s[80:83], s50 offen lds
	s_add_i32 s50, s49, 0x20080
	s_mov_b32 m0, s27
	s_add_i32 s47, s47, 0x20080
	buffer_load_dwordx4 v134, s[80:83], s50 offen lds
	s_add_i32 s50, s49, 0x40080
	s_mov_b32 m0, s30
	s_add_i32 s49, s49, 0x60080
	buffer_load_dwordx4 v134, s[80:83], s50 offen lds
	s_mov_b32 m0, s31
	s_nop 0
	buffer_load_dwordx4 v134, s[80:83], s49 offen lds
	s_mov_b32 m0, s28
	s_nop 0
	buffer_load_dwordx4 v1, s[80:83], s48 offen lds
	s_mov_b32 m0, s29
	s_nop 0
	buffer_load_dwordx4 v1, s[80:83], s47 offen lds
	s_waitcnt vmcnt(8)
	s_waitcnt lgkmcnt(0)
	s_barrier
	s_waitcnt lgkmcnt(6)
	v_mfma_scale_f32_16x16x128_f8f6f4 v[62:65], v[2:9], v[26:33], v[62:65], v138, v138 op_sel:[0,1,0] op_sel_hi:[0,0,0]
	v_mfma_scale_f32_16x16x128_f8f6f4 v[58:61], v[10:17], v[26:33], v[58:61], v138, v138 op_sel:[0,1,0] op_sel_hi:[0,0,0]
	s_waitcnt lgkmcnt(4)
	v_mfma_scale_f32_16x16x128_f8f6f4 v[54:57], v[2:9], v[158:165], v[54:57], v138, v138 op_sel:[0,1,0] op_sel_hi:[0,0,0]
	v_mfma_scale_f32_16x16x128_f8f6f4 v[50:53], v[10:17], v[158:165], v[50:53], v138, v138 op_sel:[0,1,0] op_sel_hi:[0,0,0]
	s_waitcnt lgkmcnt(2)
	v_mfma_scale_f32_16x16x128_f8f6f4 v[38:41], v[2:9], v[166:173], v[198:201], v138, v138 op_sel:[0,1,0] op_sel_hi:[0,0,0]
	v_mfma_scale_f32_16x16x128_f8f6f4 v[34:37], v[10:17], v[166:173], v[202:205], v138, v138 op_sel:[0,1,0] op_sel_hi:[0,0,0]
	s_waitcnt lgkmcnt(0)
	v_mfma_scale_f32_16x16x128_f8f6f4 v[22:25], v[2:9], v[174:181], v[214:217], v138, v138 op_sel:[0,1,0] op_sel_hi:[0,0,0]
	v_mfma_scale_f32_16x16x128_f8f6f4 v[18:21], v[10:17], v[174:181], v[218:221], v138, v138 op_sel:[0,1,0] op_sel_hi:[0,0,0]
	v_mfma_scale_f32_16x16x128_f8f6f4 v[46:49], v[142:149], v[26:33], v[222:225], v138, v138 op_sel:[0,1,0] op_sel_hi:[0,0,0]
	v_mfma_scale_f32_16x16x128_f8f6f4 v[42:45], v[150:157], v[26:33], v[226:229], v138, v138 op_sel:[0,1,0] op_sel_hi:[0,0,0]
	v_mfma_scale_f32_16x16x128_f8f6f4 v[30:33], v[142:149], v[158:165], v[230:233], v138, v138 op_sel:[0,1,0] op_sel_hi:[0,0,0]
	v_mfma_scale_f32_16x16x128_f8f6f4 v[26:29], v[150:157], v[158:165], v[234:237], v138, v138 op_sel:[0,1,0] op_sel_hi:[0,0,0]
	v_mfma_scale_f32_16x16x128_f8f6f4 v[14:17], v[142:149], v[166:173], v[238:241], v138, v138 op_sel:[0,1,0] op_sel_hi:[0,0,0]
	v_mfma_scale_f32_16x16x128_f8f6f4 v[10:13], v[150:157], v[166:173], v[242:245], v138, v138 op_sel:[0,1,0] op_sel_hi:[0,0,0]
	v_mfma_scale_f32_16x16x128_f8f6f4 v[6:9], v[142:149], v[174:181], v[246:249], v138, v138 op_sel:[0,1,0] op_sel_hi:[0,0,0]
	v_mfma_scale_f32_16x16x128_f8f6f4 v[2:5], v[150:157], v[174:181], v[250:253], v138, v138 op_sel:[0,1,0] op_sel_hi:[0,0,0]
	s_barrier
	s_add_i32 s46, s46, 2
	s_addk_i32 s44, 0x100
	s_addk_i32 s45, 0x100
	s_cmp_gt_u32 s46, 13
	s_cbranch_scc0 .LBB0_1448
	s_and_b64 vcc, exec, s[6:7]
	s_cbranch_vccz .LBB0_1451
	s_barrier

; #define PG8_STAGE(bufoff, goff, voff) do { _Pragma("unroll") for (int _i = 0; _i < 2; ++_i) \
;         __builtin_amdgcn_raw_ptr_buffer_load_lds(rsrc, (PG8_LAS void*)(lds + (bufoff) + ldsw + _i * 8192), 16, (int)(voff), (int)((goff) + _i * p1##voff), 0, 0); } while (0)
; #define PG8_LDA(dst, b, h) do { _Pragma("unroll") for (int m = 0; m < 4; ++m) dst[m] = PG8_LD8(lds + PG8_SA(b, h) + aoff + m * 2048); } while (0)
; #define PG8_LDB(dst, b, h) do { _Pragma("unroll") for (int n = 0; n < 2; ++n) dst[n] = PG8_LD8(lds + PG8_SB(b, h) + boff + n * 2048); } while (0)
; #define PG8_WAIT_V(n) asm volatile("s_waitcnt vmcnt(" #n ")" ::: "memory")
; #define PG8_WAIT_L(n) asm volatile("s_waitcnt lgkmcnt(" #n ")" ::: "memory")
; #define PG8_BAR __builtin_amdgcn_s_barrier()
; #define PG8_SCHED __builtin_amdgcn_sched_barrier(0)
; template <class Epi, class Sched, bool ALIGN_EPI, bool F8 = false, int F8SC = F8_SCALES>
; __device__ __forceinline__ void gemm_phase(PG8_LAS unsigned char* lds, const __amdgpu_buffer_rsrc_t rsrc, const int lda, const int ldb, const int K, const Sched& S, const Epi& E) {
;     ...
;             PG8_LDB(B0, 0, 0); PG8_LDB(B1, 0, 1); PG8_SCHED; PG8_LDA(At, 0, 0); PG8_STAGE(PG8_SA(1, 1), a1 + hsA, voffA);
;             PG8_WAIT_V(8); PG8_WAIT_L(0); PG8_BAR; PG8_MMA(0, 0, At, B0); PG8_MMA(0, 1, At, B1); PG8_BAR; PG8_SCHED;
;             PG8_LDA(At, 0, 1); PG8_STAGE(PG8_SB(0, 0), b2, voffB); PG8_STAGE(PG8_SB(0, 1), b2 + hsB, voffB); PG8_STAGE(PG8_SA(0, 0), a2, voffA);
;             PG8_WAIT_V(8); PG8_WAIT_L(0); PG8_BAR; PG8_MMA(1, 0, At, B0); PG8_MMA(1, 1, At, B1); PG8_BAR; PG8_SCHED;
.LBB0_1651:
	ds_read_b128 v[102:105], v155
	ds_read_b128 v[106:109], v155 offset:1024
	ds_read_b128 v[114:117], v155 offset:2048
	ds_read_b128 v[118:121], v155 offset:3072
	ds_read_b128 v[162:165], v156
	ds_read_b128 v[166:169], v156 offset:1024
	ds_read_b128 v[170:173], v156 offset:2048
	ds_read_b128 v[174:177], v156 offset:3072
	s_add_i32 s58, s55, 0xfffa0080
	s_cmp_eq_u32 s57, 12
	s_cselect_b32 s58, s5, s58
	s_cselect_b32 s60, s4, s56
	s_add_i32 s59, s58, 0x80
	s_add_i32 s61, s55, 0xfffe0000
	s_mov_b32 s80, s96
	s_mov_b32 m0, s65
	ds_read_b128 v[178:181], v157
	ds_read_b128 v[182:185], v157 offset:1024
	ds_read_b128 v[186:189], v157 offset:2048
	ds_read_b128 v[190:193], v157 offset:3072
	ds_read_b128 v[194:197], v157 offset:4096
	ds_read_b128 v[198:201], v157 offset:5120
	ds_read_b128 v[202:205], v157 offset:6144
	ds_read_b128 v[206:209], v157 offset:7168
	buffer_load_dwordx4 v1, s[80:83], s61 offen lds
	s_mov_b32 m0, s66
	s_nop 0
	buffer_load_dwordx4 v1, s[80:83], s55 offen lds
	s_waitcnt vmcnt(8)
	s_waitcnt lgkmcnt(0)
	s_barrier
	s_waitcnt lgkmcnt(6)
	v_mfma_scale_f32_16x16x128_f8f6f4 v[142:145], v[102:109], v[178:185], v[142:145], v158, v158 op_sel:[0,1,0] op_sel_hi:[0,0,0]
	v_mfma_scale_f32_16x16x128_f8f6f4 v[138:141], v[114:121], v[178:185], v[138:141], v158, v158 op_sel:[0,1,0] op_sel_hi:[0,0,0]
	s_waitcnt lgkmcnt(4)
	v_mfma_scale_f32_16x16x128_f8f6f4 v[134:137], v[102:109], v[186:193], v[134:137], v158, v158 op_sel:[0,1,0] op_sel_hi:[0,0,0]
	v_mfma_scale_f32_16x16x128_f8f6f4 v[110:113], v[114:121], v[186:193], v[110:113], v158, v158 op_sel:[0,1,0] op_sel_hi:[0,0,0]
	s_waitcnt lgkmcnt(2)
	v_mfma_scale_f32_16x16x128_f8f6f4 v[148:151], v[102:109], v[194:201], v[94:97], v158, v158 op_sel:[0,1,0] op_sel_hi:[0,0,0]
	v_mfma_scale_f32_16x16x128_f8f6f4 v[210:213], v[114:121], v[194:201], v[86:89], v158, v158 op_sel:[0,1,0] op_sel_hi:[0,0,0]
	s_waitcnt lgkmcnt(0)
	v_mfma_scale_f32_16x16x128_f8f6f4 v[214:217], v[102:109], v[202:209], v[78:81], v158, v158 op_sel:[0,1,0] op_sel_hi:[0,0,0]
	v_mfma_scale_f32_16x16x128_f8f6f4 v[218:221], v[114:121], v[202:209], v[70:73], v158, v158 op_sel:[0,1,0] op_sel_hi:[0,0,0]
	v_mfma_scale_f32_16x16x128_f8f6f4 v[130:133], v[162:169], v[178:185], v[130:133], v158, v158 op_sel:[0,1,0] op_sel_hi:[0,0,0]
	v_mfma_scale_f32_16x16x128_f8f6f4 v[126:129], v[170:177], v[178:185], v[126:129], v158, v158 op_sel:[0,1,0] op_sel_hi:[0,0,0]
	v_mfma_scale_f32_16x16x128_f8f6f4 v[122:125], v[162:169], v[186:193], v[122:125], v158, v158 op_sel:[0,1,0] op_sel_hi:[0,0,0]
	v_mfma_scale_f32_16x16x128_f8f6f4 v[98:101], v[170:177], v[186:193], v[98:101], v158, v158 op_sel:[0,1,0] op_sel_hi:[0,0,0]
	v_mfma_scale_f32_16x16x128_f8f6f4 v[178:181], v[162:169], v[194:201], v[90:93], v158, v158 op_sel:[0,1,0] op_sel_hi:[0,0,0]
	v_mfma_scale_f32_16x16x128_f8f6f4 v[182:185], v[170:177], v[194:201], v[82:85], v158, v158 op_sel:[0,1,0] op_sel_hi:[0,0,0]
	v_mfma_scale_f32_16x16x128_f8f6f4 v[186:189], v[162:169], v[202:209], v[74:77], v158, v158 op_sel:[0,1,0] op_sel_hi:[0,0,0]
	v_mfma_scale_f32_16x16x128_f8f6f4 v[190:193], v[170:177], v[202:209], v[66:69], v158, v158 op_sel:[0,1,0] op_sel_hi:[0,0,0]
	s_barrier
	s_mov_b32 m0, s28
	s_nop 3
	ds_read_b128 v[66:69], v157 offset:16384
	ds_read_b128 v[70:73], v157 offset:17408
	ds_read_b128 v[74:77], v157 offset:18432
	ds_read_b128 v[78:81], v157 offset:19456
	ds_read_b128 v[82:85], v157 offset:20480
	ds_read_b128 v[86:89], v157 offset:21504
	ds_read_b128 v[90:93], v157 offset:22528
	ds_read_b128 v[94:97], v157 offset:23552
	buffer_load_dwordx4 v154, s[80:83], s60 offen lds
	s_add_i32 s61, s60, 0x20000
	s_mov_b32 m0, s29
	s_nop 0
	buffer_load_dwordx4 v154, s[80:83], s61 offen lds
	s_add_i32 s61, s60, 0x40000
	s_mov_b32 m0, s30
	s_nop 0
	buffer_load_dwordx4 v154, s[80:83], s61 offen lds
	s_add_i32 s61, s60, 0x60000
	s_mov_b32 m0, s31
	s_nop 0
	buffer_load_dwordx4 v154, s[80:83], s61 offen lds
	s_mov_b32 m0, s27
	s_add_i32 s61, s58, 0x20000
	buffer_load_dwordx4 v1, s[80:83], s58 offen lds
	s_mov_b32 m0, s33
	s_nop 0
	buffer_load_dwordx4 v1, s[80:83], s61 offen lds
	s_waitcnt vmcnt(8)
	s_waitcnt lgkmcnt(0)
	s_barrier
	s_waitcnt lgkmcnt(6)
	v_mfma_scale_f32_16x16x128_f8f6f4 v[62:65], v[102:109], v[66:73], v[62:65], v158, v158 op_sel:[0,1,0] op_sel_hi:[0,0,0]
	v_mfma_scale_f32_16x16x128_f8f6f4 v[54:57], v[114:121], v[66:73], v[54:57], v158, v158 op_sel:[0,1,0] op_sel_hi:[0,0,0]
	s_waitcnt lgkmcnt(4)
	v_mfma_scale_f32_16x16x128_f8f6f4 v[46:49], v[102:109], v[74:81], v[46:49], v158, v158 op_sel:[0,1,0] op_sel_hi:[0,0,0]
	v_mfma_scale_f32_16x16x128_f8f6f4 v[202:205], v[114:121], v[74:81], v[38:41], v158, v158 op_sel:[0,1,0] op_sel_hi:[0,0,0]
	s_waitcnt lgkmcnt(2)
	v_mfma_scale_f32_16x16x128_f8f6f4 v[206:209], v[102:109], v[82:89], v[30:33], v158, v158 op_sel:[0,1,0] op_sel_hi:[0,0,0]
	v_mfma_scale_f32_16x16x128_f8f6f4 v[222:225], v[114:121], v[82:89], v[22:25], v158, v158 op_sel:[0,1,0] op_sel_hi:[0,0,0]
	s_waitcnt lgkmcnt(0)
	v_mfma_scale_f32_16x16x128_f8f6f4 v[226:229], v[102:109], v[90:97], v[14:17], v158, v158 op_sel:[0,1,0] op_sel_hi:[0,0,0]
	v_mfma_scale_f32_16x16x128_f8f6f4 v[230:233], v[114:121], v[90:97], v[6:9], v158, v158 op_sel:[0,1,0] op_sel_hi:[0,0,0]
	v_mfma_scale_f32_16x16x128_f8f6f4 v[58:61], v[162:169], v[66:73], v[58:61], v158, v158 op_sel:[0,1,0] op_sel_hi:[0,0,0]
	v_mfma_scale_f32_16x16x128_f8f6f4 v[50:53], v[170:177], v[66:73], v[50:53], v158, v158 op_sel:[0,1,0] op_sel_hi:[0,0,0]
	v_mfma_scale_f32_16x16x128_f8f6f4 v[42:45], v[162:169], v[74:81], v[42:45], v158, v158 op_sel:[0,1,0] op_sel_hi:[0,0,0]
	v_mfma_scale_f32_16x16x128_f8f6f4 v[234:237], v[170:177], v[74:81], v[34:37], v158, v158 op_sel:[0,1,0] op_sel_hi:[0,0,0]
	v_mfma_scale_f32_16x16x128_f8f6f4 v[238:241], v[162:169], v[82:89], v[26:29], v158, v158 op_sel:[0,1,0] op_sel_hi:[0,0,0]
	v_mfma_scale_f32_16x16x128_f8f6f4 v[242:245], v[170:177], v[82:89], v[18:21], v158, v158 op_sel:[0,1,0] op_sel_hi:[0,0,0]
	v_mfma_scale_f32_16x16x128_f8f6f4 v[246:249], v[162:169], v[90:97], v[10:13], v158, v158 op_sel:[0,1,0] op_sel_hi:[0,0,0]
	v_mfma_scale_f32_16x16x128_f8f6f4 v[250:253], v[170:177], v[90:97], v[2:5], v158, v158 op_sel:[0,1,0] op_sel_hi:[0,0,0]
	s_barrier
; #define PG8_STAGE(bufoff, goff, voff) do { _Pragma("unroll") for (int _i = 0; _i < 2; ++_i) \
;         __builtin_amdgcn_raw_ptr_buffer_load_lds(rsrc, (PG8_LAS void*)(lds + (bufoff) + ldsw + _i * 8192), 16, (int)(voff), (int)((goff) + _i * p1##voff), 0, 0); } while (0)
; #define PG8_LDA(dst, b, h) do { _Pragma("unroll") for (int m = 0; m < 4; ++m) dst[m] = PG8_LD8(lds + PG8_SA(b, h) + aoff + m * 2048); } while (0)
; #define PG8_LDB(dst, b, h) do { _Pragma("unroll") for (int n = 0; n < 2; ++n) dst[n] = PG8_LD8(lds + PG8_SB(b, h) + boff + n * 2048); } while (0)
; #define PG8_WAIT_V(n) asm volatile("s_waitcnt vmcnt(" #n ")" ::: "memory")
; #define PG8_WAIT_L(n) asm volatile("s_waitcnt lgkmcnt(" #n ")" ::: "memory")
; #define PG8_BAR __builtin_amdgcn_s_barrier()
; #define PG8_SCHED __builtin_amdgcn_sched_barrier(0)
; template <class Epi, class Sched, bool ALIGN_EPI, bool F8 = false, int F8SC = F8_SCALES>
; __device__ __forceinline__ void gemm_phase(PG8_LAS unsigned char* lds, const __amdgpu_buffer_rsrc_t rsrc, const int lda, const int ldb, const int K, const Sched& S, const Epi& E) {
;     ...
;             PG8_LDB(B0, 1, 0); PG8_LDB(B1, 1, 1); PG8_SCHED; PG8_LDA(At, 1, 0); PG8_STAGE(PG8_SA(0, 1), a2 + hsA, voffA);
;             PG8_WAIT_V(8); PG8_WAIT_L(0); PG8_BAR; PG8_MMA(0, 0, At, B0); PG8_MMA(0, 1, At, B1); PG8_BAR; PG8_SCHED;
;             PG8_LDA(At, 1, 1); PG8_STAGE(PG8_SB(1, 0), b3, voffB); PG8_STAGE(PG8_SB(1, 1), b3 + hsB, voffB); PG8_STAGE(PG8_SA(1, 0), a3, voffA);
;             PG8_WAIT_V(8); PG8_WAIT_L(0); PG8_BAR; PG8_MMA(1, 0, At, B0); PG8_MMA(1, 1, At, B1); PG8_BAR; PG8_SCHED;
;         }
	s_nop 4
	ds_read_b128 v[2:5], v159
	ds_read_b128 v[6:9], v159 offset:1024
	ds_read_b128 v[102:105], v159 offset:2048
	ds_read_b128 v[106:109], v159 offset:3072
	ds_read_b128 v[114:117], v160
	ds_read_b128 v[118:121], v160 offset:1024
	ds_read_b128 v[162:165], v160 offset:2048
	ds_read_b128 v[166:169], v160 offset:3072
	s_mov_b32 m0, s34
	s_add_i32 s61, s58, 0x40000
	ds_read_b128 v[10:13], v157 offset:32768
	ds_read_b128 v[14:17], v157 offset:33792
	ds_read_b128 v[18:21], v157 offset:34816
	ds_read_b128 v[22:25], v157 offset:35840
	ds_read_b128 v[26:29], v157 offset:36864
	ds_read_b128 v[30:33], v157 offset:37888
	ds_read_b128 v[34:37], v157 offset:38912
	ds_read_b128 v[38:41], v157 offset:39936
	buffer_load_dwordx4 v1, s[80:83], s61 offen lds
	s_add_i32 s61, s58, 0x60000
	s_mov_b32 m0, s35
	s_nop 0
	buffer_load_dwordx4 v1, s[80:83], s61 offen lds
	s_waitcnt vmcnt(8)
	s_waitcnt lgkmcnt(0)
	s_barrier
	s_waitcnt lgkmcnt(6)
	v_mfma_scale_f32_16x16x128_f8f6f4 v[142:145], v[2:9], v[10:17], v[142:145], v158, v158 op_sel:[0,1,0] op_sel_hi:[0,0,0]
	v_mfma_scale_f32_16x16x128_f8f6f4 v[138:141], v[102:109], v[10:17], v[138:141], v158, v158 op_sel:[0,1,0] op_sel_hi:[0,0,0]
	s_waitcnt lgkmcnt(4)
	v_mfma_scale_f32_16x16x128_f8f6f4 v[134:137], v[2:9], v[18:25], v[134:137], v158, v158 op_sel:[0,1,0] op_sel_hi:[0,0,0]
	v_mfma_scale_f32_16x16x128_f8f6f4 v[110:113], v[102:109], v[18:25], v[110:113], v158, v158 op_sel:[0,1,0] op_sel_hi:[0,0,0]
	s_waitcnt lgkmcnt(2)
	v_mfma_scale_f32_16x16x128_f8f6f4 v[94:97], v[2:9], v[26:33], v[148:151], v158, v158 op_sel:[0,1,0] op_sel_hi:[0,0,0]
	v_mfma_scale_f32_16x16x128_f8f6f4 v[86:89], v[102:109], v[26:33], v[210:213], v158, v158 op_sel:[0,1,0] op_sel_hi:[0,0,0]
	s_waitcnt lgkmcnt(0)
	v_mfma_scale_f32_16x16x128_f8f6f4 v[78:81], v[2:9], v[34:41], v[214:217], v158, v158 op_sel:[0,1,0] op_sel_hi:[0,0,0]
	v_mfma_scale_f32_16x16x128_f8f6f4 v[70:73], v[102:109], v[34:41], v[218:221], v158, v158 op_sel:[0,1,0] op_sel_hi:[0,0,0]
	v_mfma_scale_f32_16x16x128_f8f6f4 v[130:133], v[114:121], v[10:17], v[130:133], v158, v158 op_sel:[0,1,0] op_sel_hi:[0,0,0]
	v_mfma_scale_f32_16x16x128_f8f6f4 v[126:129], v[162:169], v[10:17], v[126:129], v158, v158 op_sel:[0,1,0] op_sel_hi:[0,0,0]
	v_mfma_scale_f32_16x16x128_f8f6f4 v[122:125], v[114:121], v[18:25], v[122:125], v158, v158 op_sel:[0,1,0] op_sel_hi:[0,0,0]
	v_mfma_scale_f32_16x16x128_f8f6f4 v[98:101], v[162:169], v[18:25], v[98:101], v158, v158 op_sel:[0,1,0] op_sel_hi:[0,0,0]
	v_mfma_scale_f32_16x16x128_f8f6f4 v[90:93], v[114:121], v[26:33], v[178:181], v158, v158 op_sel:[0,1,0] op_sel_hi:[0,0,0]
	v_mfma_scale_f32_16x16x128_f8f6f4 v[82:85], v[162:169], v[26:33], v[182:185], v158, v158 op_sel:[0,1,0] op_sel_hi:[0,0,0]
	v_mfma_scale_f32_16x16x128_f8f6f4 v[74:77], v[114:121], v[34:41], v[186:189], v158, v158 op_sel:[0,1,0] op_sel_hi:[0,0,0]
	v_mfma_scale_f32_16x16x128_f8f6f4 v[66:69], v[162:169], v[34:41], v[190:193], v158, v158 op_sel:[0,1,0] op_sel_hi:[0,0,0]
	s_barrier
	s_mov_b32 m0, s39
	s_add_i32 s61, s60, 0x80
	ds_read_b128 v[170:173], v157 offset:49152
	ds_read_b128 v[174:177], v157 offset:50176
	ds_read_b128 v[178:181], v157 offset:51200
	ds_read_b128 v[182:185], v157 offset:52224
	ds_read_b128 v[186:189], v157 offset:53248
	ds_read_b128 v[190:193], v157 offset:54272
	ds_read_b128 v[194:197], v157 offset:55296
	ds_read_b128 v[198:201], v157 offset:56320
	buffer_load_dwordx4 v154, s[80:83], s61 offen lds
	s_add_i32 s61, s60, 0x20080
	s_mov_b32 m0, s40
	s_add_i32 s58, s58, 0x20080
	buffer_load_dwordx4 v154, s[80:83], s61 offen lds
	s_add_i32 s61, s60, 0x40080
	s_mov_b32 m0, s43
	s_add_i32 s60, s60, 0x60080
	buffer_load_dwordx4 v154, s[80:83], s61 offen lds
	s_mov_b32 m0, s64
	s_nop 0
	buffer_load_dwordx4 v154, s[80:83], s60 offen lds
	s_mov_b32 m0, s41
	s_nop 0
	buffer_load_dwordx4 v1, s[80:83], s59 offen lds
	s_mov_b32 m0, s42
	s_nop 0
	buffer_load_dwordx4 v1, s[80:83], s58 offen lds
	s_waitcnt vmcnt(8)
	s_waitcnt lgkmcnt(0)
	s_barrier
	s_waitcnt lgkmcnt(6)
	v_mfma_scale_f32_16x16x128_f8f6f4 v[62:65], v[2:9], v[170:177], v[62:65], v158, v158 op_sel:[0,1,0] op_sel_hi:[0,0,0]
	v_mfma_scale_f32_16x16x128_f8f6f4 v[54:57], v[102:109], v[170:177], v[54:57], v158, v158 op_sel:[0,1,0] op_sel_hi:[0,0,0]
	s_waitcnt lgkmcnt(4)
	v_mfma_scale_f32_16x16x128_f8f6f4 v[46:49], v[2:9], v[178:185], v[46:49], v158, v158 op_sel:[0,1,0] op_sel_hi:[0,0,0]
	v_mfma_scale_f32_16x16x128_f8f6f4 v[38:41], v[102:109], v[178:185], v[202:205], v158, v158 op_sel:[0,1,0] op_sel_hi:[0,0,0]
	s_waitcnt lgkmcnt(2)
	v_mfma_scale_f32_16x16x128_f8f6f4 v[30:33], v[2:9], v[186:193], v[206:209], v158, v158 op_sel:[0,1,0] op_sel_hi:[0,0,0]
	v_mfma_scale_f32_16x16x128_f8f6f4 v[22:25], v[102:109], v[186:193], v[222:225], v158, v158 op_sel:[0,1,0] op_sel_hi:[0,0,0]
	s_waitcnt lgkmcnt(0)
	v_mfma_scale_f32_16x16x128_f8f6f4 v[14:17], v[2:9], v[194:201], v[226:229], v158, v158 op_sel:[0,1,0] op_sel_hi:[0,0,0]
	v_mfma_scale_f32_16x16x128_f8f6f4 v[6:9], v[102:109], v[194:201], v[230:233], v158, v158 op_sel:[0,1,0] op_sel_hi:[0,0,0]
	v_mfma_scale_f32_16x16x128_f8f6f4 v[58:61], v[114:121], v[170:177], v[58:61], v158, v158 op_sel:[0,1,0] op_sel_hi:[0,0,0]
	v_mfma_scale_f32_16x16x128_f8f6f4 v[50:53], v[162:169], v[170:177], v[50:53], v158, v158 op_sel:[0,1,0] op_sel_hi:[0,0,0]
	v_mfma_scale_f32_16x16x128_f8f6f4 v[42:45], v[114:121], v[178:185], v[42:45], v158, v158 op_sel:[0,1,0] op_sel_hi:[0,0,0]
	v_mfma_scale_f32_16x16x128_f8f6f4 v[34:37], v[162:169], v[178:185], v[234:237], v158, v158 op_sel:[0,1,0] op_sel_hi:[0,0,0]
	v_mfma_scale_f32_16x16x128_f8f6f4 v[26:29], v[114:121], v[186:193], v[238:241], v158, v158 op_sel:[0,1,0] op_sel_hi:[0,0,0]
	v_mfma_scale_f32_16x16x128_f8f6f4 v[18:21], v[162:169], v[186:193], v[242:245], v158, v158 op_sel:[0,1,0] op_sel_hi:[0,0,0]
	v_mfma_scale_f32_16x16x128_f8f6f4 v[10:13], v[114:121], v[194:201], v[246:249], v158, v158 op_sel:[0,1,0] op_sel_hi:[0,0,0]
	v_mfma_scale_f32_16x16x128_f8f6f4 v[2:5], v[162:169], v[194:201], v[250:253], v158, v158 op_sel:[0,1,0] op_sel_hi:[0,0,0]
	s_barrier
	s_add_i32 s57, s57, 2
	s_addk_i32 s55, 0x100
	s_addk_i32 s56, 0x100
	s_cmp_gt_u32 s57, 13
	s_cbranch_scc0 .LBB0_1651
	s_and_b64 vcc, exec, s[8:9]
	s_cbranch_vccz .LBB0_1654
	s_barrier

; #define PG8_STAGE(bufoff, goff, voff) do { _Pragma("unroll") for (int _i = 0; _i < 2; ++_i) \
;         __builtin_amdgcn_raw_ptr_buffer_load_lds(rsrc, (PG8_LAS void*)(lds + (bufoff) + ldsw + _i * 8192), 16, (int)(voff), (int)((goff) + _i * p1##voff), 0, 0); } while (0)
; #define PG8_LDA(dst, b, h) do { _Pragma("unroll") for (int m = 0; m < 4; ++m) dst[m] = PG8_LD8(lds + PG8_SA(b, h) + aoff + m * 2048); } while (0)
; #define PG8_LDB(dst, b, h) do { _Pragma("unroll") for (int n = 0; n < 2; ++n) dst[n] = PG8_LD8(lds + PG8_SB(b, h) + boff + n * 2048); } while (0)
; #define PG8_WAIT_V(n) asm volatile("s_waitcnt vmcnt(" #n ")" ::: "memory")
; #define PG8_WAIT_L(n) asm volatile("s_waitcnt lgkmcnt(" #n ")" ::: "memory")
; #define PG8_BAR __builtin_amdgcn_s_barrier()
; #define PG8_SCHED __builtin_amdgcn_sched_barrier(0)
; template <class Epi, class Sched, bool ALIGN_EPI, bool F8 = false, int F8SC = F8_SCALES>
; __device__ __forceinline__ void gemm_phase(PG8_LAS unsigned char* lds, const __amdgpu_buffer_rsrc_t rsrc, const int lda, const int ldb, const int K, const Sched& S, const Epi& E) {
;     ...
;             PG8_LDB(B0, 0, 0); PG8_LDB(B1, 0, 1); PG8_SCHED; PG8_LDA(At, 0, 0); PG8_STAGE(PG8_SA(1, 1), a1 + hsA, voffA);
;             PG8_WAIT_V(8); PG8_WAIT_L(0); PG8_BAR; PG8_MMA(0, 0, At, B0); PG8_MMA(0, 1, At, B1); PG8_BAR; PG8_SCHED;
;             PG8_LDA(At, 0, 1); PG8_STAGE(PG8_SB(0, 0), b2, voffB); PG8_STAGE(PG8_SB(0, 1), b2 + hsB, voffB); PG8_STAGE(PG8_SA(0, 0), a2, voffA);
;             PG8_WAIT_V(8); PG8_WAIT_L(0); PG8_BAR; PG8_MMA(1, 0, At, B0); PG8_MMA(1, 1, At, B1); PG8_BAR; PG8_SCHED;
.LBB0_1725:
	ds_read_b128 v[130:133], v169
	ds_read_b128 v[134:137], v169 offset:1024
	ds_read_b128 v[138:141], v169 offset:2048
	ds_read_b128 v[142:145], v169 offset:3072
	s_waitcnt vmcnt(0)
	ds_read_b128 v[150:153], v170
	ds_read_b128 v[154:157], v170 offset:1024
	ds_read_b128 v[158:161], v170 offset:2048
	ds_read_b128 v[162:165], v170 offset:3072
	s_add_i32 s50, s4, 0xfffa0080
	s_cmp_eq_u32 s49, 12
	s_cselect_b32 s50, s47, s50
	s_cselect_b32 s52, s46, s5
	s_add_i32 s51, s50, 0x80
	s_add_i32 s53, s4, 0xfffe0000
	s_mov_b32 s80, s96
	s_mov_b32 m0, s30
	ds_read_b128 v[176:179], v171
	ds_read_b128 v[180:183], v171 offset:1024
	ds_read_b128 v[184:187], v171 offset:2048
	ds_read_b128 v[188:191], v171 offset:3072
	ds_read_b128 v[192:195], v171 offset:4096
	ds_read_b128 v[196:199], v171 offset:5120
	ds_read_b128 v[200:203], v171 offset:6144
	ds_read_b128 v[204:207], v171 offset:7168
	buffer_load_dwordx4 v1, s[80:83], s53 offen lds
	s_mov_b32 m0, s31
	s_nop 0
	buffer_load_dwordx4 v1, s[80:83], s4 offen lds
	s_waitcnt vmcnt(8)
	s_waitcnt lgkmcnt(0)
	s_barrier
	s_waitcnt lgkmcnt(6)
	v_mfma_scale_f32_16x16x128_f8f6f4 v[126:129], v[130:137], v[176:183], v[126:129], v172, v172 op_sel:[0,1,0] op_sel_hi:[0,0,0]
	v_mfma_scale_f32_16x16x128_f8f6f4 v[122:125], v[138:145], v[176:183], v[122:125], v172, v172 op_sel:[0,1,0] op_sel_hi:[0,0,0]
	s_waitcnt lgkmcnt(4)
	v_mfma_scale_f32_16x16x128_f8f6f4 v[110:113], v[130:137], v[184:191], v[110:113], v172, v172 op_sel:[0,1,0] op_sel_hi:[0,0,0]
	v_mfma_scale_f32_16x16x128_f8f6f4 v[106:109], v[138:145], v[184:191], v[106:109], v172, v172 op_sel:[0,1,0] op_sel_hi:[0,0,0]
	s_waitcnt lgkmcnt(2)
	v_mfma_scale_f32_16x16x128_f8f6f4 v[208:211], v[130:137], v[192:199], v[94:97], v172, v172 op_sel:[0,1,0] op_sel_hi:[0,0,0]
	v_mfma_scale_f32_16x16x128_f8f6f4 v[212:215], v[138:145], v[192:199], v[90:93], v172, v172 op_sel:[0,1,0] op_sel_hi:[0,0,0]
	s_waitcnt lgkmcnt(0)
	v_mfma_scale_f32_16x16x128_f8f6f4 v[216:219], v[130:137], v[200:207], v[78:81], v172, v172 op_sel:[0,1,0] op_sel_hi:[0,0,0]
	v_mfma_scale_f32_16x16x128_f8f6f4 v[220:223], v[138:145], v[200:207], v[74:77], v172, v172 op_sel:[0,1,0] op_sel_hi:[0,0,0]
	v_mfma_scale_f32_16x16x128_f8f6f4 v[118:121], v[150:157], v[176:183], v[118:121], v172, v172 op_sel:[0,1,0] op_sel_hi:[0,0,0]
	v_mfma_scale_f32_16x16x128_f8f6f4 v[114:117], v[158:165], v[176:183], v[114:117], v172, v172 op_sel:[0,1,0] op_sel_hi:[0,0,0]
	v_mfma_scale_f32_16x16x128_f8f6f4 v[102:105], v[150:157], v[184:191], v[102:105], v172, v172 op_sel:[0,1,0] op_sel_hi:[0,0,0]
	v_mfma_scale_f32_16x16x128_f8f6f4 v[98:101], v[158:165], v[184:191], v[98:101], v172, v172 op_sel:[0,1,0] op_sel_hi:[0,0,0]
	v_mfma_scale_f32_16x16x128_f8f6f4 v[176:179], v[150:157], v[192:199], v[86:89], v172, v172 op_sel:[0,1,0] op_sel_hi:[0,0,0]
	v_mfma_scale_f32_16x16x128_f8f6f4 v[180:183], v[158:165], v[192:199], v[82:85], v172, v172 op_sel:[0,1,0] op_sel_hi:[0,0,0]
	v_mfma_scale_f32_16x16x128_f8f6f4 v[184:187], v[150:157], v[200:207], v[70:73], v172, v172 op_sel:[0,1,0] op_sel_hi:[0,0,0]
	v_mfma_scale_f32_16x16x128_f8f6f4 v[188:191], v[158:165], v[200:207], v[66:69], v172, v172 op_sel:[0,1,0] op_sel_hi:[0,0,0]
	s_barrier
	s_mov_b32 m0, s16
	s_nop 3
	ds_read_b128 v[66:69], v171 offset:16384
	ds_read_b128 v[70:73], v171 offset:17408
	ds_read_b128 v[74:77], v171 offset:18432
	ds_read_b128 v[78:81], v171 offset:19456
	ds_read_b128 v[82:85], v171 offset:20480
	ds_read_b128 v[86:89], v171 offset:21504
	ds_read_b128 v[90:93], v171 offset:22528
	ds_read_b128 v[94:97], v171 offset:23552
	buffer_load_dwordx4 v168, s[80:83], s52 offen lds
	s_add_i32 s53, s52, 0x20000
	s_mov_b32 m0, s17
	s_nop 0
	buffer_load_dwordx4 v168, s[80:83], s53 offen lds
	s_add_i32 s53, s52, 0x40000
	s_mov_b32 m0, s18
	s_nop 0
	buffer_load_dwordx4 v168, s[80:83], s53 offen lds
	s_add_i32 s53, s52, 0x60000
	s_mov_b32 m0, s19
	s_nop 0
	buffer_load_dwordx4 v168, s[80:83], s53 offen lds
	s_mov_b32 m0, s15
	s_add_i32 s53, s50, 0x20000
	buffer_load_dwordx4 v1, s[80:83], s50 offen lds
	s_mov_b32 m0, s20
	s_nop 0
	buffer_load_dwordx4 v1, s[80:83], s53 offen lds
	s_waitcnt vmcnt(8)
	s_waitcnt lgkmcnt(0)
	s_barrier
	s_waitcnt lgkmcnt(6)
	v_mfma_scale_f32_16x16x128_f8f6f4 v[62:65], v[130:137], v[66:73], v[62:65], v172, v172 op_sel:[0,1,0] op_sel_hi:[0,0,0]
	v_mfma_scale_f32_16x16x128_f8f6f4 v[58:61], v[138:145], v[66:73], v[58:61], v172, v172 op_sel:[0,1,0] op_sel_hi:[0,0,0]
	s_waitcnt lgkmcnt(4)
	v_mfma_scale_f32_16x16x128_f8f6f4 v[192:195], v[130:137], v[74:81], v[46:49], v172, v172 op_sel:[0,1,0] op_sel_hi:[0,0,0]
	v_mfma_scale_f32_16x16x128_f8f6f4 v[196:199], v[138:145], v[74:81], v[42:45], v172, v172 op_sel:[0,1,0] op_sel_hi:[0,0,0]
	s_waitcnt lgkmcnt(2)
	v_mfma_scale_f32_16x16x128_f8f6f4 v[200:203], v[130:137], v[82:89], v[30:33], v172, v172 op_sel:[0,1,0] op_sel_hi:[0,0,0]
	v_mfma_scale_f32_16x16x128_f8f6f4 v[204:207], v[138:145], v[82:89], v[26:29], v172, v172 op_sel:[0,1,0] op_sel_hi:[0,0,0]
	s_waitcnt lgkmcnt(0)
	v_mfma_scale_f32_16x16x128_f8f6f4 v[224:227], v[130:137], v[90:97], v[14:17], v172, v172 op_sel:[0,1,0] op_sel_hi:[0,0,0]
	v_mfma_scale_f32_16x16x128_f8f6f4 v[228:231], v[138:145], v[90:97], v[10:13], v172, v172 op_sel:[0,1,0] op_sel_hi:[0,0,0]
	v_mfma_scale_f32_16x16x128_f8f6f4 v[54:57], v[150:157], v[66:73], v[54:57], v172, v172 op_sel:[0,1,0] op_sel_hi:[0,0,0]
	v_mfma_scale_f32_16x16x128_f8f6f4 v[50:53], v[158:165], v[66:73], v[50:53], v172, v172 op_sel:[0,1,0] op_sel_hi:[0,0,0]
	v_mfma_scale_f32_16x16x128_f8f6f4 v[232:235], v[150:157], v[74:81], v[38:41], v172, v172 op_sel:[0,1,0] op_sel_hi:[0,0,0]
	v_mfma_scale_f32_16x16x128_f8f6f4 v[236:239], v[158:165], v[74:81], v[34:37], v172, v172 op_sel:[0,1,0] op_sel_hi:[0,0,0]
	v_mfma_scale_f32_16x16x128_f8f6f4 v[240:243], v[150:157], v[82:89], v[22:25], v172, v172 op_sel:[0,1,0] op_sel_hi:[0,0,0]
	v_mfma_scale_f32_16x16x128_f8f6f4 v[244:247], v[158:165], v[82:89], v[18:21], v172, v172 op_sel:[0,1,0] op_sel_hi:[0,0,0]
	v_mfma_scale_f32_16x16x128_f8f6f4 v[248:251], v[150:157], v[90:97], v[6:9], v172, v172 op_sel:[0,1,0] op_sel_hi:[0,0,0]
	v_mfma_scale_f32_16x16x128_f8f6f4 v[146:149], v[158:165], v[90:97], v[2:5], v172, v172 op_sel:[0,1,0] op_sel_hi:[0,0,0]
	s_barrier
; #define PG8_STAGE(bufoff, goff, voff) do { _Pragma("unroll") for (int _i = 0; _i < 2; ++_i) \
;         __builtin_amdgcn_raw_ptr_buffer_load_lds(rsrc, (PG8_LAS void*)(lds + (bufoff) + ldsw + _i * 8192), 16, (int)(voff), (int)((goff) + _i * p1##voff), 0, 0); } while (0)
; #define PG8_LDA(dst, b, h) do { _Pragma("unroll") for (int m = 0; m < 4; ++m) dst[m] = PG8_LD8(lds + PG8_SA(b, h) + aoff + m * 2048); } while (0)
; #define PG8_LDB(dst, b, h) do { _Pragma("unroll") for (int n = 0; n < 2; ++n) dst[n] = PG8_LD8(lds + PG8_SB(b, h) + boff + n * 2048); } while (0)
; #define PG8_WAIT_V(n) asm volatile("s_waitcnt vmcnt(" #n ")" ::: "memory")
; #define PG8_WAIT_L(n) asm volatile("s_waitcnt lgkmcnt(" #n ")" ::: "memory")
; #define PG8_BAR __builtin_amdgcn_s_barrier()
; #define PG8_SCHED __builtin_amdgcn_sched_barrier(0)
; template <class Epi, class Sched, bool ALIGN_EPI, bool F8 = false, int F8SC = F8_SCALES>
; __device__ __forceinline__ void gemm_phase(PG8_LAS unsigned char* lds, const __amdgpu_buffer_rsrc_t rsrc, const int lda, const int ldb, const int K, const Sched& S, const Epi& E) {
;     ...
;             PG8_LDB(B0, 1, 0); PG8_LDB(B1, 1, 1); PG8_SCHED; PG8_LDA(At, 1, 0); PG8_STAGE(PG8_SA(0, 1), a2 + hsA, voffA);
;             PG8_WAIT_V(8); PG8_WAIT_L(0); PG8_BAR; PG8_MMA(0, 0, At, B0); PG8_MMA(0, 1, At, B1); PG8_BAR; PG8_SCHED;
;             PG8_LDA(At, 1, 1); PG8_STAGE(PG8_SB(1, 0), b3, voffB); PG8_STAGE(PG8_SB(1, 1), b3 + hsB, voffB); PG8_STAGE(PG8_SA(1, 0), a3, voffA);
;             PG8_WAIT_V(8); PG8_WAIT_L(0); PG8_BAR; PG8_MMA(1, 0, At, B0); PG8_MMA(1, 1, At, B1); PG8_BAR; PG8_SCHED;
;         }
	s_nop 4
	ds_read_b128 v[2:5], v173
	ds_read_b128 v[6:9], v173 offset:1024
	ds_read_b128 v[18:21], v173 offset:2048
	ds_read_b128 v[22:25], v173 offset:3072
	ds_read_b128 v[130:133], v174
	ds_read_b128 v[134:137], v174 offset:1024
	ds_read_b128 v[138:141], v174 offset:2048
	ds_read_b128 v[142:145], v174 offset:3072
	s_mov_b32 m0, s21
	s_add_i32 s53, s50, 0x40000
	ds_read_b128 v[10:13], v171 offset:32768
	ds_read_b128 v[14:17], v171 offset:33792
	ds_read_b128 v[26:29], v171 offset:34816
	ds_read_b128 v[30:33], v171 offset:35840
	ds_read_b128 v[34:37], v171 offset:36864
	ds_read_b128 v[38:41], v171 offset:37888
	ds_read_b128 v[42:45], v171 offset:38912
	ds_read_b128 v[46:49], v171 offset:39936
	buffer_load_dwordx4 v1, s[80:83], s53 offen lds
	s_add_i32 s53, s50, 0x60000
	s_mov_b32 m0, s22
	s_nop 0
	buffer_load_dwordx4 v1, s[80:83], s53 offen lds
	s_waitcnt vmcnt(8)
	s_waitcnt lgkmcnt(0)
	s_barrier
	s_waitcnt lgkmcnt(6)
	v_mfma_scale_f32_16x16x128_f8f6f4 v[126:129], v[2:9], v[10:17], v[126:129], v172, v172 op_sel:[0,1,0] op_sel_hi:[0,0,0]
	v_mfma_scale_f32_16x16x128_f8f6f4 v[122:125], v[18:25], v[10:17], v[122:125], v172, v172 op_sel:[0,1,0] op_sel_hi:[0,0,0]
	s_waitcnt lgkmcnt(4)
	v_mfma_scale_f32_16x16x128_f8f6f4 v[110:113], v[2:9], v[26:33], v[110:113], v172, v172 op_sel:[0,1,0] op_sel_hi:[0,0,0]
	v_mfma_scale_f32_16x16x128_f8f6f4 v[106:109], v[18:25], v[26:33], v[106:109], v172, v172 op_sel:[0,1,0] op_sel_hi:[0,0,0]
	s_waitcnt lgkmcnt(2)
	v_mfma_scale_f32_16x16x128_f8f6f4 v[94:97], v[2:9], v[34:41], v[208:211], v172, v172 op_sel:[0,1,0] op_sel_hi:[0,0,0]
	v_mfma_scale_f32_16x16x128_f8f6f4 v[90:93], v[18:25], v[34:41], v[212:215], v172, v172 op_sel:[0,1,0] op_sel_hi:[0,0,0]
	s_waitcnt lgkmcnt(0)
	v_mfma_scale_f32_16x16x128_f8f6f4 v[78:81], v[2:9], v[42:49], v[216:219], v172, v172 op_sel:[0,1,0] op_sel_hi:[0,0,0]
	v_mfma_scale_f32_16x16x128_f8f6f4 v[74:77], v[18:25], v[42:49], v[220:223], v172, v172 op_sel:[0,1,0] op_sel_hi:[0,0,0]
	v_mfma_scale_f32_16x16x128_f8f6f4 v[118:121], v[130:137], v[10:17], v[118:121], v172, v172 op_sel:[0,1,0] op_sel_hi:[0,0,0]
	v_mfma_scale_f32_16x16x128_f8f6f4 v[114:117], v[138:145], v[10:17], v[114:117], v172, v172 op_sel:[0,1,0] op_sel_hi:[0,0,0]
	v_mfma_scale_f32_16x16x128_f8f6f4 v[102:105], v[130:137], v[26:33], v[102:105], v172, v172 op_sel:[0,1,0] op_sel_hi:[0,0,0]
	v_mfma_scale_f32_16x16x128_f8f6f4 v[98:101], v[138:145], v[26:33], v[98:101], v172, v172 op_sel:[0,1,0] op_sel_hi:[0,0,0]
	v_mfma_scale_f32_16x16x128_f8f6f4 v[86:89], v[130:137], v[34:41], v[176:179], v172, v172 op_sel:[0,1,0] op_sel_hi:[0,0,0]
	v_mfma_scale_f32_16x16x128_f8f6f4 v[82:85], v[138:145], v[34:41], v[180:183], v172, v172 op_sel:[0,1,0] op_sel_hi:[0,0,0]
	v_mfma_scale_f32_16x16x128_f8f6f4 v[70:73], v[130:137], v[42:49], v[184:187], v172, v172 op_sel:[0,1,0] op_sel_hi:[0,0,0]
	v_mfma_scale_f32_16x16x128_f8f6f4 v[66:69], v[138:145], v[42:49], v[188:191], v172, v172 op_sel:[0,1,0] op_sel_hi:[0,0,0]
	s_barrier
	s_mov_b32 m0, s24
	s_add_i32 s53, s52, 0x80
	ds_read_b128 v[34:37], v171 offset:49152
	ds_read_b128 v[38:41], v171 offset:50176
	ds_read_b128 v[150:153], v171 offset:51200
	ds_read_b128 v[154:157], v171 offset:52224
	ds_read_b128 v[158:161], v171 offset:53248
	ds_read_b128 v[162:165], v171 offset:54272
	ds_read_b128 v[176:179], v171 offset:55296
	ds_read_b128 v[180:183], v171 offset:56320
	buffer_load_dwordx4 v168, s[80:83], s53 offen lds
	s_add_i32 s53, s52, 0x20080
	s_mov_b32 m0, s25
	s_add_i32 s50, s50, 0x20080
	buffer_load_dwordx4 v168, s[80:83], s53 offen lds
	s_add_i32 s53, s52, 0x40080
	s_mov_b32 m0, s28
	s_add_i32 s52, s52, 0x60080
	buffer_load_dwordx4 v168, s[80:83], s53 offen lds
	s_mov_b32 m0, s29
	s_nop 0
	buffer_load_dwordx4 v168, s[80:83], s52 offen lds
	s_mov_b32 m0, s26
	s_nop 0
	buffer_load_dwordx4 v1, s[80:83], s51 offen lds
	s_mov_b32 m0, s27
	s_nop 0
	buffer_load_dwordx4 v1, s[80:83], s50 offen lds
	s_waitcnt vmcnt(8)
	s_waitcnt lgkmcnt(0)
	s_barrier
	s_waitcnt lgkmcnt(6)
	v_mfma_scale_f32_16x16x128_f8f6f4 v[62:65], v[2:9], v[34:41], v[62:65], v172, v172 op_sel:[0,1,0] op_sel_hi:[0,0,0]
	v_mfma_scale_f32_16x16x128_f8f6f4 v[58:61], v[18:25], v[34:41], v[58:61], v172, v172 op_sel:[0,1,0] op_sel_hi:[0,0,0]
	s_waitcnt lgkmcnt(4)
	v_mfma_scale_f32_16x16x128_f8f6f4 v[46:49], v[2:9], v[150:157], v[192:195], v172, v172 op_sel:[0,1,0] op_sel_hi:[0,0,0]
	v_mfma_scale_f32_16x16x128_f8f6f4 v[42:45], v[18:25], v[150:157], v[196:199], v172, v172 op_sel:[0,1,0] op_sel_hi:[0,0,0]
	s_waitcnt lgkmcnt(2)
	v_mfma_scale_f32_16x16x128_f8f6f4 v[30:33], v[2:9], v[158:165], v[200:203], v172, v172 op_sel:[0,1,0] op_sel_hi:[0,0,0]
	v_mfma_scale_f32_16x16x128_f8f6f4 v[26:29], v[18:25], v[158:165], v[204:207], v172, v172 op_sel:[0,1,0] op_sel_hi:[0,0,0]
	s_waitcnt lgkmcnt(0)
	v_mfma_scale_f32_16x16x128_f8f6f4 v[14:17], v[2:9], v[176:183], v[224:227], v172, v172 op_sel:[0,1,0] op_sel_hi:[0,0,0]
	v_mfma_scale_f32_16x16x128_f8f6f4 v[10:13], v[18:25], v[176:183], v[228:231], v172, v172 op_sel:[0,1,0] op_sel_hi:[0,0,0]
	v_mfma_scale_f32_16x16x128_f8f6f4 v[54:57], v[130:137], v[34:41], v[54:57], v172, v172 op_sel:[0,1,0] op_sel_hi:[0,0,0]
	v_mfma_scale_f32_16x16x128_f8f6f4 v[50:53], v[138:145], v[34:41], v[50:53], v172, v172 op_sel:[0,1,0] op_sel_hi:[0,0,0]
	v_mfma_scale_f32_16x16x128_f8f6f4 v[38:41], v[130:137], v[150:157], v[232:235], v172, v172 op_sel:[0,1,0] op_sel_hi:[0,0,0]
	v_mfma_scale_f32_16x16x128_f8f6f4 v[34:37], v[138:145], v[150:157], v[236:239], v172, v172 op_sel:[0,1,0] op_sel_hi:[0,0,0]
	v_mfma_scale_f32_16x16x128_f8f6f4 v[22:25], v[130:137], v[158:165], v[240:243], v172, v172 op_sel:[0,1,0] op_sel_hi:[0,0,0]
	v_mfma_scale_f32_16x16x128_f8f6f4 v[18:21], v[138:145], v[158:165], v[244:247], v172, v172 op_sel:[0,1,0] op_sel_hi:[0,0,0]
	v_mfma_scale_f32_16x16x128_f8f6f4 v[6:9], v[130:137], v[176:183], v[248:251], v172, v172 op_sel:[0,1,0] op_sel_hi:[0,0,0]
	v_mfma_scale_f32_16x16x128_f8f6f4 v[2:5], v[138:145], v[176:183], v[146:149], v172, v172 op_sel:[0,1,0] op_sel_hi:[0,0,0]
	s_barrier
	s_add_i32 s49, s49, 2
	s_addk_i32 s4, 0x100
	s_addk_i32 s5, 0x100
	s_cmp_gt_u32 s49, 13
	s_cbranch_scc0 .LBB0_1725
	s_and_b64 vcc, exec, s[10:11]
	s_cbranch_vccz .LBB0_1728
	s_barrier

; #define LAS __attribute__((address_space(3)))
; __global__ void __launch_bounds__(NWAVES * 64, 2) mk_fwd(Args args) {
;     extern __shared__ __attribute__((aligned(16))) unsigned char lds[];
;     Frame F;
;     F.lds = (LAS unsigned char*)lds;
;     F.MISC = (volatile LAS unsigned*)(F.lds + MISC_OFF);
;     F.tid = threadIdx.x; F.lane = F.tid & 63; F.wave = __builtin_amdgcn_readfirstlane(F.tid >> 6);
	.amdhsa_kernel _Z6mk_fwd4Args
		.amdhsa_group_segment_fixed_size 0
		.amdhsa_private_segment_fixed_size 0
		.amdhsa_kernarg_size 488
		.amdhsa_user_sgpr_count 2
		.amdhsa_user_sgpr_dispatch_ptr 0
		.amdhsa_user_sgpr_queue_ptr 0
		.amdhsa_user_sgpr_kernarg_segment_ptr 1
		.amdhsa_user_sgpr_dispatch_id 0
		.amdhsa_user_sgpr_kernarg_preload_length 0
		.amdhsa_user_sgpr_kernarg_preload_offset 0
		.amdhsa_user_sgpr_private_segment_size 0
		.amdhsa_uses_dynamic_stack 0
		.amdhsa_enable_private_segment 0
		.amdhsa_system_sgpr_workgroup_id_x 1
		.amdhsa_system_sgpr_workgroup_id_y 0
		.amdhsa_system_sgpr_workgroup_id_z 0
		.amdhsa_system_sgpr_workgroup_info 0
		.amdhsa_system_vgpr_workitem_id 0
		.amdhsa_next_free_vgpr 256
		.amdhsa_next_free_sgpr 98
		.amdhsa_accum_offset 256
		.amdhsa_reserve_vcc 1
		.amdhsa_float_round_mode_32 0
		.amdhsa_float_round_mode_16_64 0
		.amdhsa_float_denorm_mode_32 3
		.amdhsa_float_denorm_mode_16_64 3
		.amdhsa_dx10_clamp 1
		.amdhsa_ieee_mode 1
		.amdhsa_fp16_overflow 0
		.amdhsa_tg_split 0
		.amdhsa_exception_fp_ieee_invalid_op 0
		.amdhsa_exception_fp_denorm_src 0
		.amdhsa_exception_fp_ieee_div_zero 0
		.amdhsa_exception_fp_ieee_overflow 0
		.amdhsa_exception_fp_ieee_underflow 0
		.amdhsa_exception_fp_ieee_inexact 0
		.amdhsa_exception_int_div_zero 0
	.end_amdhsa_kernel

; __global__ void __launch_bounds__(NWAVES * 64, 2) mk_fwd(Args args) {
amdhsa.kernels:
  - .agpr_count:     0
    .args:
      - .offset:         0
        .size:           232
        .value_kind:     by_value
      - .offset:         232
        .size:           4
        .value_kind:     hidden_block_count_x
      - .offset:         236
        .size:           4
        .value_kind:     hidden_block_count_y
      - .offset:         240
        .size:           4
        .value_kind:     hidden_block_count_z
      - .offset:         244
        .size:           2
        .value_kind:     hidden_group_size_x
      - .offset:         246
        .size:           2
        .value_kind:     hidden_group_size_y
      - .offset:         248
        .size:           2
        .value_kind:     hidden_group_size_z
      - .offset:         250
        .size:           2
        .value_kind:     hidden_remainder_x
      - .offset:         252
        .size:           2
        .value_kind:     hidden_remainder_y
      - .offset:         254
        .size:           2
        .value_kind:     hidden_remainder_z
      - .offset:         272
        .size:           8
        .value_kind:     hidden_global_offset_x
      - .offset:         280
        .size:           8
        .value_kind:     hidden_global_offset_y
      - .offset:         288
        .size:           8
        .value_kind:     hidden_global_offset_z
      - .offset:         296
        .size:           2
        .value_kind:     hidden_grid_dims
      - .offset:         352
        .size:           4
        .value_kind:     hidden_dynamic_lds_size
    .group_segment_fixed_size: 0
    .kernarg_segment_align: 8
    .kernarg_segment_size: 488
    .language:       OpenCL C
    .language_version:
      - 2
      - 0
    .max_flat_workgroup_size: 512
    .name:           _Z6mk_fwd4Args
    .private_segment_fixed_size: 0
    .sgpr_count:     104
    .sgpr_spill_count: 160
    .symbol:         _Z6mk_fwd4Args.kd
    .uniform_work_group_size: 1
    .uses_dynamic_stack: false
    .vgpr_count:     256
    .vgpr_spill_count: 0
    .wavefront_size: 64
